# speedup vs baseline: 1.0493x; 1.0444x over previous
_ZN12_GLOBAL__N_110k_convpoolEPKtS1_PKfPKiPtS3_S6_:
	v_lshlrev_b32_e32 v70, 4, v0
	v_lshlrev_b32_e32 v1, 1, v0
	v_lshrrev_b32_e32 v86, 2, v0
	v_and_b32_e32 v2, 32, v1
	v_and_b32_e32 v3, 48, v70
	v_lshlrev_b32_e32 v5, 6, v86
	s_lshl_b32 s3, s2, 2
	v_bitop3_b32 v4, v1, v3, 32 bitop3:0x6c
	v_bitop3_b32 v72, v5, v2, v3 bitop3:0xf6
	v_mov_b32_e32 v3, 0x2000
	s_and_b32 s21, s3, 28
	s_ashr_i32 s3, s2, 6
	v_bitop3_b32 v3, v70, 48, v3 bitop3:0xc8
	s_add_i32 s21, s21, s3
	v_or_b32_e32 v2, 0x2000, v70
	v_bitop3_b32 v3, v1, v3, 32 bitop3:0x6c
	s_movk_i32 s3, 0x3fc0
	s_load_dwordx4 s[4:7], s[0:1], 0x0
	s_load_dwordx4 s[12:15], s[0:1], 0x28
	v_and_or_b32 v68, v2, s3, v3
	v_mov_b32_e32 v3, 0x6000
	v_and_b32_e32 v2, 0x1fc0, v70
	s_movk_i32 s3, 0x4000
	v_bitop3_b32 v3, v70, 48, v3 bitop3:0xc8
	v_readfirstlane_b32 s20, v0
	v_or3_b32 v66, v2, v4, s3
	v_or_b32_e32 v2, 0x6000, v70
	v_bitop3_b32 v1, v1, v3, 32 bitop3:0x6c
	s_movk_i32 s3, 0x7fc0
	v_and_or_b32 v74, v2, s3, v1
	v_and_b32_e32 v1, 0x3c0, v70
	s_mov_b32 s3, 0x8000
	s_bfe_u32 s22, s2, 0x30003
	s_mul_i32 s8, s21, 0x52800
	s_and_b32 s29, s20, 0x3ffffc0
	v_or3_b32 v78, v1, v4, s3
	s_mul_hi_i32 s3, s21, 0x52800
	s_waitcnt lgkmcnt(0)
	v_cmp_lt_u32_e32 vcc, 0xbf, v0
	s_mul_i32 s48, s2, 6
	s_mov_b32 s49, 0x18000
	v_cndmask_b32_e64 v200, 0, 1, vcc
	v_mul_u32_u24_e32 v201, 0xc0, v200
	v_sub_u32_e32 v201, v0, v201
	v_add_u32_e32 v200, s48, v200
	v_lshlrev_b32_e32 v200, 6, v200
	v_and_b32_e32 v202, 3, v201
	v_lshl_add_u32 v200, v202, 4, v200
	v_lshrrev_b32_e32 v201, 2, v201
	v_mul_lo_u32 v201, v201, s49
	v_add_u32_e32 v200, v200, v201
	v_mov_b32_e32 v201, 0
	v_lshl_add_u64 v[200:201], s[14:15], 0, v[200:201]
	s_add_u32 s10, s4, s8
	s_addc_u32 s11, s5, s3
	s_lshl_b32 s30, s20, 4
	s_mul_i32 s9, s22, 0x1e000
	s_and_b32 s3, s30, 0xfffffc00
	s_add_u32 s16, s6, s9
	s_addc_u32 s17, s7, 0
	s_add_i32 s28, s3, 0
	s_add_i32 s27, s28, 0x2000
	s_add_i32 s26, s28, 0x4000
	s_add_i32 s23, s28, 0x6000
	s_cmp_lt_u32 s20, 64
	s_cselect_b64 s[6:7], -1, 0
	s_add_i32 s24, s28, 0x8000
	s_cmpk_lt_u32 s20, 0x140
	s_cselect_b64 s[8:9], -1, 0
	s_mov_b32 m0, s28
	s_and_b64 s[4:5], s[8:9], exec
	v_mov_b32_e32 v73, 0
	global_load_lds_dwordx4 v72, s[10:11]
	s_mov_b32 m0, s27
	s_cselect_b32 s3, 0xa000, 0
	v_add_u32_e32 v80, 0xfffffc00, v70
	global_load_lds_dwordx4 v68, s[10:11]
	s_mov_b32 m0, s26
	v_mov_b32_e32 v79, v73
	v_mov_b32_e32 v81, v73
	s_add_i32 s25, s28, s3
	global_load_lds_dwordx4 v66, s[10:11]
	s_mov_b32 m0, s23
	v_lshl_add_u64 v[4:5], s[10:11], 0, v[78:79]
	v_lshl_add_u64 v[6:7], s[16:17], 0, v[80:81]
	s_add_u32 s4, s10, 0x8400
	v_add_u32_e32 v76, 0x1c00, v70
	global_load_lds_dwordx4 v74, s[10:11]
	v_cndmask_b32_e64 v5, v7, v5, s[6:7]
	v_cndmask_b32_e64 v4, v6, v4, s[6:7]
	s_mov_b32 m0, s24
	v_mov_b32_e32 v77, v73
	s_addc_u32 s5, s11, 0
	v_lshl_add_u64 v[2:3], s[10:11], 0, v[72:73]
	global_load_lds_dwordx4 v[4:5], off
	v_lshl_add_u64 v[4:5], s[16:17], 0, v[76:77]
	s_add_u32 s18, s16, 0x3000
	v_cndmask_b32_e64 v3, v3, v5, s[8:9]
	v_cndmask_b32_e64 v2, v2, v4, s[8:9]
	s_mov_b32 m0, s25
	s_addc_u32 s19, s17, 0
	s_add_i32 s43, s28, 0xb400
	global_load_lds_dwordx4 v[2:3], off
	s_mov_b32 m0, s43
	s_add_i32 s42, s28, 0xd400
	global_load_lds_dwordx4 v72, s[4:5]
	s_mov_b32 m0, s42
	s_add_i32 s39, s28, 0xf400
	global_load_lds_dwordx4 v68, s[4:5]
	s_mov_b32 m0, s39
	s_add_i32 s36, s28, 0x11400
	global_load_lds_dwordx4 v66, s[4:5]
	s_mov_b32 m0, s36
	v_lshl_add_u64 v[2:3], s[4:5], 0, v[72:73]
	global_load_lds_dwordx4 v74, s[4:5]
	v_lshl_add_u64 v[4:5], s[4:5], 0, v[78:79]
	s_mul_hi_i32 s5, s2, 0x2400
	s_mul_i32 s4, s2, 0x2400
	s_add_i32 s37, s28, 0x13400
	s_add_i32 s35, s25, 0xb400
	s_lshl_b64 s[2:3], s[4:5], 2
	s_add_u32 s2, s12, s2
	v_lshl_add_u64 v[6:7], s[18:19], 0, v[80:81]
	s_addc_u32 s3, s13, s3
	s_lshl_b64 s[4:5], s[4:5], 1
	v_cndmask_b32_e64 v5, v7, v5, s[6:7]
	v_cndmask_b32_e64 v4, v6, v4, s[6:7]
	s_mov_b32 m0, s37
	s_add_u32 s12, s14, s4
	v_lshlrev_b32_e32 v123, 2, v0
	global_load_lds_dwordx4 v[4:5], off
	v_lshl_add_u64 v[4:5], s[18:19], 0, v[76:77]
	s_addc_u32 s13, s15, s5
	v_and_b32_e32 v1, 0x3fc, v123
	s_and_b32 s4, s30, 0xc00
	v_cndmask_b32_e64 v3, v3, v5, s[8:9]
	v_cndmask_b32_e64 v2, v2, v4, s[8:9]
	s_mov_b32 m0, s35
	s_add_i32 s38, s28, 0x22910
	s_add_i32 s33, s4, 0
	v_lshlrev_b32_e32 v84, 2, v1
	v_mov_b32_e32 v85, v73
	global_load_lds_dwordx4 v[2:3], off
	s_add_i32 s33, s33, 0x24910
	s_mov_b32 m0, s38
	v_lshl_add_u64 v[2:3], s[2:3], 0, v[84:85]
	s_mov_b64 s[18:19], 0x2000
	s_waitcnt vmcnt(6)
	s_barrier
	global_load_lds_dwordx4 v70, s[2:3] nt
	v_lshl_add_u64 v[2:3], v[2:3], 0, s[18:19]
	s_mov_b32 m0, s33
	v_and_b32_e32 v89, 15, v0
	global_load_lds_dwordx4 v[2:3], off nt
	v_or_b32_e32 v2, s29, v89
	v_add_u32_e32 v6, 1, v2
	v_lshlrev_b32_e32 v7, 6, v6
	v_lshlrev_b32_e32 v6, 3, v6
	v_and_b32_e32 v88, 48, v0
	v_and_b32_e32 v8, 0x3c0, v7
	v_and_b32_e32 v6, 32, v6
	v_lshlrev_b32_e32 v1, 6, v2
	v_bitop3_b32 v6, v8, v6, v88 bitop3:0x36
	s_movk_i32 s4, 0xf400
	v_add_u32_e32 v2, 2, v2
	v_and_or_b32 v94, v7, s4, v6
	v_lshlrev_b32_e32 v6, 6, v2
	v_lshlrev_b32_e32 v2, 3, v2
	v_and_b32_e32 v3, 0x3c0, v1
	v_and_b32_e32 v4, 0xfffff000, v1
	v_lshlrev_b32_e32 v1, 3, v0
	v_and_b32_e32 v7, 0x3c0, v6
	v_and_b32_e32 v2, 32, v2
	v_and_b32_e32 v5, 32, v1
	v_bitop3_b32 v2, v7, v2, v88 bitop3:0x36
	v_bitop3_b32 v3, v3, v5, v88 bitop3:0x36
	v_and_or_b32 v102, v6, s4, v2
	v_lshl_or_b32 v2, v89, 6, v88
	v_add3_u32 v91, 0, v3, v4
	v_xad_u32 v90, v2, v5, 0
	v_mov_b32_e32 v71, v73
	v_lshl_add_u64 v[82:83], s[12:13], 0, v[70:71]
	ds_read_b128 v[2:5], v91
	ds_read_b128 v[6:9], v91 offset:1024
	ds_read_b128 v[10:13], v91 offset:2048
	ds_read_b128 v[14:17], v91 offset:3072
	s_add_u32 s12, s16, 0x6000
	ds_read_b128 v[18:21], v90 offset:33792
	ds_read_b128 v[22:25], v90 offset:34816
	ds_read_b128 v[26:29], v90 offset:35840
	ds_read_b128 v[30:33], v90 offset:36864
	s_addc_u32 s13, s17, 0
	v_add_u32_e32 v71, 0, v94
	s_add_u32 s14, s10, 0x10800
	ds_read_b128 v[42:45], v71
	ds_read_b128 v[46:49], v71 offset:1024
	ds_read_b128 v[50:53], v71 offset:2048
	ds_read_b128 v[54:57], v71 offset:3072
	ds_read_b128 v[62:65], v90 offset:37888
	ds_read_b128 v[96:99], v90 offset:38912
	ds_read_b128 v[104:107], v90 offset:39936
	ds_read_b128 v[108:111], v90 offset:40960
	s_addc_u32 s15, s11, 0
	v_lshl_add_u64 v[34:35], s[14:15], 0, v[78:79]
	v_lshl_add_u64 v[36:37], s[12:13], 0, v[80:81]
	v_lshl_add_u64 v[38:39], s[12:13], 0, v[76:77]
	v_lshl_add_u64 v[40:41], s[14:15], 0, v[72:73]
	v_cndmask_b32_e64 v101, v37, v35, s[6:7]
	v_cndmask_b32_e64 v100, v36, v34, s[6:7]
	s_waitcnt lgkmcnt(0)
	v_mfma_f32_16x16x32_f16 v[34:37], v[18:21], v[2:5], 0
	v_cndmask_b32_e64 v121, v41, v39, s[8:9]
	v_cndmask_b32_e64 v120, v40, v38, s[8:9]
	s_movk_i32 s4, 0x180
	v_mfma_f32_16x16x32_f16 v[38:41], v[22:25], v[2:5], 0
	v_mov_b32_e32 v69, v73
	v_mov_b32_e32 v67, v73
	v_mov_b32_e32 v75, v73
	v_mfma_f32_16x16x32_f16 v[58:61], v[26:29], v[2:5], 0
	v_cmp_gt_u32_e64 s[4:5], s4, v0
	s_add_i32 s34, s28, 0x16800
	s_add_i32 s30, s28, 0x1e800
	v_mfma_f32_16x16x32_f16 v[2:5], v[30:33], v[2:5], 0
	s_add_i32 s31, s28, 0x1c800
	s_add_i32 s29, s25, 0x16800
	v_lshlrev_b32_e32 v87, 5, v0
	s_mov_b32 m0, s34
	s_nop 0
	global_load_lds_dwordx4 v72, s[14:15]
	v_mfma_f32_16x16x32_f16 v[112:115], v[18:21], v[6:9], 0
	s_add_i32 s40, s28, 0x18800
	v_mfma_f32_16x16x32_f16 v[116:119], v[22:25], v[6:9], 0
	v_mfma_f32_16x16x32_f16 v[124:127], v[26:29], v[6:9], 0
	v_mfma_f32_16x16x32_f16 v[6:9], v[30:33], v[6:9], 0
	s_mov_b32 m0, s40
	s_nop 0
	global_load_lds_dwordx4 v68, s[14:15]
	v_mfma_f32_16x16x32_f16 v[128:131], v[18:21], v[10:13], 0
	s_add_i32 s41, s28, 0x1a800
	v_mfma_f32_16x16x32_f16 v[132:135], v[22:25], v[10:13], 0
	v_mfma_f32_16x16x32_f16 v[136:139], v[26:29], v[10:13], 0
	v_mfma_f32_16x16x32_f16 v[10:13], v[30:33], v[10:13], 0
	s_mov_b32 m0, s41
	s_nop 0
	global_load_lds_dwordx4 v66, s[14:15]
	v_add_u32_e32 v92, 0, v102
	v_mfma_f32_16x16x32_f16 v[18:21], v[18:21], v[14:17], 0
	v_mfma_f32_16x16x32_f16 v[22:25], v[22:25], v[14:17], 0
	v_mfma_f32_16x16x32_f16 v[26:29], v[26:29], v[14:17], 0
	v_mfma_f32_16x16x32_f16 v[14:17], v[30:33], v[14:17], 0
	v_mfma_f32_16x16x32_f16 v[30:33], v[62:65], v[42:45], v[34:37]
	v_mfma_f32_16x16x32_f16 v[34:37], v[96:99], v[42:45], v[38:41]
	s_nop 2
	ds_read_b128 v[38:41], v92
	ds_read_b128 v[140:143], v92 offset:1024
	ds_read_b128 v[144:147], v92 offset:2048
	ds_read_b128 v[148:151], v92 offset:3072
	ds_read_b128 v[152:155], v90 offset:41984
	ds_read_b128 v[156:159], v90 offset:43008
	ds_read_b128 v[160:163], v90 offset:44032
	ds_read_b128 v[164:167], v90 offset:45056
	v_mfma_f32_16x16x32_f16 v[58:61], v[104:107], v[42:45], v[58:61]
	v_mfma_f32_16x16x32_f16 v[2:5], v[108:111], v[42:45], v[2:5]
	s_mov_b32 m0, s31
	s_nop 0
	global_load_lds_dwordx4 v74, s[14:15]
	v_mfma_f32_16x16x32_f16 v[42:45], v[62:65], v[46:49], v[112:115]
	v_mfma_f32_16x16x32_f16 v[112:115], v[96:99], v[46:49], v[116:119]
	v_mfma_f32_16x16x32_f16 v[116:119], v[104:107], v[46:49], v[124:127]
	v_mfma_f32_16x16x32_f16 v[6:9], v[108:111], v[46:49], v[6:9]
	s_mov_b32 m0, s30
	s_nop 0
	global_load_lds_dwordx4 v[100:101], off
	v_mfma_f32_16x16x32_f16 v[46:49], v[62:65], v[50:53], v[128:131]
	v_mfma_f32_16x16x32_f16 v[124:127], v[96:99], v[50:53], v[132:135]
	v_mfma_f32_16x16x32_f16 v[128:131], v[104:107], v[50:53], v[136:139]
	v_mfma_f32_16x16x32_f16 v[10:13], v[108:111], v[50:53], v[10:13]
	v_mfma_f32_16x16x32_f16 v[18:21], v[62:65], v[54:57], v[18:21]
	v_mfma_f32_16x16x32_f16 v[22:25], v[96:99], v[54:57], v[22:25]
	v_mfma_f32_16x16x32_f16 v[26:29], v[104:107], v[54:57], v[26:29]
	v_mfma_f32_16x16x32_f16 v[14:17], v[108:111], v[54:57], v[14:17]
	s_waitcnt lgkmcnt(0)
	v_mfma_f32_16x16x32_f16 v[30:33], v[152:155], v[38:41], v[30:33]
	v_mfma_f32_16x16x32_f16 v[34:37], v[156:159], v[38:41], v[34:37]
	v_mfma_f32_16x16x32_f16 v[50:53], v[160:163], v[38:41], v[58:61]
	v_mfma_f32_16x16x32_f16 v[2:5], v[164:167], v[38:41], v[2:5]
	s_mov_b32 m0, s29
	s_nop 0
	global_load_lds_dwordx4 v[120:121], off
	s_add_u32 s12, s16, 0x9000
	s_addc_u32 s13, s17, 0
	s_waitcnt vmcnt(8)
	v_add_u32_e32 v99, 0x13800, v90
	v_add_u32_e32 v101, 0x14000, v90
	s_add_u32 s14, s10, 0x18c00
	v_mfma_f32_16x16x32_f16 v[38:41], v[152:155], v[140:143], v[42:45]
	s_waitcnt lgkmcnt(0)
	s_barrier
	ds_read_b128 v[58:61], v91 offset:46080
	ds_read_b128 v[62:65], v91 offset:47104
	v_mfma_f32_16x16x32_f16 v[42:45], v[156:159], v[140:143], v[112:115]
	v_add_u32_e32 v100, 0x13c00, v90
	v_add_u32_e32 v103, 0x14400, v90
	s_addc_u32 s15, s11, 0
	v_mfma_f32_16x16x32_f16 v[54:57], v[160:163], v[140:143], v[116:119]
	ds_read_b128 v[106:109], v91 offset:48128
	s_nop 1
	ds_read_b128 v[116:119], v91 offset:49152
	ds_read_b128 v[132:135], v99
	ds_read_b128 v[136:139], v100
	v_lshl_add_u64 v[96:97], s[14:15], 0, v[78:79]
	v_mfma_f32_16x16x32_f16 v[6:9], v[164:167], v[140:143], v[6:9]
	v_lshl_add_u64 v[104:105], s[12:13], 0, v[80:81]
	v_cndmask_b32_e64 v97, v105, v97, s[6:7]
	v_cndmask_b32_e64 v96, v104, v96, s[6:7]
	v_mfma_f32_16x16x32_f16 v[46:49], v[152:155], v[144:147], v[46:49]
	v_lshl_add_u64 v[104:105], s[12:13], 0, v[76:77]
	v_lshl_add_u64 v[110:111], s[14:15], 0, v[72:73]
	v_cndmask_b32_e64 v113, v111, v105, s[8:9]
	v_mfma_f32_16x16x32_f16 v[124:127], v[156:159], v[144:147], v[124:127]
	v_cndmask_b32_e64 v112, v110, v104, s[8:9]
	v_add_u32_e32 v104, 0x14800, v90
	v_add_u32_e32 v111, 0x15000, v90
	v_mfma_f32_16x16x32_f16 v[128:131], v[160:163], v[144:147], v[128:131]
	v_add_u32_e32 v105, 0x14c00, v90
	v_add_u32_e32 v114, 0x15400, v90
	v_mfma_f32_16x16x32_f16 v[10:13], v[164:167], v[144:147], v[10:13]
	ds_read_b128 v[140:143], v101
	ds_read_b128 v[144:147], v103
	v_mfma_f32_16x16x32_f16 v[18:21], v[152:155], v[148:151], v[18:21]
	v_mfma_f32_16x16x32_f16 v[22:25], v[156:159], v[148:151], v[22:25]
	v_mfma_f32_16x16x32_f16 v[26:29], v[160:163], v[148:151], v[26:29]
	v_mfma_f32_16x16x32_f16 v[14:17], v[164:167], v[148:151], v[14:17]
	ds_read_b128 v[148:151], v71 offset:46080
	ds_read_b128 v[152:155], v71 offset:47104
	ds_read_b128 v[156:159], v71 offset:48128
	ds_read_b128 v[160:163], v71 offset:49152
	ds_read_b128 v[164:167], v104
	ds_read_b128 v[168:171], v105
	ds_read_b128 v[172:175], v111
	ds_read_b128 v[176:179], v114
	s_waitcnt lgkmcnt(0)
	v_mfma_f32_16x16x32_f16 v[30:33], v[132:135], v[58:61], v[30:33]
	v_mfma_f32_16x16x32_f16 v[34:37], v[136:139], v[58:61], v[34:37]
	v_mfma_f32_16x16x32_f16 v[50:53], v[140:143], v[58:61], v[50:53]
	v_mfma_f32_16x16x32_f16 v[2:5], v[144:147], v[58:61], v[2:5]
	s_mov_b32 m0, s28
	s_nop 0
	global_load_lds_dwordx4 v72, s[14:15]
	v_mfma_f32_16x16x32_f16 v[38:41], v[132:135], v[62:65], v[38:41]
	v_mfma_f32_16x16x32_f16 v[42:45], v[136:139], v[62:65], v[42:45]
	v_mfma_f32_16x16x32_f16 v[54:57], v[140:143], v[62:65], v[54:57]
	v_mfma_f32_16x16x32_f16 v[6:9], v[144:147], v[62:65], v[6:9]
	s_mov_b32 m0, s27
	s_nop 0
	global_load_lds_dwordx4 v68, s[14:15]
	v_mfma_f32_16x16x32_f16 v[46:49], v[132:135], v[106:109], v[46:49]
	v_mfma_f32_16x16x32_f16 v[58:61], v[136:139], v[106:109], v[124:127]
	v_mfma_f32_16x16x32_f16 v[62:65], v[140:143], v[106:109], v[128:131]
	v_mfma_f32_16x16x32_f16 v[10:13], v[144:147], v[106:109], v[10:13]
	s_mov_b32 m0, s26
	s_nop 0
	global_load_lds_dwordx4 v66, s[14:15]
	v_add_u32_e32 v108, 0x15800, v90
	v_add_u32_e32 v115, 0x16000, v90
	v_mfma_f32_16x16x32_f16 v[18:21], v[132:135], v[116:119], v[18:21]
	v_add_u32_e32 v109, 0x15c00, v90
	v_mfma_f32_16x16x32_f16 v[22:25], v[136:139], v[116:119], v[22:25]
	v_mfma_f32_16x16x32_f16 v[26:29], v[140:143], v[116:119], v[26:29]
	v_mfma_f32_16x16x32_f16 v[14:17], v[144:147], v[116:119], v[14:17]
	ds_read_b128 v[118:121], v92 offset:46080
	ds_read_b128 v[124:127], v92 offset:47104
	ds_read_b128 v[128:131], v92 offset:48128
	ds_read_b128 v[132:135], v92 offset:49152
	ds_read_b128 v[136:139], v108
	ds_read_b128 v[140:143], v109
	v_add_u32_e32 v116, 0x16400, v90
	ds_read_b128 v[144:147], v115
	ds_read_b128 v[180:183], v116
	v_mfma_f32_16x16x32_f16 v[30:33], v[164:167], v[148:151], v[30:33]
	v_mfma_f32_16x16x32_f16 v[34:37], v[168:171], v[148:151], v[34:37]
	v_mfma_f32_16x16x32_f16 v[50:53], v[172:175], v[148:151], v[50:53]
	v_mfma_f32_16x16x32_f16 v[2:5], v[176:179], v[148:151], v[2:5]
	s_mov_b32 m0, s23
	s_nop 0
	global_load_lds_dwordx4 v74, s[14:15]
	v_mfma_f32_16x16x32_f16 v[6:9], v[176:179], v[152:155], v[6:9]
	v_mfma_f32_16x16x32_f16 v[148:151], v[164:167], v[152:155], v[38:41]
	v_mfma_f32_16x16x32_f16 v[184:187], v[168:171], v[152:155], v[42:45]
	v_mfma_f32_16x16x32_f16 v[188:191], v[172:175], v[152:155], v[54:57]
	s_mov_b32 m0, s24
	s_nop 0
	global_load_lds_dwordx4 v[96:97], off
	v_mfma_f32_16x16x32_f16 v[192:195], v[168:171], v[156:159], v[58:61]
	v_mfma_f32_16x16x32_f16 v[196:199], v[172:175], v[156:159], v[62:65]
	v_mfma_f32_16x16x32_f16 v[10:13], v[176:179], v[156:159], v[10:13]
	v_mfma_f32_16x16x32_f16 v[18:21], v[164:167], v[160:163], v[18:21]
	s_waitcnt lgkmcnt(0)
	v_mfma_f32_16x16x32_f16 v[62:65], v[136:139], v[118:121], v[30:33]
	v_mfma_f32_16x16x32_f16 v[58:61], v[140:143], v[118:121], v[34:37]
	v_mfma_f32_16x16x32_f16 v[54:57], v[144:147], v[118:121], v[50:53]
	v_mfma_f32_16x16x32_f16 v[38:41], v[180:183], v[118:121], v[2:5]
	v_mfma_f32_16x16x32_f16 v[152:155], v[164:167], v[156:159], v[46:49]
	v_mfma_f32_16x16x32_f16 v[156:159], v[168:171], v[160:163], v[22:25]
	v_mfma_f32_16x16x32_f16 v[164:167], v[172:175], v[160:163], v[26:29]
	v_mfma_f32_16x16x32_f16 v[160:163], v[176:179], v[160:163], v[14:17]
	s_mov_b32 m0, s25
	s_nop 0
	global_load_lds_dwordx4 v[112:113], off
	v_mfma_f32_16x16x32_f16 v[42:45], v[136:139], v[124:127], v[148:151]
	s_waitcnt vmcnt(6)
	s_waitcnt lgkmcnt(0)
	v_add_u32_e32 v107, 0, v87
	v_mfma_f32_16x16x32_f16 v[46:49], v[140:143], v[124:127], v[184:187]
	s_barrier
	v_mfma_f32_16x16x32_f16 v[50:53], v[144:147], v[124:127], v[188:191]
	v_mfma_f32_16x16x32_f16 v[34:37], v[180:183], v[124:127], v[6:9]
	v_mfma_f32_16x16x32_f16 v[22:25], v[136:139], v[128:131], v[152:155]
	v_mfma_f32_16x16x32_f16 v[26:29], v[140:143], v[128:131], v[192:195]
	v_mfma_f32_16x16x32_f16 v[30:33], v[144:147], v[128:131], v[196:199]
	v_mfma_f32_16x16x32_f16 v[14:17], v[180:183], v[128:131], v[10:13]
	v_mfma_f32_16x16x32_f16 v[2:5], v[136:139], v[132:135], v[18:21]
	v_mfma_f32_16x16x32_f16 v[6:9], v[140:143], v[132:135], v[156:159]
	v_mfma_f32_16x16x32_f16 v[10:13], v[144:147], v[132:135], v[164:167]
	v_mfma_f32_16x16x32_f16 v[18:21], v[180:183], v[132:135], v[160:163]
	s_and_saveexec_b64 s[12:13], s[4:5]
	s_cbranch_execz .LBB2_2
	v_add_u32_e32 v87, 0x22910, v107
	ds_read_b128 v[118:121], v87 offset:16
	ds_read_b128 v[124:127], v87
	s_waitcnt lgkmcnt(0)
	v_cvt_pk_f16_f32 v121, v120, v121
	v_cvt_pk_f16_f32 v120, v118, v119
	v_cvt_pk_f16_f32 v119, v126, v127
	v_cvt_pk_f16_f32 v118, v124, v125
	global_store_dwordx4 v[200:201], v[118:121], off
.LBB2_2:
	s_or_b64 exec, exec, s[12:13]
	s_add_u32 s44, s16, 0xc000
	s_addc_u32 s45, s17, 0
	v_add_u32_e32 v95, 0x16800, v91
	v_add_u32_e32 v87, 0x17000, v91
	v_add_u32_e32 v106, 0x1ec00, v90
	v_add_u32_e32 v97, 0x1f400, v90
	s_add_u32 s46, s10, 0x21000
	v_add_u32_e32 v96, 0x16c00, v91
	ds_read_b128 v[124:127], v95
	ds_read_b128 v[128:131], v96
	v_add_u32_e32 v93, 0x17400, v91
	ds_read_b128 v[132:135], v87
	ds_read_b128 v[136:139], v93
	v_add_u32_e32 v110, 0x1f000, v90
	ds_read_b128 v[140:143], v106
	ds_read_b128 v[144:147], v110
	v_add_u32_e32 v98, 0x1f800, v90
	ds_read_b128 v[148:151], v97
	ds_read_b128 v[152:155], v98
	s_addc_u32 s47, s11, 0
	v_lshl_add_u64 v[112:113], s[46:47], 0, v[78:79]
	v_lshl_add_u64 v[118:119], s[44:45], 0, v[80:81]
	v_cndmask_b32_e64 v189, v119, v113, s[6:7]
	v_cndmask_b32_e64 v188, v118, v112, s[6:7]
	v_lshl_add_u64 v[112:113], s[44:45], 0, v[76:77]
	v_lshl_add_u64 v[120:121], s[46:47], 0, v[72:73]
	s_add_i32 s44, 0, 0x16800
	v_cndmask_b32_e64 v192, v120, v112, s[8:9]
	v_add_u32_e32 v94, s44, v94
	v_add_u32_e32 v117, 0x1fc00, v90
	v_add_u32_e32 v112, 0x20400, v90
	s_load_dwordx4 s[12:15], s[0:1], 0x10
	v_cndmask_b32_e64 v193, v121, v113, s[8:9]
	ds_read_b128 v[156:159], v94
	ds_read_b128 v[160:163], v94 offset:1024
	ds_read_b128 v[164:167], v94 offset:2048
	ds_read_b128 v[168:171], v94 offset:3072
	v_add_u32_e32 v118, 0x20000, v90
	ds_read_b128 v[172:175], v117
	ds_read_b128 v[176:179], v118
	v_add_u32_e32 v113, 0x20800, v90
	ds_read_b128 v[180:183], v112
	ds_read_b128 v[184:187], v113
	s_waitcnt lgkmcnt(0)
	v_mfma_f32_16x16x32_f16 v[62:65], v[140:143], v[124:127], v[62:65]
	v_lshl_add_u64 v[190:191], s[46:47], 0, v[74:75]
	v_mfma_f32_16x16x32_f16 v[58:61], v[144:147], v[124:127], v[58:61]
	v_mfma_f32_16x16x32_f16 v[54:57], v[148:151], v[124:127], v[54:57]
	v_mfma_f32_16x16x32_f16 v[38:41], v[152:155], v[124:127], v[38:41]
	s_mov_b32 m0, s43
	s_nop 0
	global_load_lds_dwordx4 v[120:121], off
	v_mfma_f32_16x16x32_f16 v[42:45], v[140:143], v[128:131], v[42:45]
	v_lshl_add_u64 v[120:121], s[46:47], 0, v[68:69]
	v_mfma_f32_16x16x32_f16 v[46:49], v[144:147], v[128:131], v[46:49]
	v_mfma_f32_16x16x32_f16 v[50:53], v[148:151], v[128:131], v[50:53]
	v_mfma_f32_16x16x32_f16 v[34:37], v[152:155], v[128:131], v[34:37]
	s_mov_b32 m0, s42
	s_nop 0
	global_load_lds_dwordx4 v[120:121], off
	v_mfma_f32_16x16x32_f16 v[22:25], v[140:143], v[132:135], v[22:25]
	v_lshl_add_u64 v[120:121], s[46:47], 0, v[66:67]
	v_mfma_f32_16x16x32_f16 v[26:29], v[144:147], v[132:135], v[26:29]
	v_mfma_f32_16x16x32_f16 v[30:33], v[148:151], v[132:135], v[30:33]
	v_mfma_f32_16x16x32_f16 v[14:17], v[152:155], v[132:135], v[14:17]
	s_mov_b32 m0, s39
	s_nop 0
	global_load_lds_dwordx4 v[120:121], off
	v_add_u32_e32 v102, s44, v102
	v_add_u32_e32 v121, 0x20c00, v90
	v_add_u32_e32 v119, 0x21400, v90
	v_mfma_f32_16x16x32_f16 v[2:5], v[140:143], v[136:139], v[2:5]
	ds_read_b128 v[124:127], v102
	ds_read_b128 v[128:131], v102 offset:1024
	v_add_u32_e32 v122, 0x21000, v90
	v_add_u32_e32 v120, 0x21800, v90
	v_mfma_f32_16x16x32_f16 v[6:9], v[144:147], v[136:139], v[6:9]
	v_mfma_f32_16x16x32_f16 v[10:13], v[148:151], v[136:139], v[10:13]
	v_mfma_f32_16x16x32_f16 v[18:21], v[152:155], v[136:139], v[18:21]
	ds_read_b128 v[132:135], v102 offset:2048
	ds_read_b128 v[136:139], v102 offset:3072
	ds_read_b128 v[140:143], v121
	ds_read_b128 v[144:147], v122
	ds_read_b128 v[148:151], v119
	ds_read_b128 v[152:155], v120
	v_mfma_f32_16x16x32_f16 v[62:65], v[172:175], v[156:159], v[62:65]
	v_mfma_f32_16x16x32_f16 v[58:61], v[176:179], v[156:159], v[58:61]
	v_mfma_f32_16x16x32_f16 v[54:57], v[180:183], v[156:159], v[54:57]
	v_mfma_f32_16x16x32_f16 v[38:41], v[184:187], v[156:159], v[38:41]
	s_mov_b32 m0, s36
	s_nop 0
	global_load_lds_dwordx4 v[190:191], off
	v_mfma_f32_16x16x32_f16 v[42:45], v[172:175], v[160:163], v[42:45]
	v_mfma_f32_16x16x32_f16 v[46:49], v[176:179], v[160:163], v[46:49]
	v_mfma_f32_16x16x32_f16 v[50:53], v[180:183], v[160:163], v[50:53]
	v_mfma_f32_16x16x32_f16 v[34:37], v[184:187], v[160:163], v[34:37]
	s_mov_b32 m0, s37
	s_nop 0
	global_load_lds_dwordx4 v[188:189], off
	v_mfma_f32_16x16x32_f16 v[22:25], v[172:175], v[164:167], v[22:25]
	v_mfma_f32_16x16x32_f16 v[26:29], v[176:179], v[164:167], v[26:29]
	v_mfma_f32_16x16x32_f16 v[30:33], v[180:183], v[164:167], v[30:33]
	v_mfma_f32_16x16x32_f16 v[14:17], v[184:187], v[164:167], v[14:17]
	v_mfma_f32_16x16x32_f16 v[2:5], v[172:175], v[168:171], v[2:5]
	v_mfma_f32_16x16x32_f16 v[6:9], v[176:179], v[168:171], v[6:9]
	v_mfma_f32_16x16x32_f16 v[10:13], v[180:183], v[168:171], v[10:13]
	v_mfma_f32_16x16x32_f16 v[18:21], v[184:187], v[168:171], v[18:21]
	s_waitcnt lgkmcnt(0)
	v_mfma_f32_16x16x32_f16 v[62:65], v[140:143], v[124:127], v[62:65]
	v_mfma_f32_16x16x32_f16 v[58:61], v[144:147], v[124:127], v[58:61]
	v_mfma_f32_16x16x32_f16 v[54:57], v[148:151], v[124:127], v[54:57]
	v_mfma_f32_16x16x32_f16 v[38:41], v[152:155], v[124:127], v[38:41]
	s_mov_b32 m0, s35
	s_nop 0
	global_load_lds_dwordx4 v[192:193], off
	s_add_u32 s44, s2, 0x3000
	s_addc_u32 s45, s3, 0
	s_mov_b32 m0, s38
	s_waitcnt vmcnt(6)
	v_lshlrev_b32_e32 v123, 2, v123
	v_lshl_add_u64 v[124:125], s[44:45], 0, v[84:85]
	s_waitcnt lgkmcnt(0)
	s_barrier
	global_load_lds_dwordx4 v123, s[44:45] nt
	v_lshl_add_u64 v[124:125], v[124:125], 0, s[18:19]
	s_mov_b32 m0, s33
	s_add_u32 s18, s16, 0xf000
	global_load_lds_dwordx4 v[124:125], off nt
	s_addc_u32 s19, s17, 0
	s_add_u32 s44, s10, 0x29400
	v_mfma_f32_16x16x32_f16 v[42:45], v[140:143], v[128:131], v[42:45]
	s_addc_u32 s45, s11, 0
	v_lshl_add_u64 v[192:193], s[44:45], 0, v[72:73]
	v_lshl_add_u64 v[190:191], s[44:45], 0, v[74:75]
	v_mfma_f32_16x16x32_f16 v[46:49], v[144:147], v[128:131], v[46:49]
	v_mfma_f32_16x16x32_f16 v[50:53], v[148:151], v[128:131], v[50:53]
	v_mfma_f32_16x16x32_f16 v[34:37], v[152:155], v[128:131], v[34:37]
	ds_read_b128 v[124:127], v91
	ds_read_b128 v[128:131], v91 offset:1024
	v_mfma_f32_16x16x32_f16 v[22:25], v[140:143], v[132:135], v[22:25]
	v_mfma_f32_16x16x32_f16 v[26:29], v[144:147], v[132:135], v[26:29]
	v_mfma_f32_16x16x32_f16 v[30:33], v[148:151], v[132:135], v[30:33]
	v_mfma_f32_16x16x32_f16 v[14:17], v[152:155], v[132:135], v[14:17]
	ds_read_b128 v[132:135], v91 offset:2048
	ds_read_b128 v[156:159], v91 offset:3072
	v_mfma_f32_16x16x32_f16 v[2:5], v[140:143], v[136:139], v[2:5]
	ds_read_b128 v[140:143], v90 offset:33792
	ds_read_b128 v[160:163], v90 offset:34816
	v_mfma_f32_16x16x32_f16 v[6:9], v[144:147], v[136:139], v[6:9]
	ds_read_b128 v[144:147], v90 offset:35840
	ds_read_b128 v[164:167], v90 offset:36864
	v_mfma_f32_16x16x32_f16 v[10:13], v[148:151], v[136:139], v[10:13]
	v_lshl_add_u64 v[148:149], s[44:45], 0, v[78:79]
	v_lshl_add_u64 v[150:151], s[18:19], 0, v[80:81]
	v_cndmask_b32_e64 v189, v151, v149, s[6:7]
	v_mfma_f32_16x16x32_f16 v[18:21], v[152:155], v[136:139], v[18:21]
	v_lshl_add_u64 v[136:137], s[18:19], 0, v[76:77]
	v_cndmask_b32_e64 v188, v150, v148, s[6:7]
	v_cndmask_b32_e64 v195, v193, v137, s[8:9]
	v_cndmask_b32_e64 v194, v192, v136, s[8:9]
	ds_read_b128 v[136:139], v71
	ds_read_b128 v[148:151], v71 offset:1024
	ds_read_b128 v[152:155], v71 offset:2048
	ds_read_b128 v[168:171], v71 offset:3072
	ds_read_b128 v[172:175], v90 offset:37888
	ds_read_b128 v[176:179], v90 offset:38912
	ds_read_b128 v[180:183], v90 offset:39936
	ds_read_b128 v[184:187], v90 offset:40960
	s_waitcnt lgkmcnt(0)
	v_mfma_f32_16x16x32_f16 v[62:65], v[140:143], v[124:127], v[62:65]
	v_mfma_f32_16x16x32_f16 v[58:61], v[160:163], v[124:127], v[58:61]
	v_mfma_f32_16x16x32_f16 v[54:57], v[144:147], v[124:127], v[54:57]
	v_mfma_f32_16x16x32_f16 v[38:41], v[164:167], v[124:127], v[38:41]
	s_mov_b32 m0, s34
	s_nop 0
	global_load_lds_dwordx4 v[192:193], off
	v_mfma_f32_16x16x32_f16 v[42:45], v[140:143], v[128:131], v[42:45]
	v_lshl_add_u64 v[124:125], s[44:45], 0, v[68:69]
	v_mfma_f32_16x16x32_f16 v[46:49], v[160:163], v[128:131], v[46:49]
	v_mfma_f32_16x16x32_f16 v[50:53], v[144:147], v[128:131], v[50:53]
	v_mfma_f32_16x16x32_f16 v[34:37], v[164:167], v[128:131], v[34:37]
	s_mov_b32 m0, s40
	s_nop 0
	global_load_lds_dwordx4 v[124:125], off
	v_mfma_f32_16x16x32_f16 v[22:25], v[140:143], v[132:135], v[22:25]
	v_lshl_add_u64 v[124:125], s[44:45], 0, v[66:67]
	v_mfma_f32_16x16x32_f16 v[26:29], v[160:163], v[132:135], v[26:29]
	v_mfma_f32_16x16x32_f16 v[30:33], v[144:147], v[132:135], v[30:33]
	v_mfma_f32_16x16x32_f16 v[14:17], v[164:167], v[132:135], v[14:17]
	s_mov_b32 m0, s41
	s_nop 0
	global_load_lds_dwordx4 v[124:125], off
	v_mfma_f32_16x16x32_f16 v[2:5], v[140:143], v[156:159], v[2:5]
	ds_read_b128 v[124:127], v92
	ds_read_b128 v[128:131], v92 offset:1024
	ds_read_b128 v[132:135], v92 offset:2048
	ds_read_b128 v[140:143], v92 offset:3072
	v_mfma_f32_16x16x32_f16 v[6:9], v[160:163], v[156:159], v[6:9]
	v_mfma_f32_16x16x32_f16 v[10:13], v[144:147], v[156:159], v[10:13]
	v_mfma_f32_16x16x32_f16 v[18:21], v[164:167], v[156:159], v[18:21]
	ds_read_b128 v[144:147], v90 offset:41984
	ds_read_b128 v[156:159], v90 offset:43008
	ds_read_b128 v[160:163], v90 offset:44032
	ds_read_b128 v[164:167], v90 offset:45056
	v_mfma_f32_16x16x32_f16 v[62:65], v[172:175], v[136:139], v[62:65]
	v_mfma_f32_16x16x32_f16 v[58:61], v[176:179], v[136:139], v[58:61]
	v_mfma_f32_16x16x32_f16 v[54:57], v[180:183], v[136:139], v[54:57]
	v_mfma_f32_16x16x32_f16 v[38:41], v[184:187], v[136:139], v[38:41]
	s_mov_b32 m0, s31
	s_nop 0
	global_load_lds_dwordx4 v[190:191], off
	v_mfma_f32_16x16x32_f16 v[42:45], v[172:175], v[148:151], v[42:45]
	v_mfma_f32_16x16x32_f16 v[46:49], v[176:179], v[148:151], v[46:49]
	v_mfma_f32_16x16x32_f16 v[50:53], v[180:183], v[148:151], v[50:53]
	v_mfma_f32_16x16x32_f16 v[34:37], v[184:187], v[148:151], v[34:37]
	s_mov_b32 m0, s30
	s_nop 0
	global_load_lds_dwordx4 v[188:189], off
	v_mfma_f32_16x16x32_f16 v[22:25], v[172:175], v[152:155], v[22:25]
	v_mfma_f32_16x16x32_f16 v[26:29], v[176:179], v[152:155], v[26:29]
	v_mfma_f32_16x16x32_f16 v[30:33], v[180:183], v[152:155], v[30:33]
	v_mfma_f32_16x16x32_f16 v[14:17], v[184:187], v[152:155], v[14:17]
	v_mfma_f32_16x16x32_f16 v[2:5], v[172:175], v[168:171], v[2:5]
	v_mfma_f32_16x16x32_f16 v[6:9], v[176:179], v[168:171], v[6:9]
	v_mfma_f32_16x16x32_f16 v[10:13], v[180:183], v[168:171], v[10:13]
	v_mfma_f32_16x16x32_f16 v[18:21], v[184:187], v[168:171], v[18:21]
	s_waitcnt lgkmcnt(0)
	v_mfma_f32_16x16x32_f16 v[62:65], v[144:147], v[124:127], v[62:65]
	v_mfma_f32_16x16x32_f16 v[58:61], v[156:159], v[124:127], v[58:61]
	v_mfma_f32_16x16x32_f16 v[54:57], v[160:163], v[124:127], v[54:57]
	v_mfma_f32_16x16x32_f16 v[38:41], v[164:167], v[124:127], v[38:41]
	s_mov_b32 m0, s29
	s_nop 0
	global_load_lds_dwordx4 v[194:195], off
	s_add_u32 s18, s16, 0x12000
	s_addc_u32 s19, s17, 0
	s_waitcnt vmcnt(8)
	s_add_u32 s44, s10, 0x31800
	v_mfma_f32_16x16x32_f16 v[42:45], v[144:147], v[128:131], v[42:45]
	s_waitcnt lgkmcnt(0)
	s_barrier
	s_addc_u32 s45, s11, 0
	v_mfma_f32_16x16x32_f16 v[46:49], v[156:159], v[128:131], v[46:49]
	v_lshl_add_u64 v[192:193], s[44:45], 0, v[72:73]
	v_lshl_add_u64 v[190:191], s[44:45], 0, v[74:75]
	v_mfma_f32_16x16x32_f16 v[50:53], v[160:163], v[128:131], v[50:53]
	v_mfma_f32_16x16x32_f16 v[34:37], v[164:167], v[128:131], v[34:37]
	ds_read_b128 v[124:127], v91 offset:46080
	ds_read_b128 v[128:131], v91 offset:47104
	v_mfma_f32_16x16x32_f16 v[22:25], v[144:147], v[132:135], v[22:25]
	v_mfma_f32_16x16x32_f16 v[26:29], v[156:159], v[132:135], v[26:29]
	v_mfma_f32_16x16x32_f16 v[30:33], v[160:163], v[132:135], v[30:33]
	v_mfma_f32_16x16x32_f16 v[14:17], v[164:167], v[132:135], v[14:17]
	ds_read_b128 v[132:135], v91 offset:48128
	ds_read_b128 v[136:139], v91 offset:49152
	v_mfma_f32_16x16x32_f16 v[2:5], v[144:147], v[140:143], v[2:5]
	ds_read_b128 v[144:147], v99
	ds_read_b128 v[148:151], v100
	v_mfma_f32_16x16x32_f16 v[6:9], v[156:159], v[140:143], v[6:9]
	ds_read_b128 v[152:155], v101
	ds_read_b128 v[156:159], v103
	v_mfma_f32_16x16x32_f16 v[10:13], v[160:163], v[140:143], v[10:13]
	v_lshl_add_u64 v[160:161], s[44:45], 0, v[78:79]
	v_lshl_add_u64 v[162:163], s[18:19], 0, v[80:81]
	v_cndmask_b32_e64 v189, v163, v161, s[6:7]
	v_mfma_f32_16x16x32_f16 v[18:21], v[164:167], v[140:143], v[18:21]
	v_lshl_add_u64 v[140:141], s[18:19], 0, v[76:77]
	v_cndmask_b32_e64 v188, v162, v160, s[6:7]
	v_cndmask_b32_e64 v195, v193, v141, s[8:9]
	v_cndmask_b32_e64 v194, v192, v140, s[8:9]
	ds_read_b128 v[140:143], v71 offset:46080
	ds_read_b128 v[160:163], v71 offset:47104
	ds_read_b128 v[164:167], v71 offset:48128
	ds_read_b128 v[168:171], v71 offset:49152
	ds_read_b128 v[172:175], v104
	ds_read_b128 v[176:179], v105
	ds_read_b128 v[180:183], v111
	ds_read_b128 v[184:187], v114
	s_waitcnt lgkmcnt(0)
	v_mfma_f32_16x16x32_f16 v[62:65], v[144:147], v[124:127], v[62:65]
	v_mfma_f32_16x16x32_f16 v[58:61], v[148:151], v[124:127], v[58:61]
	v_mfma_f32_16x16x32_f16 v[54:57], v[152:155], v[124:127], v[54:57]
	v_mfma_f32_16x16x32_f16 v[38:41], v[156:159], v[124:127], v[38:41]
	s_mov_b32 m0, s28
	s_nop 0
	global_load_lds_dwordx4 v[192:193], off
	v_mfma_f32_16x16x32_f16 v[42:45], v[144:147], v[128:131], v[42:45]
	v_lshl_add_u64 v[124:125], s[44:45], 0, v[68:69]
	v_mfma_f32_16x16x32_f16 v[46:49], v[148:151], v[128:131], v[46:49]
	v_mfma_f32_16x16x32_f16 v[50:53], v[152:155], v[128:131], v[50:53]
	v_mfma_f32_16x16x32_f16 v[34:37], v[156:159], v[128:131], v[34:37]
	s_mov_b32 m0, s27
	s_nop 0
	global_load_lds_dwordx4 v[124:125], off
	v_mfma_f32_16x16x32_f16 v[22:25], v[144:147], v[132:135], v[22:25]
	v_lshl_add_u64 v[124:125], s[44:45], 0, v[66:67]
	v_mfma_f32_16x16x32_f16 v[26:29], v[148:151], v[132:135], v[26:29]
	v_mfma_f32_16x16x32_f16 v[30:33], v[152:155], v[132:135], v[30:33]
	v_mfma_f32_16x16x32_f16 v[14:17], v[156:159], v[132:135], v[14:17]
	s_mov_b32 m0, s26
	s_nop 0
	global_load_lds_dwordx4 v[124:125], off
	v_mfma_f32_16x16x32_f16 v[2:5], v[144:147], v[136:139], v[2:5]
	v_mfma_f32_16x16x32_f16 v[6:9], v[148:151], v[136:139], v[6:9]
	v_mfma_f32_16x16x32_f16 v[10:13], v[152:155], v[136:139], v[10:13]
	v_mfma_f32_16x16x32_f16 v[18:21], v[156:159], v[136:139], v[18:21]
	ds_read_b128 v[124:127], v92 offset:46080
	ds_read_b128 v[128:131], v92 offset:47104
	ds_read_b128 v[132:135], v92 offset:48128
	ds_read_b128 v[136:139], v92 offset:49152
	ds_read_b128 v[144:147], v108
	ds_read_b128 v[148:151], v109
	ds_read_b128 v[152:155], v115
	ds_read_b128 v[156:159], v116
	v_mfma_f32_16x16x32_f16 v[62:65], v[172:175], v[140:143], v[62:65]
	v_mfma_f32_16x16x32_f16 v[58:61], v[176:179], v[140:143], v[58:61]
	v_mfma_f32_16x16x32_f16 v[54:57], v[180:183], v[140:143], v[54:57]
	v_mfma_f32_16x16x32_f16 v[38:41], v[184:187], v[140:143], v[38:41]
	s_mov_b32 m0, s23
	s_nop 0
	global_load_lds_dwordx4 v[190:191], off
	v_mfma_f32_16x16x32_f16 v[42:45], v[172:175], v[160:163], v[42:45]
	v_mfma_f32_16x16x32_f16 v[46:49], v[176:179], v[160:163], v[46:49]
	v_mfma_f32_16x16x32_f16 v[50:53], v[180:183], v[160:163], v[50:53]
	v_mfma_f32_16x16x32_f16 v[34:37], v[184:187], v[160:163], v[34:37]
	s_mov_b32 m0, s24
	s_nop 0
	global_load_lds_dwordx4 v[188:189], off
	v_mfma_f32_16x16x32_f16 v[22:25], v[172:175], v[164:167], v[22:25]
	v_mfma_f32_16x16x32_f16 v[26:29], v[176:179], v[164:167], v[26:29]
	v_mfma_f32_16x16x32_f16 v[30:33], v[180:183], v[164:167], v[30:33]
	v_mfma_f32_16x16x32_f16 v[14:17], v[184:187], v[164:167], v[14:17]
	v_mfma_f32_16x16x32_f16 v[2:5], v[172:175], v[168:171], v[2:5]
	v_mfma_f32_16x16x32_f16 v[6:9], v[176:179], v[168:171], v[6:9]
	v_mfma_f32_16x16x32_f16 v[10:13], v[180:183], v[168:171], v[10:13]
	v_mfma_f32_16x16x32_f16 v[18:21], v[184:187], v[168:171], v[18:21]
	s_waitcnt lgkmcnt(0)
	v_mfma_f32_16x16x32_f16 v[62:65], v[144:147], v[124:127], v[62:65]
	v_mfma_f32_16x16x32_f16 v[58:61], v[148:151], v[124:127], v[58:61]
	v_mfma_f32_16x16x32_f16 v[54:57], v[152:155], v[124:127], v[54:57]
	v_mfma_f32_16x16x32_f16 v[38:41], v[156:159], v[124:127], v[38:41]
	s_mov_b32 m0, s25
	s_nop 0
	global_load_lds_dwordx4 v[194:195], off
	v_mfma_f32_16x16x32_f16 v[42:45], v[144:147], v[128:131], v[42:45]
	s_waitcnt vmcnt(6)
	s_waitcnt lgkmcnt(0)
	s_barrier
	v_mfma_f32_16x16x32_f16 v[46:49], v[148:151], v[128:131], v[46:49]
	v_mfma_f32_16x16x32_f16 v[50:53], v[152:155], v[128:131], v[50:53]
	v_mfma_f32_16x16x32_f16 v[34:37], v[156:159], v[128:131], v[34:37]
	v_mfma_f32_16x16x32_f16 v[22:25], v[144:147], v[132:135], v[22:25]
	v_mfma_f32_16x16x32_f16 v[26:29], v[148:151], v[132:135], v[26:29]
	v_mfma_f32_16x16x32_f16 v[30:33], v[152:155], v[132:135], v[30:33]
	v_mfma_f32_16x16x32_f16 v[14:17], v[156:159], v[132:135], v[14:17]
	v_mfma_f32_16x16x32_f16 v[2:5], v[144:147], v[136:139], v[2:5]
	v_mfma_f32_16x16x32_f16 v[6:9], v[148:151], v[136:139], v[6:9]
	v_mfma_f32_16x16x32_f16 v[10:13], v[152:155], v[136:139], v[10:13]
	v_mfma_f32_16x16x32_f16 v[18:21], v[156:159], v[136:139], v[18:21]
	s_and_saveexec_b64 s[18:19], s[4:5]
	s_cbranch_execz .LBB2_4
	v_add_u32_e32 v85, 0x22910, v107
	ds_read_b128 v[124:127], v85 offset:16
	ds_read_b128 v[128:131], v85
	s_waitcnt lgkmcnt(0)
	v_cvt_pk_f16_f32 v127, v126, v127
	v_cvt_pk_f16_f32 v126, v124, v125
	v_cvt_pk_f16_f32 v124, v128, v129
	v_add_co_u32_e32 v128, vcc, 0x1000, v82
	v_cvt_pk_f16_f32 v125, v130, v131
	s_nop 0
	v_addc_co_u32_e32 v129, vcc, 0, v83, vcc
	global_store_dwordx4 v[200:201], v[124:127], off offset:128
.LBB2_4:
	s_or_b64 exec, exec, s[18:19]
	s_add_u32 s18, s16, 0x15000
	s_addc_u32 s19, s17, 0
	s_add_u32 s44, s10, 0x39c00
	s_addc_u32 s45, s11, 0
	ds_read_b128 v[124:127], v95
	ds_read_b128 v[128:131], v96
	ds_read_b128 v[132:135], v87
	ds_read_b128 v[136:139], v93
	ds_read_b128 v[140:143], v106
	ds_read_b128 v[144:147], v110
	ds_read_b128 v[148:151], v97
	ds_read_b128 v[152:155], v98
	v_lshl_add_u64 v[156:157], s[44:45], 0, v[78:79]
	v_lshl_add_u64 v[158:159], s[18:19], 0, v[80:81]
	v_cndmask_b32_e64 v189, v159, v157, s[6:7]
	v_cndmask_b32_e64 v188, v158, v156, s[6:7]
	v_lshl_add_u64 v[156:157], s[18:19], 0, v[76:77]
	v_lshl_add_u64 v[192:193], s[44:45], 0, v[72:73]
	v_cndmask_b32_e64 v195, v193, v157, s[8:9]
	v_cndmask_b32_e64 v194, v192, v156, s[8:9]
	ds_read_b128 v[156:159], v94
	ds_read_b128 v[160:163], v94 offset:1024
	ds_read_b128 v[164:167], v94 offset:2048
	ds_read_b128 v[168:171], v94 offset:3072
	ds_read_b128 v[172:175], v117
	ds_read_b128 v[176:179], v118
	ds_read_b128 v[180:183], v112
	ds_read_b128 v[184:187], v113
	s_load_dwordx2 s[0:1], s[0:1], 0x20
	s_waitcnt lgkmcnt(0)
	v_mfma_f32_16x16x32_f16 v[62:65], v[140:143], v[124:127], v[62:65]
	v_lshl_add_u64 v[190:191], s[44:45], 0, v[74:75]
	v_mfma_f32_16x16x32_f16 v[58:61], v[144:147], v[124:127], v[58:61]
	v_mfma_f32_16x16x32_f16 v[54:57], v[148:151], v[124:127], v[54:57]
	v_mfma_f32_16x16x32_f16 v[38:41], v[152:155], v[124:127], v[38:41]
	s_mov_b32 m0, s43
	s_nop 0
	global_load_lds_dwordx4 v[192:193], off
	v_mfma_f32_16x16x32_f16 v[42:45], v[140:143], v[128:131], v[42:45]
	v_lshl_add_u64 v[124:125], s[44:45], 0, v[68:69]
	v_mfma_f32_16x16x32_f16 v[46:49], v[144:147], v[128:131], v[46:49]
	v_mfma_f32_16x16x32_f16 v[50:53], v[148:151], v[128:131], v[50:53]
	v_mfma_f32_16x16x32_f16 v[34:37], v[152:155], v[128:131], v[34:37]
	s_mov_b32 m0, s42
	s_nop 0
	global_load_lds_dwordx4 v[124:125], off
	v_mfma_f32_16x16x32_f16 v[22:25], v[140:143], v[132:135], v[22:25]
	v_lshl_add_u64 v[124:125], s[44:45], 0, v[66:67]
	v_mfma_f32_16x16x32_f16 v[26:29], v[144:147], v[132:135], v[26:29]
	v_mfma_f32_16x16x32_f16 v[30:33], v[148:151], v[132:135], v[30:33]
	v_mfma_f32_16x16x32_f16 v[14:17], v[152:155], v[132:135], v[14:17]
	s_mov_b32 m0, s39
	s_nop 0
	global_load_lds_dwordx4 v[124:125], off
	v_mfma_f32_16x16x32_f16 v[2:5], v[140:143], v[136:139], v[2:5]
	v_mfma_f32_16x16x32_f16 v[6:9], v[144:147], v[136:139], v[6:9]
	v_mfma_f32_16x16x32_f16 v[10:13], v[148:151], v[136:139], v[10:13]
	v_mfma_f32_16x16x32_f16 v[18:21], v[152:155], v[136:139], v[18:21]
	ds_read_b128 v[124:127], v102
	ds_read_b128 v[128:131], v102 offset:1024
	ds_read_b128 v[132:135], v102 offset:2048
	ds_read_b128 v[136:139], v102 offset:3072
	ds_read_b128 v[140:143], v121
	ds_read_b128 v[144:147], v122
	ds_read_b128 v[148:151], v119
	ds_read_b128 v[152:155], v120
	v_mfma_f32_16x16x32_f16 v[62:65], v[172:175], v[156:159], v[62:65]
	v_mfma_f32_16x16x32_f16 v[58:61], v[176:179], v[156:159], v[58:61]
	v_mfma_f32_16x16x32_f16 v[54:57], v[180:183], v[156:159], v[54:57]
	v_mfma_f32_16x16x32_f16 v[38:41], v[184:187], v[156:159], v[38:41]
	s_mov_b32 m0, s36
	s_nop 0
	global_load_lds_dwordx4 v[190:191], off
	v_mfma_f32_16x16x32_f16 v[42:45], v[172:175], v[160:163], v[42:45]
	v_mfma_f32_16x16x32_f16 v[46:49], v[176:179], v[160:163], v[46:49]
	v_mfma_f32_16x16x32_f16 v[50:53], v[180:183], v[160:163], v[50:53]
	v_mfma_f32_16x16x32_f16 v[34:37], v[184:187], v[160:163], v[34:37]
	s_mov_b32 m0, s37
	s_nop 0
	global_load_lds_dwordx4 v[188:189], off
	v_mfma_f32_16x16x32_f16 v[22:25], v[172:175], v[164:167], v[22:25]
	v_mfma_f32_16x16x32_f16 v[26:29], v[176:179], v[164:167], v[26:29]
	v_mfma_f32_16x16x32_f16 v[30:33], v[180:183], v[164:167], v[30:33]
	v_mfma_f32_16x16x32_f16 v[14:17], v[184:187], v[164:167], v[14:17]
	v_mfma_f32_16x16x32_f16 v[2:5], v[172:175], v[168:171], v[2:5]
	v_mfma_f32_16x16x32_f16 v[6:9], v[176:179], v[168:171], v[6:9]
	v_mfma_f32_16x16x32_f16 v[10:13], v[180:183], v[168:171], v[10:13]
	v_mfma_f32_16x16x32_f16 v[18:21], v[184:187], v[168:171], v[18:21]
	s_waitcnt lgkmcnt(0)
	v_mfma_f32_16x16x32_f16 v[62:65], v[140:143], v[124:127], v[62:65]
	v_mfma_f32_16x16x32_f16 v[58:61], v[144:147], v[124:127], v[58:61]
	v_mfma_f32_16x16x32_f16 v[54:57], v[148:151], v[124:127], v[54:57]
	v_mfma_f32_16x16x32_f16 v[38:41], v[152:155], v[124:127], v[38:41]
	s_mov_b32 m0, s35
	s_nop 0
	global_load_lds_dwordx4 v[194:195], off
	s_add_u32 s2, s2, 0x6000
	s_mov_b32 m0, s38
	s_waitcnt vmcnt(6)
	s_addc_u32 s3, s3, 0
	v_mov_b32_e32 v85, 0
	s_waitcnt lgkmcnt(0)
	s_barrier
	global_load_lds_dwordx4 v123, s[2:3] nt
	v_lshl_add_u64 v[84:85], s[2:3], 0, v[84:85]
	s_mov_b64 s[2:3], 0x2000
	v_lshl_add_u64 v[84:85], v[84:85], 0, s[2:3]
	s_mov_b32 m0, s33
	s_add_u32 s2, s16, 0x18000
	global_load_lds_dwordx4 v[84:85], off nt
	s_addc_u32 s3, s17, 0
	s_add_u32 s18, s10, 0x42000
	v_mfma_f32_16x16x32_f16 v[42:45], v[140:143], v[128:131], v[42:45]
	s_addc_u32 s19, s11, 0
	v_lshl_add_u64 v[84:85], s[18:19], 0, v[78:79]
	v_lshl_add_u64 v[190:191], s[18:19], 0, v[72:73]
	v_mfma_f32_16x16x32_f16 v[46:49], v[144:147], v[128:131], v[46:49]
	v_lshl_add_u64 v[188:189], s[18:19], 0, v[74:75]
	v_mfma_f32_16x16x32_f16 v[50:53], v[148:151], v[128:131], v[50:53]
	v_mfma_f32_16x16x32_f16 v[34:37], v[152:155], v[128:131], v[34:37]
	ds_read_b128 v[124:127], v91
	ds_read_b128 v[128:131], v91 offset:1024
	v_mfma_f32_16x16x32_f16 v[22:25], v[140:143], v[132:135], v[22:25]
	v_mfma_f32_16x16x32_f16 v[26:29], v[144:147], v[132:135], v[26:29]
	v_mfma_f32_16x16x32_f16 v[30:33], v[148:151], v[132:135], v[30:33]
	v_mfma_f32_16x16x32_f16 v[14:17], v[152:155], v[132:135], v[14:17]
	ds_read_b128 v[132:135], v91 offset:2048
	ds_read_b128 v[156:159], v91 offset:3072
	v_mfma_f32_16x16x32_f16 v[2:5], v[140:143], v[136:139], v[2:5]
	ds_read_b128 v[140:143], v90 offset:33792
	ds_read_b128 v[160:163], v90 offset:34816
	v_mfma_f32_16x16x32_f16 v[6:9], v[144:147], v[136:139], v[6:9]
	ds_read_b128 v[144:147], v90 offset:35840
	ds_read_b128 v[164:167], v90 offset:36864
	v_mfma_f32_16x16x32_f16 v[10:13], v[148:151], v[136:139], v[10:13]
	v_lshl_add_u64 v[148:149], s[2:3], 0, v[80:81]
	v_cndmask_b32_e64 v85, v149, v85, s[6:7]
	v_cndmask_b32_e64 v84, v148, v84, s[6:7]
	v_mfma_f32_16x16x32_f16 v[18:21], v[152:155], v[136:139], v[18:21]
	v_lshl_add_u64 v[136:137], s[2:3], 0, v[76:77]
	v_cndmask_b32_e64 v193, v191, v137, s[8:9]
	v_cndmask_b32_e64 v192, v190, v136, s[8:9]
	ds_read_b128 v[136:139], v71
	ds_read_b128 v[148:151], v71 offset:1024
	ds_read_b128 v[152:155], v71 offset:2048
	ds_read_b128 v[168:171], v71 offset:3072
	ds_read_b128 v[172:175], v90 offset:37888
	ds_read_b128 v[176:179], v90 offset:38912
	ds_read_b128 v[180:183], v90 offset:39936
	ds_read_b128 v[184:187], v90 offset:40960
	s_waitcnt lgkmcnt(0)
	v_mfma_f32_16x16x32_f16 v[62:65], v[140:143], v[124:127], v[62:65]
	v_mfma_f32_16x16x32_f16 v[58:61], v[160:163], v[124:127], v[58:61]
	v_mfma_f32_16x16x32_f16 v[54:57], v[144:147], v[124:127], v[54:57]
	v_mfma_f32_16x16x32_f16 v[38:41], v[164:167], v[124:127], v[38:41]
	s_mov_b32 m0, s34
	s_nop 0
	global_load_lds_dwordx4 v[190:191], off
	v_mfma_f32_16x16x32_f16 v[42:45], v[140:143], v[128:131], v[42:45]
	v_lshl_add_u64 v[124:125], s[18:19], 0, v[68:69]
	v_mfma_f32_16x16x32_f16 v[46:49], v[160:163], v[128:131], v[46:49]
	v_mfma_f32_16x16x32_f16 v[50:53], v[144:147], v[128:131], v[50:53]
	v_mfma_f32_16x16x32_f16 v[34:37], v[164:167], v[128:131], v[34:37]
	s_mov_b32 m0, s40
	s_nop 0
	global_load_lds_dwordx4 v[124:125], off
	v_mfma_f32_16x16x32_f16 v[22:25], v[140:143], v[132:135], v[22:25]
	v_lshl_add_u64 v[124:125], s[18:19], 0, v[66:67]
	v_mfma_f32_16x16x32_f16 v[26:29], v[160:163], v[132:135], v[26:29]
	v_mfma_f32_16x16x32_f16 v[30:33], v[144:147], v[132:135], v[30:33]
	v_mfma_f32_16x16x32_f16 v[14:17], v[164:167], v[132:135], v[14:17]
	s_mov_b32 m0, s41
	s_nop 0
	global_load_lds_dwordx4 v[124:125], off
	v_mfma_f32_16x16x32_f16 v[2:5], v[140:143], v[156:159], v[2:5]
	ds_read_b128 v[124:127], v92
	ds_read_b128 v[128:131], v92 offset:1024
	ds_read_b128 v[132:135], v92 offset:2048
	ds_read_b128 v[140:143], v92 offset:3072
	v_mfma_f32_16x16x32_f16 v[6:9], v[160:163], v[156:159], v[6:9]
	v_mfma_f32_16x16x32_f16 v[10:13], v[144:147], v[156:159], v[10:13]
	v_mfma_f32_16x16x32_f16 v[18:21], v[164:167], v[156:159], v[18:21]
	ds_read_b128 v[144:147], v90 offset:41984
	ds_read_b128 v[156:159], v90 offset:43008
	ds_read_b128 v[160:163], v90 offset:44032
	ds_read_b128 v[164:167], v90 offset:45056
	v_mfma_f32_16x16x32_f16 v[62:65], v[172:175], v[136:139], v[62:65]
	v_mfma_f32_16x16x32_f16 v[58:61], v[176:179], v[136:139], v[58:61]
	v_mfma_f32_16x16x32_f16 v[54:57], v[180:183], v[136:139], v[54:57]
	v_mfma_f32_16x16x32_f16 v[38:41], v[184:187], v[136:139], v[38:41]
	s_mov_b32 m0, s31
	s_nop 0
	global_load_lds_dwordx4 v[188:189], off
	v_mfma_f32_16x16x32_f16 v[42:45], v[172:175], v[148:151], v[42:45]
	v_mfma_f32_16x16x32_f16 v[46:49], v[176:179], v[148:151], v[46:49]
	v_mfma_f32_16x16x32_f16 v[50:53], v[180:183], v[148:151], v[50:53]
	v_mfma_f32_16x16x32_f16 v[34:37], v[184:187], v[148:151], v[34:37]
	s_mov_b32 m0, s30
	s_nop 0
	global_load_lds_dwordx4 v[84:85], off
	v_mfma_f32_16x16x32_f16 v[22:25], v[172:175], v[152:155], v[22:25]
	v_mfma_f32_16x16x32_f16 v[26:29], v[176:179], v[152:155], v[26:29]
	v_mfma_f32_16x16x32_f16 v[30:33], v[180:183], v[152:155], v[30:33]
	v_mfma_f32_16x16x32_f16 v[14:17], v[184:187], v[152:155], v[14:17]
	v_mfma_f32_16x16x32_f16 v[2:5], v[172:175], v[168:171], v[2:5]
	v_mfma_f32_16x16x32_f16 v[6:9], v[176:179], v[168:171], v[6:9]
	v_mfma_f32_16x16x32_f16 v[10:13], v[180:183], v[168:171], v[10:13]
	v_mfma_f32_16x16x32_f16 v[18:21], v[184:187], v[168:171], v[18:21]
	s_waitcnt lgkmcnt(0)
	v_mfma_f32_16x16x32_f16 v[62:65], v[144:147], v[124:127], v[62:65]
	v_mfma_f32_16x16x32_f16 v[58:61], v[156:159], v[124:127], v[58:61]
	v_mfma_f32_16x16x32_f16 v[54:57], v[160:163], v[124:127], v[54:57]
	v_mfma_f32_16x16x32_f16 v[38:41], v[164:167], v[124:127], v[38:41]
	s_mov_b32 m0, s29
	s_nop 0
	global_load_lds_dwordx4 v[192:193], off
	s_add_u32 s2, s16, 0x1b000
	s_addc_u32 s3, s17, 0
	s_waitcnt vmcnt(8)
	s_add_u32 s10, s10, 0x4a400
	v_mfma_f32_16x16x32_f16 v[42:45], v[144:147], v[128:131], v[42:45]
	s_waitcnt lgkmcnt(0)
	s_barrier
	s_addc_u32 s11, s11, 0
	v_mfma_f32_16x16x32_f16 v[46:49], v[156:159], v[128:131], v[46:49]
	v_lshl_add_u64 v[78:79], s[10:11], 0, v[78:79]
	v_lshl_add_u64 v[80:81], s[2:3], 0, v[80:81]
	v_lshl_add_u64 v[84:85], s[10:11], 0, v[74:75]
	v_mfma_f32_16x16x32_f16 v[50:53], v[160:163], v[128:131], v[50:53]
	v_lshl_add_u64 v[74:75], s[2:3], 0, v[76:77]
	v_cndmask_b32_e64 v81, v81, v79, s[6:7]
	v_cndmask_b32_e64 v80, v80, v78, s[6:7]
	v_mfma_f32_16x16x32_f16 v[34:37], v[164:167], v[128:131], v[34:37]
	ds_read_b128 v[124:127], v91 offset:46080
	ds_read_b128 v[128:131], v91 offset:47104
	v_mfma_f32_16x16x32_f16 v[22:25], v[144:147], v[132:135], v[22:25]
	v_mfma_f32_16x16x32_f16 v[26:29], v[156:159], v[132:135], v[26:29]
	v_mfma_f32_16x16x32_f16 v[30:33], v[160:163], v[132:135], v[30:33]
	v_mfma_f32_16x16x32_f16 v[14:17], v[164:167], v[132:135], v[14:17]
	ds_read_b128 v[132:135], v91 offset:48128
	ds_read_b128 v[136:139], v91 offset:49152
	v_mfma_f32_16x16x32_f16 v[2:5], v[144:147], v[140:143], v[2:5]
	ds_read_b128 v[144:147], v99
	ds_read_b128 v[148:151], v100
	v_mfma_f32_16x16x32_f16 v[6:9], v[156:159], v[140:143], v[6:9]
	ds_read_b128 v[152:155], v101
	ds_read_b128 v[156:159], v103
	v_lshl_add_u64 v[100:101], s[10:11], 0, v[72:73]
	v_cndmask_b32_e64 v181, v101, v75, s[8:9]
	v_mfma_f32_16x16x32_f16 v[10:13], v[160:163], v[140:143], v[10:13]
	v_cndmask_b32_e64 v180, v100, v74, s[8:9]
	v_mfma_f32_16x16x32_f16 v[18:21], v[164:167], v[140:143], v[18:21]
	ds_read_b128 v[72:75], v71 offset:46080
	ds_read_b128 v[76:79], v71 offset:47104
	ds_read_b128 v[140:143], v71 offset:48128
	ds_read_b128 v[160:163], v71 offset:49152
	ds_read_b128 v[164:167], v104
	ds_read_b128 v[168:171], v105
	ds_read_b128 v[172:175], v111
	ds_read_b128 v[176:179], v114
	s_waitcnt lgkmcnt(0)
	v_mfma_f32_16x16x32_f16 v[62:65], v[144:147], v[124:127], v[62:65]
	v_mfma_f32_16x16x32_f16 v[58:61], v[148:151], v[124:127], v[58:61]
	v_mfma_f32_16x16x32_f16 v[54:57], v[152:155], v[124:127], v[54:57]
	v_mfma_f32_16x16x32_f16 v[38:41], v[156:159], v[124:127], v[38:41]
	s_mov_b32 m0, s28
	s_nop 0
	global_load_lds_dwordx4 v[100:101], off
	v_mfma_f32_16x16x32_f16 v[42:45], v[144:147], v[128:131], v[42:45]
	v_lshl_add_u64 v[68:69], s[10:11], 0, v[68:69]
	v_mfma_f32_16x16x32_f16 v[46:49], v[148:151], v[128:131], v[46:49]
	v_mfma_f32_16x16x32_f16 v[50:53], v[152:155], v[128:131], v[50:53]
	v_mfma_f32_16x16x32_f16 v[34:37], v[156:159], v[128:131], v[34:37]
	s_mov_b32 m0, s27
	s_nop 0
	global_load_lds_dwordx4 v[68:69], off
	v_mfma_f32_16x16x32_f16 v[22:25], v[144:147], v[132:135], v[22:25]
	v_lshl_add_u64 v[66:67], s[10:11], 0, v[66:67]
	v_mfma_f32_16x16x32_f16 v[26:29], v[148:151], v[132:135], v[26:29]
	v_mfma_f32_16x16x32_f16 v[30:33], v[152:155], v[132:135], v[30:33]
	v_mfma_f32_16x16x32_f16 v[14:17], v[156:159], v[132:135], v[14:17]
	s_mov_b32 m0, s26
	s_nop 0
	global_load_lds_dwordx4 v[66:67], off
	v_mfma_f32_16x16x32_f16 v[2:5], v[144:147], v[136:139], v[2:5]
	ds_read_b128 v[66:69], v92 offset:46080
	ds_read_b128 v[124:127], v92 offset:47104
	ds_read_b128 v[128:131], v92 offset:48128
	ds_read_b128 v[132:135], v92 offset:49152
	v_mfma_f32_16x16x32_f16 v[6:9], v[148:151], v[136:139], v[6:9]
	v_mfma_f32_16x16x32_f16 v[10:13], v[152:155], v[136:139], v[10:13]
	v_mfma_f32_16x16x32_f16 v[18:21], v[156:159], v[136:139], v[18:21]
	ds_read_b128 v[136:139], v108
	ds_read_b128 v[144:147], v109
	ds_read_b128 v[148:151], v115
	ds_read_b128 v[152:155], v116
	v_mfma_f32_16x16x32_f16 v[62:65], v[164:167], v[72:75], v[62:65]
	v_mfma_f32_16x16x32_f16 v[58:61], v[168:171], v[72:75], v[58:61]
	v_mfma_f32_16x16x32_f16 v[54:57], v[172:175], v[72:75], v[54:57]
	v_mfma_f32_16x16x32_f16 v[38:41], v[176:179], v[72:75], v[38:41]
	s_mov_b32 m0, s23
	s_nop 0
	global_load_lds_dwordx4 v[84:85], off
	v_mfma_f32_16x16x32_f16 v[42:45], v[164:167], v[76:79], v[42:45]
	v_mfma_f32_16x16x32_f16 v[34:37], v[176:179], v[76:79], v[34:37]
	v_mfma_f32_16x16x32_f16 v[72:75], v[168:171], v[76:79], v[46:49]
	v_mfma_f32_16x16x32_f16 v[156:159], v[172:175], v[76:79], v[50:53]
	s_mov_b32 m0, s24
	s_nop 0
	global_load_lds_dwordx4 v[80:81], off
	v_mfma_f32_16x16x32_f16 v[22:25], v[164:167], v[140:143], v[22:25]
	v_mfma_f32_16x16x32_f16 v[26:29], v[168:171], v[140:143], v[26:29]
	v_mfma_f32_16x16x32_f16 v[30:33], v[172:175], v[140:143], v[30:33]
	v_mfma_f32_16x16x32_f16 v[76:79], v[176:179], v[140:143], v[14:17]
	v_mfma_f32_16x16x32_f16 v[140:143], v[164:167], v[160:163], v[2:5]
	v_mfma_f32_16x16x32_f16 v[164:167], v[168:171], v[160:163], v[6:9]
	v_mfma_f32_16x16x32_f16 v[168:171], v[172:175], v[160:163], v[10:13]
	s_waitcnt lgkmcnt(0)
	v_mfma_f32_16x16x32_f16 v[14:17], v[136:139], v[66:69], v[62:65]
	v_mfma_f32_16x16x32_f16 v[10:13], v[144:147], v[66:69], v[58:61]
	v_mfma_f32_16x16x32_f16 v[2:5], v[148:151], v[66:69], v[54:57]
	v_mfma_f32_16x16x32_f16 v[6:9], v[152:155], v[66:69], v[38:41]
	v_mfma_f32_16x16x32_f16 v[160:163], v[176:179], v[160:163], v[18:21]
	s_mov_b32 m0, s25
	s_nop 0
	global_load_lds_dwordx4 v[180:181], off
	v_mfma_f32_16x16x32_f16 v[46:49], v[136:139], v[124:127], v[42:45]
	s_waitcnt vmcnt(6)
	s_waitcnt lgkmcnt(0)
	s_barrier
	v_mfma_f32_16x16x32_f16 v[50:53], v[144:147], v[124:127], v[72:75]
	v_mfma_f32_16x16x32_f16 v[54:57], v[148:151], v[124:127], v[156:159]
	v_mfma_f32_16x16x32_f16 v[58:61], v[152:155], v[124:127], v[34:37]
	v_mfma_f32_16x16x32_f16 v[18:21], v[136:139], v[128:131], v[22:25]
	v_mfma_f32_16x16x32_f16 v[22:25], v[144:147], v[128:131], v[26:29]
	v_mfma_f32_16x16x32_f16 v[26:29], v[148:151], v[128:131], v[30:33]
	v_mfma_f32_16x16x32_f16 v[30:33], v[152:155], v[128:131], v[76:79]
	v_mfma_f32_16x16x32_f16 v[34:37], v[136:139], v[132:135], v[140:143]
	v_mfma_f32_16x16x32_f16 v[38:41], v[144:147], v[132:135], v[164:167]
	v_mfma_f32_16x16x32_f16 v[42:45], v[148:151], v[132:135], v[168:171]
	v_mfma_f32_16x16x32_f16 v[62:65], v[152:155], v[132:135], v[160:163]
	s_and_saveexec_b64 s[2:3], s[4:5]
	s_cbranch_execz .LBB2_6
	v_add_u32_e32 v72, 0x22910, v107
	ds_read_b128 v[66:69], v72 offset:16
	ds_read_b128 v[72:75], v72
	s_waitcnt lgkmcnt(0)
	v_cvt_pk_f16_f32 v69, v68, v69
	v_cvt_pk_f16_f32 v68, v66, v67
	v_cvt_pk_f16_f32 v66, v72, v73
	v_add_co_u32_e32 v72, vcc, 0x3000, v82
	v_cvt_pk_f16_f32 v67, v74, v75
	s_nop 0
	v_addc_co_u32_e32 v73, vcc, 0, v83, vcc
	global_store_dwordx4 v[200:201], v[66:69], off offset:256

	.amdhsa_kernel _ZN12_GLOBAL__N_110k_convpoolEPKtS1_PKfPKiPtS3_S6_
		.amdhsa_group_segment_fixed_size 0
		.amdhsa_private_segment_fixed_size 0
		.amdhsa_kernarg_size 56
		.amdhsa_user_sgpr_count 2
		.amdhsa_user_sgpr_dispatch_ptr 0
		.amdhsa_user_sgpr_queue_ptr 0
		.amdhsa_user_sgpr_kernarg_segment_ptr 1
		.amdhsa_user_sgpr_dispatch_id 0
		.amdhsa_user_sgpr_kernarg_preload_length 0
		.amdhsa_user_sgpr_kernarg_preload_offset 0
		.amdhsa_user_sgpr_private_segment_size 0
		.amdhsa_uses_dynamic_stack 0
		.amdhsa_enable_private_segment 0
		.amdhsa_system_sgpr_workgroup_id_x 1
		.amdhsa_system_sgpr_workgroup_id_y 0
		.amdhsa_system_sgpr_workgroup_id_z 0
		.amdhsa_system_sgpr_workgroup_info 0
		.amdhsa_system_vgpr_workitem_id 0
		.amdhsa_next_free_vgpr 208
		.amdhsa_next_free_sgpr 52
		.amdhsa_accum_offset 208
		.amdhsa_reserve_vcc 1
		.amdhsa_float_round_mode_32 0
		.amdhsa_float_round_mode_16_64 0
		.amdhsa_float_denorm_mode_32 3
		.amdhsa_float_denorm_mode_16_64 3
		.amdhsa_dx10_clamp 1
		.amdhsa_ieee_mode 1
		.amdhsa_fp16_overflow 0
		.amdhsa_tg_split 0
		.amdhsa_exception_fp_ieee_invalid_op 0
		.amdhsa_exception_fp_denorm_src 0
		.amdhsa_exception_fp_ieee_div_zero 0
		.amdhsa_exception_fp_ieee_overflow 0
		.amdhsa_exception_fp_ieee_underflow 0
		.amdhsa_exception_fp_ieee_inexact 0
		.amdhsa_exception_int_div_zero 0
	.end_amdhsa_kernel

_ZN12_GLOBAL__N_14k_fcEPKtPKiS1_PKfS5_Pf:
	s_load_dwordx8 s[4:11], s[0:1], 0x0
	s_load_dwordx4 s[12:15], s[0:1], 0x20
	s_and_b32 s3, s2, 7
	s_lshr_b32 s20, s2, 3
	s_lshr_b32 s19, s20, 2
	s_lshl_b32 s3, s3, 3
	s_add_u32 s19, s19, s3
	s_and_b32 s20, s20, 3
	v_lshrrev_b32_e32 v1, 6, v0
	v_and_b32_e32 v12, 63, v0
	v_and_b32_e32 v13, 15, v0
	v_readfirstlane_b32 s16, v1
	v_lshrrev_b32_e32 v14, 4, v12
	s_nop 3
	s_lshr_b32 s17, s16, 2
	s_and_b32 s18, s16, 3
	v_lshrrev_b32_e32 v70, 2, v12
	s_lshl_b32 s90, s19, 8
	s_lshl_b32 s91, s16, 5
	s_add_u32 s90, s90, s91
	v_add_u32_e32 v73, s90, v70
	v_add_u32_e32 v74, 16, v73
	v_lshlrev_b32_e32 v75, 3, v73
	v_lshlrev_b32_e32 v76, 3, v74
	s_waitcnt lgkmcnt(0)
	global_load_dwordx2 v[64:65], v75, s[6:7]
	global_load_dwordx2 v[66:67], v76, s[6:7]
	s_mul_i32 s90, s20, 0x180
	s_mul_i32 s91, s18, 96
	s_add_u32 s90, s90, s91
	v_lshl_add_u32 v15, v14, 2, s90
	v_lshlrev_b32_e32 v15, 2, v15
	global_load_dwordx4 v[16:19], v15, s[10:11] offset:0
	global_load_dwordx4 v[20:23], v15, s[10:11] offset:64
	global_load_dwordx4 v[24:27], v15, s[10:11] offset:128
	global_load_dwordx4 v[28:31], v15, s[10:11] offset:192
	global_load_dwordx4 v[32:35], v15, s[10:11] offset:256
	global_load_dwordx4 v[36:39], v15, s[10:11] offset:320
	v_mul_u32_u24_e32 v77, 0x1800, v13
	v_add_u32_e32 v77, v77, v15
	v_mov_b32_e32 v40, 0
	v_mov_b32_e32 v41, 0
	v_mov_b32_e32 v42, 0
	v_mov_b32_e32 v43, 0
	v_mov_b32_e32 v44, 0
	v_mov_b32_e32 v45, 0
	v_mov_b32_e32 v46, 0
	v_mov_b32_e32 v47, 0
	v_mov_b32_e32 v48, 0
	v_mov_b32_e32 v49, 0
	v_mov_b32_e32 v50, 0
	v_mov_b32_e32 v51, 0
	v_mov_b32_e32 v52, 0
	v_mov_b32_e32 v53, 0
	v_mov_b32_e32 v54, 0
	v_mov_b32_e32 v55, 0
	v_mov_b32_e32 v56, 0
	v_mov_b32_e32 v57, 0
	v_mov_b32_e32 v58, 0
	v_mov_b32_e32 v59, 0
	v_mov_b32_e32 v60, 0
	v_mov_b32_e32 v61, 0
	v_mov_b32_e32 v62, 0
	v_mov_b32_e32 v63, 0
	s_mov_b32 exec_lo, 0xff00ff
	s_mov_b32 exec_hi, 0xff00ff
	global_load_dwordx4 v[40:43], v77, s[12:13] offset:0
	global_load_dwordx4 v[44:47], v77, s[12:13] offset:64
	global_load_dwordx4 v[48:51], v77, s[12:13] offset:128
	global_load_dwordx4 v[52:55], v77, s[12:13] offset:192
	global_load_dwordx4 v[56:59], v77, s[12:13] offset:256
	global_load_dwordx4 v[60:63], v77, s[12:13] offset:320
	s_mov_b64 exec, -1
	v_lshlrev_b32_e32 v15, 6, v13
	v_lshl_add_u32 v15, v14, 4, v15
	v_lshrrev_b32_e32 v78, 3, v13
	v_lshlrev_b32_e32 v78, 5, v78
	v_xor_b32_e32 v15, v15, v78
	s_lshl_b32 s90, s17, 13
	v_add_u32_e32 v1, s90, v15
	v_add_u32_e32 v2, 0x14000, v1
	s_mul_i32 s90, s18, 0x1800
	s_add_u32 s90, s90, 0x4000
	v_add_u32_e32 v3, s90, v15
	v_add_u32_e32 v4, 0x14000, v3
	v_and_b32_e32 v71, 3, v12
	v_lshrrev_b32_e32 v72, 5, v12
	v_lshlrev_b32_e32 v72, 1, v72
	v_xor_b32_e32 v71, v71, v72
	v_lshlrev_b32_e32 v71, 4, v71
	v_lshl_add_u32 v11, v70, 6, v71
	s_mul_i32 s90, s20, 0x180
	s_mul_i32 s91, s16, 48
	s_add_u32 s90, s90, s91
	s_lshl_b32 s90, s90, 6
	s_add_u32 s28, s8, s90
	s_addc_u32 s29, s9, 0
	s_add_u32 s30, s28, 0x18000
	s_addc_u32 s31, s29, 0
	s_add_u32 s32, s28, 0x400
	s_addc_u32 s33, s29, 0
	s_add_u32 s34, s32, 0x18000
	s_addc_u32 s35, s33, 0
	s_add_u32 s36, s28, 0x800
	s_addc_u32 s37, s29, 0
	s_add_u32 s38, s36, 0x18000
	s_addc_u32 s39, s37, 0
	s_mov_b64 s[24:25], s[4:5]
	s_add_u32 s26, s4, 64
	s_addc_u32 s27, s5, 0
	s_add_u32 s96, s4, 0x1000000
	s_addc_u32 s97, s5, 0
	s_lshl_b32 s22, s16, 11
	s_mul_i32 s23, s16, 0xc00
	s_add_u32 s23, s23, 0x4000
	s_mov_b32 s21, 0
	s_lshr_b32 s92, s19, 1
	s_lshl_b32 s92, s92, 9
	s_movk_i32 s93, 0x1ff
	s_movk_i32 s94, 0x200
	s_waitcnt vmcnt(12)
	v_med3_i32 v64, v64, 0, s93
	v_med3_i32 v65, v65, 1, s94
	v_med3_i32 v66, v66, 0, s93
	v_med3_i32 v67, v67, 1, s94
	v_add_u32_e32 v64, s92, v64
	v_add_u32_e32 v66, s92, v66
	v_add_u32_e32 v65, s92, v65
	v_add_u32_e32 v67, s92, v67
	v_add_u32_e32 v65, -1, v65
	v_add_u32_e32 v67, -1, v67
	v_lshl_add_u32 v5, v64, 10, v71
	v_lshl_add_u32 v6, v66, 10, v71
	v_lshl_add_u32 v7, v73, 10, v71
	v_lshl_add_u32 v8, v74, 10, v71
	v_lshl_add_u32 v9, v65, 10, v71
	v_lshl_add_u32 v10, v67, 10, v71
	s_cmp_lg_u32 s17, 0
	s_cbranch_scc1 .Lfc_h1_entry
	s_add_u32 m0, s22, 0x0
	s_nop 0
	global_load_lds_dwordx4 v5, s[24:25]
	s_add_u32 m0, s22, 0x400
	s_nop 0
	global_load_lds_dwordx4 v6, s[24:25]
	s_add_u32 m0, s23, 0x0
	s_nop 0
	global_load_lds_dwordx4 v11, s[28:29]
	s_add_u32 m0, s23, 0x400
	s_nop 0
	global_load_lds_dwordx4 v11, s[32:33]
	s_add_u32 m0, s23, 0x800
	s_nop 0
	global_load_lds_dwordx4 v11, s[36:37]
	s_add_u32 s24, s24, 0x80
	s_addc_u32 s25, s25, 0
	s_add_u32 s28, s28, 0x30000
	s_addc_u32 s29, s29, 0
	s_add_u32 s32, s32, 0x30000
	s_addc_u32 s33, s33, 0
	s_add_u32 s36, s36, 0x30000
	s_addc_u32 s37, s37, 0
	s_add_u32 m0, s22, 0xa000
	s_nop 0
	global_load_lds_dwordx4 v5, s[26:27]
	s_add_u32 m0, s22, 0xa400
	s_nop 0
	global_load_lds_dwordx4 v6, s[26:27]
	s_add_u32 m0, s23, 0xa000
	s_nop 0
	global_load_lds_dwordx4 v11, s[30:31]
	s_add_u32 m0, s23, 0xa400
	s_nop 0
	global_load_lds_dwordx4 v11, s[34:35]
	s_add_u32 m0, s23, 0xa800
	s_nop 0
	global_load_lds_dwordx4 v11, s[38:39]
	s_add_u32 s26, s26, 0x80
	s_addc_u32 s27, s27, 0
	s_add_u32 s30, s30, 0x30000
	s_addc_u32 s31, s31, 0
	s_add_u32 s34, s34, 0x30000
	s_addc_u32 s35, s35, 0
	s_add_u32 s38, s38, 0x30000
	s_addc_u32 s39, s39, 0
	s_add_u32 m0, s22, 0x14000
	s_nop 0
	global_load_lds_dwordx4 v5, s[24:25]
	s_add_u32 m0, s22, 0x14400
	s_nop 0
	global_load_lds_dwordx4 v6, s[24:25]
	s_add_u32 m0, s23, 0x14000
	s_nop 0
	global_load_lds_dwordx4 v11, s[28:29]
	s_add_u32 m0, s23, 0x14400
	s_nop 0
	global_load_lds_dwordx4 v11, s[32:33]
	s_add_u32 m0, s23, 0x14800
	s_nop 0
	global_load_lds_dwordx4 v11, s[36:37]
	s_add_u32 s24, s24, 0x80
	s_addc_u32 s25, s25, 0
	s_add_u32 s28, s28, 0x30000
	s_addc_u32 s29, s29, 0
	s_add_u32 s32, s32, 0x30000
	s_addc_u32 s33, s33, 0
	s_add_u32 s36, s36, 0x30000
	s_addc_u32 s37, s37, 0
	s_add_u32 m0, s22, 0x1e000
	s_nop 0
	global_load_lds_dwordx4 v5, s[26:27]
	s_add_u32 m0, s22, 0x1e400
	s_nop 0
	global_load_lds_dwordx4 v6, s[26:27]
	s_add_u32 m0, s23, 0x1e000
	s_nop 0
	global_load_lds_dwordx4 v11, s[30:31]
	s_add_u32 m0, s23, 0x1e400
	s_nop 0
	global_load_lds_dwordx4 v11, s[34:35]
	s_add_u32 m0, s23, 0x1e800
	s_nop 0
	global_load_lds_dwordx4 v11, s[38:39]
	s_add_u32 s26, s26, 0x80
	s_addc_u32 s27, s27, 0
	s_add_u32 s30, s30, 0x30000
	s_addc_u32 s31, s31, 0
	s_add_u32 s34, s34, 0x30000
	s_addc_u32 s35, s35, 0
	s_add_u32 s38, s38, 0x30000
	s_addc_u32 s39, s39, 0
	s_waitcnt vmcnt(20)
	v_cvt_pk_f16_f32 v12, v40, v41
	v_cvt_pk_f16_f32 v13, v42, v43
	v_cvt_pk_f16_f32 v14, v44, v45
	v_cvt_pk_f16_f32 v15, v46, v47
	v_cvt_pk_f16_f32 v56, v56, v57
	v_cvt_pk_f16_f32 v57, v58, v59
	v_cvt_pk_f16_f32 v58, v60, v61
	v_cvt_pk_f16_f32 v59, v62, v63
	v_cvt_pk_f16_f32 v60, v48, v49
	v_cvt_pk_f16_f32 v61, v50, v51
	v_cvt_pk_f16_f32 v62, v52, v53
	v_cvt_pk_f16_f32 v63, v54, v55
	v_mov_b32_e32 v64, v16
	v_mov_b32_e32 v65, v17
	v_mov_b32_e32 v66, v18
	v_mov_b32_e32 v67, v19
	v_mov_b32_e32 v68, v20
	v_mov_b32_e32 v69, v21
	v_mov_b32_e32 v70, v22
	v_mov_b32_e32 v71, v23
	v_mov_b32_e32 v72, v24
	v_mov_b32_e32 v73, v25
	v_mov_b32_e32 v74, v26
	v_mov_b32_e32 v75, v27
	v_mov_b32_e32 v76, v28
	v_mov_b32_e32 v77, v29
	v_mov_b32_e32 v78, v30
	v_mov_b32_e32 v79, v31
	v_mov_b32_e32 v80, v32
	v_mov_b32_e32 v81, v33
	v_mov_b32_e32 v82, v34
	v_mov_b32_e32 v83, v35
	v_mov_b32_e32 v84, v36
	v_mov_b32_e32 v85, v37
	v_mov_b32_e32 v86, v38
	v_mov_b32_e32 v87, v39
	v_mov_b32_e32 v88, v16
	v_mov_b32_e32 v89, v17
	v_mov_b32_e32 v90, v18
	v_mov_b32_e32 v91, v19
	v_mov_b32_e32 v92, v20
	v_mov_b32_e32 v93, v21
	v_mov_b32_e32 v94, v22
	v_mov_b32_e32 v95, v23
	v_mov_b32_e32 v96, v24
	v_mov_b32_e32 v97, v25
	v_mov_b32_e32 v98, v26
	v_mov_b32_e32 v99, v27
	v_mov_b32_e32 v100, v28
	v_mov_b32_e32 v101, v29
	v_mov_b32_e32 v102, v30
	v_mov_b32_e32 v103, v31
	v_mov_b32_e32 v104, v32
	v_mov_b32_e32 v105, v33
	v_mov_b32_e32 v106, v34
	v_mov_b32_e32 v107, v35
	v_mov_b32_e32 v108, v36
	v_mov_b32_e32 v109, v37
	v_mov_b32_e32 v110, v38
	v_mov_b32_e32 v111, v39
	v_mov_b32_e32 v112, v16
	v_mov_b32_e32 v113, v17
	v_mov_b32_e32 v114, v18
	v_mov_b32_e32 v115, v19
	v_mov_b32_e32 v116, v20
	v_mov_b32_e32 v117, v21
	v_mov_b32_e32 v118, v22
	v_mov_b32_e32 v119, v23
	v_mov_b32_e32 v120, v24
	v_mov_b32_e32 v121, v25
	v_mov_b32_e32 v122, v26
	v_mov_b32_e32 v123, v27
	v_mov_b32_e32 v124, v28
	v_mov_b32_e32 v125, v29
	v_mov_b32_e32 v126, v30
	v_mov_b32_e32 v127, v31
	v_mov_b32_e32 v128, v32
	v_mov_b32_e32 v129, v33
	v_mov_b32_e32 v130, v34
	v_mov_b32_e32 v131, v35
	v_mov_b32_e32 v132, v36
	v_mov_b32_e32 v133, v37
	v_mov_b32_e32 v134, v38
	v_mov_b32_e32 v135, v39
	v_mov_b32_e32 v136, v16
	v_mov_b32_e32 v137, v17
	v_mov_b32_e32 v138, v18
	v_mov_b32_e32 v139, v19
	v_mov_b32_e32 v140, v20
	v_mov_b32_e32 v141, v21
	v_mov_b32_e32 v142, v22
	v_mov_b32_e32 v143, v23
	v_mov_b32_e32 v144, v24
	v_mov_b32_e32 v145, v25
	v_mov_b32_e32 v146, v26
	v_mov_b32_e32 v147, v27
	v_mov_b32_e32 v148, v28
	v_mov_b32_e32 v149, v29
	v_mov_b32_e32 v150, v30
	v_mov_b32_e32 v151, v31
	v_mov_b32_e32 v152, v32
	v_mov_b32_e32 v153, v33
	v_mov_b32_e32 v154, v34
	v_mov_b32_e32 v155, v35
	v_mov_b32_e32 v156, v36
	v_mov_b32_e32 v157, v37
	v_mov_b32_e32 v158, v38
	v_mov_b32_e32 v159, v39
	v_mov_b32_e32 v160, v16
	v_mov_b32_e32 v161, v17
	v_mov_b32_e32 v162, v18
	v_mov_b32_e32 v163, v19
	v_mov_b32_e32 v164, v20
	v_mov_b32_e32 v165, v21
	v_mov_b32_e32 v166, v22
	v_mov_b32_e32 v167, v23
	v_mov_b32_e32 v168, v24
	v_mov_b32_e32 v169, v25
	v_mov_b32_e32 v170, v26
	v_mov_b32_e32 v171, v27
	v_mov_b32_e32 v172, v28
	v_mov_b32_e32 v173, v29
	v_mov_b32_e32 v174, v30
	v_mov_b32_e32 v175, v31
	v_mov_b32_e32 v176, v32
	v_mov_b32_e32 v177, v33
	v_mov_b32_e32 v178, v34
	v_mov_b32_e32 v179, v35
	v_mov_b32_e32 v180, v36
	v_mov_b32_e32 v181, v37
	v_mov_b32_e32 v182, v38
	v_mov_b32_e32 v183, v39
	v_mov_b32_e32 v184, v16
	v_mov_b32_e32 v185, v17
	v_mov_b32_e32 v186, v18
	v_mov_b32_e32 v187, v19
	v_mov_b32_e32 v188, v20
	v_mov_b32_e32 v189, v21
	v_mov_b32_e32 v190, v22
	v_mov_b32_e32 v191, v23
	v_mov_b32_e32 v192, v24
	v_mov_b32_e32 v193, v25
	v_mov_b32_e32 v194, v26
	v_mov_b32_e32 v195, v27
	v_mov_b32_e32 v196, v28
	v_mov_b32_e32 v197, v29
	v_mov_b32_e32 v198, v30
	v_mov_b32_e32 v199, v31
	v_mov_b32_e32 v200, v32
	v_mov_b32_e32 v201, v33
	v_mov_b32_e32 v202, v34
	v_mov_b32_e32 v203, v35
	v_mov_b32_e32 v204, v36
	v_mov_b32_e32 v205, v37
	v_mov_b32_e32 v206, v38
	v_mov_b32_e32 v207, v39
	v_mov_b32_e32 v208, v16
	v_mov_b32_e32 v209, v17
	v_mov_b32_e32 v210, v18
	v_mov_b32_e32 v211, v19
	v_mov_b32_e32 v212, v20
	v_mov_b32_e32 v213, v21
	v_mov_b32_e32 v214, v22
	v_mov_b32_e32 v215, v23
	v_mov_b32_e32 v216, v24
	v_mov_b32_e32 v217, v25
	v_mov_b32_e32 v218, v26
	v_mov_b32_e32 v219, v27
	v_mov_b32_e32 v220, v28
	v_mov_b32_e32 v221, v29
	v_mov_b32_e32 v222, v30
	v_mov_b32_e32 v223, v31
	v_mov_b32_e32 v224, v32
	v_mov_b32_e32 v225, v33
	v_mov_b32_e32 v226, v34
	v_mov_b32_e32 v227, v35
	v_mov_b32_e32 v228, v36
	v_mov_b32_e32 v229, v37
	v_mov_b32_e32 v230, v38
	v_mov_b32_e32 v231, v39
	v_mov_b32_e32 v232, v16
	v_mov_b32_e32 v233, v17
	v_mov_b32_e32 v234, v18
	v_mov_b32_e32 v235, v19
	v_mov_b32_e32 v236, v20
	v_mov_b32_e32 v237, v21
	v_mov_b32_e32 v238, v22
	v_mov_b32_e32 v239, v23
	v_mov_b32_e32 v240, v24
	v_mov_b32_e32 v241, v25
	v_mov_b32_e32 v242, v26
	v_mov_b32_e32 v243, v27
	v_mov_b32_e32 v244, v28
	v_mov_b32_e32 v245, v29
	v_mov_b32_e32 v246, v30
	v_mov_b32_e32 v247, v31
	v_mov_b32_e32 v248, v32
	v_mov_b32_e32 v249, v33
	v_mov_b32_e32 v250, v34
	v_mov_b32_e32 v251, v35
	v_mov_b32_e32 v252, v36
	v_mov_b32_e32 v253, v37
	v_mov_b32_e32 v254, v38
	v_mov_b32_e32 v255, v39
	s_waitcnt vmcnt(15)
	s_barrier
.Lfc_h0_loop:
	ds_read_b128 v[16:19], v3 offset:0
	ds_read_b128 v[20:23], v3 offset:1024
	ds_read_b128 v[24:27], v3 offset:2048
	ds_read_b128 v[28:31], v3 offset:3072
	ds_read_b128 v[32:35], v3 offset:4096
	ds_read_b128 v[36:39], v3 offset:5120
	ds_read_b128 v[40:43], v1 offset:0
	ds_read_b128 v[44:47], v1 offset:1024
	ds_read_b128 v[48:51], v1 offset:2048
	ds_read_b128 v[52:55], v1 offset:3072
	s_cmp_eq_u32 s21, 0
	s_cbranch_scc1 .Lfc_ng_1
	s_add_u32 m0, s22, 0x14000
	s_nop 0
	global_load_lds_dwordx4 v5, s[24:25]
	s_add_u32 m0, s22, 0x14400
	s_nop 0
	global_load_lds_dwordx4 v6, s[24:25]
	s_add_u32 m0, s23, 0x14000
	s_nop 0
	global_load_lds_dwordx4 v11, s[28:29]
	s_add_u32 m0, s23, 0x14400
	s_nop 0
	global_load_lds_dwordx4 v11, s[32:33]
	s_add_u32 m0, s23, 0x14800
	s_nop 0
	global_load_lds_dwordx4 v11, s[36:37]
	s_add_u32 s24, s24, 0x80
	s_addc_u32 s25, s25, 0
	s_add_u32 s28, s28, 0x30000
	s_addc_u32 s29, s29, 0
	s_add_u32 s32, s32, 0x30000
	s_addc_u32 s33, s33, 0
	s_add_u32 s36, s36, 0x30000
	s_addc_u32 s37, s37, 0
.Lfc_ng_1:
	s_barrier
	s_waitcnt lgkmcnt(0)
	v_mfma_f32_16x16x32_f16 v[64:67], v[16:19], v[40:43], v[64:67]
	v_mfma_f32_16x16x32_f16 v[68:71], v[20:23], v[40:43], v[68:71]
	v_mfma_f32_16x16x32_f16 v[72:75], v[24:27], v[40:43], v[72:75]
	v_mfma_f32_16x16x32_f16 v[76:79], v[28:31], v[40:43], v[76:79]
	v_mfma_f32_16x16x32_f16 v[80:83], v[32:35], v[40:43], v[80:83]
	v_mfma_f32_16x16x32_f16 v[84:87], v[36:39], v[40:43], v[84:87]
	v_mfma_f32_16x16x32_f16 v[88:91], v[16:19], v[44:47], v[88:91]
	ds_read_b128 v[40:43], v1 offset:4096
	v_mfma_f32_16x16x32_f16 v[92:95], v[20:23], v[44:47], v[92:95]
	v_mfma_f32_16x16x32_f16 v[96:99], v[24:27], v[44:47], v[96:99]
	v_mfma_f32_16x16x32_f16 v[100:103], v[28:31], v[44:47], v[100:103]
	v_mfma_f32_16x16x32_f16 v[104:107], v[32:35], v[44:47], v[104:107]
	v_mfma_f32_16x16x32_f16 v[108:111], v[36:39], v[44:47], v[108:111]
	v_mfma_f32_16x16x32_f16 v[112:115], v[16:19], v[48:51], v[112:115]
	ds_read_b128 v[44:47], v1 offset:5120
	v_mfma_f32_16x16x32_f16 v[116:119], v[20:23], v[48:51], v[116:119]
	v_mfma_f32_16x16x32_f16 v[120:123], v[24:27], v[48:51], v[120:123]
	v_mfma_f32_16x16x32_f16 v[124:127], v[28:31], v[48:51], v[124:127]
	v_mfma_f32_16x16x32_f16 v[128:131], v[32:35], v[48:51], v[128:131]
	v_mfma_f32_16x16x32_f16 v[132:135], v[36:39], v[48:51], v[132:135]
	v_mfma_f32_16x16x32_f16 v[136:139], v[16:19], v[52:55], v[136:139]
	ds_read_b128 v[48:51], v1 offset:6144
	v_mfma_f32_16x16x32_f16 v[140:143], v[20:23], v[52:55], v[140:143]
	v_mfma_f32_16x16x32_f16 v[144:147], v[24:27], v[52:55], v[144:147]
	v_mfma_f32_16x16x32_f16 v[148:151], v[28:31], v[52:55], v[148:151]
	v_mfma_f32_16x16x32_f16 v[152:155], v[32:35], v[52:55], v[152:155]
	v_mfma_f32_16x16x32_f16 v[156:159], v[36:39], v[52:55], v[156:159]
	s_waitcnt lgkmcnt(2)
	v_mfma_f32_16x16x32_f16 v[160:163], v[16:19], v[40:43], v[160:163]
	ds_read_b128 v[52:55], v1 offset:7168
	v_mfma_f32_16x16x32_f16 v[164:167], v[20:23], v[40:43], v[164:167]
	v_mfma_f32_16x16x32_f16 v[168:171], v[24:27], v[40:43], v[168:171]
	v_mfma_f32_16x16x32_f16 v[172:175], v[28:31], v[40:43], v[172:175]
	v_mfma_f32_16x16x32_f16 v[176:179], v[32:35], v[40:43], v[176:179]
	v_mfma_f32_16x16x32_f16 v[180:183], v[36:39], v[40:43], v[180:183]
	s_waitcnt lgkmcnt(2)
	v_mfma_f32_16x16x32_f16 v[184:187], v[16:19], v[44:47], v[184:187]
	v_mfma_f32_16x16x32_f16 v[188:191], v[20:23], v[44:47], v[188:191]
	v_mfma_f32_16x16x32_f16 v[192:195], v[24:27], v[44:47], v[192:195]
	v_mfma_f32_16x16x32_f16 v[196:199], v[28:31], v[44:47], v[196:199]
	v_mfma_f32_16x16x32_f16 v[200:203], v[32:35], v[44:47], v[200:203]
	v_mfma_f32_16x16x32_f16 v[204:207], v[36:39], v[44:47], v[204:207]
	s_waitcnt lgkmcnt(1)
	v_mfma_f32_16x16x32_f16 v[208:211], v[16:19], v[48:51], v[208:211]
	v_mfma_f32_16x16x32_f16 v[212:215], v[20:23], v[48:51], v[212:215]
	v_mfma_f32_16x16x32_f16 v[216:219], v[24:27], v[48:51], v[216:219]
	v_mfma_f32_16x16x32_f16 v[220:223], v[28:31], v[48:51], v[220:223]
	v_mfma_f32_16x16x32_f16 v[224:227], v[32:35], v[48:51], v[224:227]
	v_mfma_f32_16x16x32_f16 v[228:231], v[36:39], v[48:51], v[228:231]
	s_waitcnt lgkmcnt(0)
	v_mfma_f32_16x16x32_f16 v[232:235], v[16:19], v[52:55], v[232:235]
	v_mfma_f32_16x16x32_f16 v[236:239], v[20:23], v[52:55], v[236:239]
	v_mfma_f32_16x16x32_f16 v[240:243], v[24:27], v[52:55], v[240:243]
	v_mfma_f32_16x16x32_f16 v[244:247], v[28:31], v[52:55], v[244:247]
	v_mfma_f32_16x16x32_f16 v[248:251], v[32:35], v[52:55], v[248:251]
	v_mfma_f32_16x16x32_f16 v[252:255], v[36:39], v[52:55], v[252:255]
	s_cmp_eq_u32 s21, 11
	s_cbranch_scc1 .Lfc_w0_2
	s_waitcnt vmcnt(5)
	s_branch .Lfc_w1_2
.Lfc_w0_2:
	s_waitcnt vmcnt(0)
.Lfc_w1_2:
	s_barrier
	ds_read_b128 v[16:19], v3 offset:40960
	ds_read_b128 v[20:23], v3 offset:41984
	ds_read_b128 v[24:27], v3 offset:43008
	ds_read_b128 v[28:31], v3 offset:44032
	ds_read_b128 v[32:35], v3 offset:45056
	ds_read_b128 v[36:39], v3 offset:46080
	ds_read_b128 v[40:43], v1 offset:40960
	ds_read_b128 v[44:47], v1 offset:41984
	ds_read_b128 v[48:51], v1 offset:43008
	ds_read_b128 v[52:55], v1 offset:44032
	s_cmp_eq_u32 s21, 0
	s_cbranch_scc1 .Lfc_ng_3
	s_add_u32 m0, s22, 0x1e000
	s_nop 0
	global_load_lds_dwordx4 v5, s[26:27]
	s_add_u32 m0, s22, 0x1e400
	s_nop 0
	global_load_lds_dwordx4 v6, s[26:27]
	s_add_u32 m0, s23, 0x1e000
	s_nop 0
	global_load_lds_dwordx4 v11, s[30:31]
	s_add_u32 m0, s23, 0x1e400
	s_nop 0
	global_load_lds_dwordx4 v11, s[34:35]
	s_add_u32 m0, s23, 0x1e800
	s_nop 0
	global_load_lds_dwordx4 v11, s[38:39]
	s_add_u32 s26, s26, 0x80
	s_addc_u32 s27, s27, 0
	s_add_u32 s30, s30, 0x30000
	s_addc_u32 s31, s31, 0
	s_add_u32 s34, s34, 0x30000
	s_addc_u32 s35, s35, 0
	s_add_u32 s38, s38, 0x30000
	s_addc_u32 s39, s39, 0
	s_cmp_eq_u32 s21, 3
	s_cbranch_scc1 .Lfc_sw_4
	s_cmp_eq_u32 s21, 7
	s_cbranch_scc0 .Lfc_swd_4
.Lfc_sw_4:
	s_mov_b64 s[24:25], s[96:97]
	s_add_u32 s26, s96, 64
	s_addc_u32 s27, s97, 0
	s_mov_b64 s[96:97], s[4:5]
	v_mov_b32_e32 v5, v7
	v_mov_b32_e32 v6, v8
	v_mov_b32_e32 v7, v9
	v_mov_b32_e32 v8, v10
.Lfc_swd_4:
.Lfc_ng_3:
	s_barrier
	s_waitcnt lgkmcnt(0)
	v_mfma_f32_16x16x32_f16 v[64:67], v[16:19], v[40:43], v[64:67]
	v_mfma_f32_16x16x32_f16 v[68:71], v[20:23], v[40:43], v[68:71]
	v_mfma_f32_16x16x32_f16 v[72:75], v[24:27], v[40:43], v[72:75]
	v_mfma_f32_16x16x32_f16 v[76:79], v[28:31], v[40:43], v[76:79]
	v_mfma_f32_16x16x32_f16 v[80:83], v[32:35], v[40:43], v[80:83]
	v_mfma_f32_16x16x32_f16 v[84:87], v[36:39], v[40:43], v[84:87]
	v_mfma_f32_16x16x32_f16 v[88:91], v[16:19], v[44:47], v[88:91]
	ds_read_b128 v[40:43], v1 offset:45056
	v_mfma_f32_16x16x32_f16 v[92:95], v[20:23], v[44:47], v[92:95]
	v_mfma_f32_16x16x32_f16 v[96:99], v[24:27], v[44:47], v[96:99]
	v_mfma_f32_16x16x32_f16 v[100:103], v[28:31], v[44:47], v[100:103]
	v_mfma_f32_16x16x32_f16 v[104:107], v[32:35], v[44:47], v[104:107]
	v_mfma_f32_16x16x32_f16 v[108:111], v[36:39], v[44:47], v[108:111]
	v_mfma_f32_16x16x32_f16 v[112:115], v[16:19], v[48:51], v[112:115]
	ds_read_b128 v[44:47], v1 offset:46080
	v_mfma_f32_16x16x32_f16 v[116:119], v[20:23], v[48:51], v[116:119]
	v_mfma_f32_16x16x32_f16 v[120:123], v[24:27], v[48:51], v[120:123]
	v_mfma_f32_16x16x32_f16 v[124:127], v[28:31], v[48:51], v[124:127]
	v_mfma_f32_16x16x32_f16 v[128:131], v[32:35], v[48:51], v[128:131]
	v_mfma_f32_16x16x32_f16 v[132:135], v[36:39], v[48:51], v[132:135]
	v_mfma_f32_16x16x32_f16 v[136:139], v[16:19], v[52:55], v[136:139]
	ds_read_b128 v[48:51], v1 offset:47104
	v_mfma_f32_16x16x32_f16 v[140:143], v[20:23], v[52:55], v[140:143]
	v_mfma_f32_16x16x32_f16 v[144:147], v[24:27], v[52:55], v[144:147]
	v_mfma_f32_16x16x32_f16 v[148:151], v[28:31], v[52:55], v[148:151]
	v_mfma_f32_16x16x32_f16 v[152:155], v[32:35], v[52:55], v[152:155]
	v_mfma_f32_16x16x32_f16 v[156:159], v[36:39], v[52:55], v[156:159]
	s_waitcnt lgkmcnt(2)
	v_mfma_f32_16x16x32_f16 v[160:163], v[16:19], v[40:43], v[160:163]
	ds_read_b128 v[52:55], v1 offset:48128
	v_mfma_f32_16x16x32_f16 v[164:167], v[20:23], v[40:43], v[164:167]
	v_mfma_f32_16x16x32_f16 v[168:171], v[24:27], v[40:43], v[168:171]
	v_mfma_f32_16x16x32_f16 v[172:175], v[28:31], v[40:43], v[172:175]
	v_mfma_f32_16x16x32_f16 v[176:179], v[32:35], v[40:43], v[176:179]
	v_mfma_f32_16x16x32_f16 v[180:183], v[36:39], v[40:43], v[180:183]
	s_waitcnt lgkmcnt(2)
	v_mfma_f32_16x16x32_f16 v[184:187], v[16:19], v[44:47], v[184:187]
	v_mfma_f32_16x16x32_f16 v[188:191], v[20:23], v[44:47], v[188:191]
	v_mfma_f32_16x16x32_f16 v[192:195], v[24:27], v[44:47], v[192:195]
	v_mfma_f32_16x16x32_f16 v[196:199], v[28:31], v[44:47], v[196:199]
	v_mfma_f32_16x16x32_f16 v[200:203], v[32:35], v[44:47], v[200:203]
	v_mfma_f32_16x16x32_f16 v[204:207], v[36:39], v[44:47], v[204:207]
	s_waitcnt lgkmcnt(1)
	v_mfma_f32_16x16x32_f16 v[208:211], v[16:19], v[48:51], v[208:211]
	v_mfma_f32_16x16x32_f16 v[212:215], v[20:23], v[48:51], v[212:215]
	v_mfma_f32_16x16x32_f16 v[216:219], v[24:27], v[48:51], v[216:219]
	v_mfma_f32_16x16x32_f16 v[220:223], v[28:31], v[48:51], v[220:223]
	v_mfma_f32_16x16x32_f16 v[224:227], v[32:35], v[48:51], v[224:227]
	v_mfma_f32_16x16x32_f16 v[228:231], v[36:39], v[48:51], v[228:231]
	s_waitcnt lgkmcnt(0)
	v_mfma_f32_16x16x32_f16 v[232:235], v[16:19], v[52:55], v[232:235]
	v_mfma_f32_16x16x32_f16 v[236:239], v[20:23], v[52:55], v[236:239]
	v_mfma_f32_16x16x32_f16 v[240:243], v[24:27], v[52:55], v[240:243]
	v_mfma_f32_16x16x32_f16 v[244:247], v[28:31], v[52:55], v[244:247]
	v_mfma_f32_16x16x32_f16 v[248:251], v[32:35], v[52:55], v[248:251]
	v_mfma_f32_16x16x32_f16 v[252:255], v[36:39], v[52:55], v[252:255]
	s_cmp_eq_u32 s21, 11
	s_cbranch_scc1 .Lfc_w0_5
	s_waitcnt vmcnt(5)
	s_branch .Lfc_w1_5

.Lfc_w1_5:
	s_barrier
	ds_read_b128 v[16:19], v4 offset:0
	ds_read_b128 v[20:23], v4 offset:1024
	ds_read_b128 v[24:27], v4 offset:2048
	ds_read_b128 v[28:31], v4 offset:3072
	ds_read_b128 v[32:35], v4 offset:4096
	ds_read_b128 v[36:39], v4 offset:5120
	ds_read_b128 v[40:43], v2 offset:0
	ds_read_b128 v[44:47], v2 offset:1024
	ds_read_b128 v[48:51], v2 offset:2048
	ds_read_b128 v[52:55], v2 offset:3072
	s_cmp_eq_u32 s21, 11
	s_cbranch_scc1 .Lfc_ng_6
	s_add_u32 m0, s22, 0x0
	s_nop 0
	global_load_lds_dwordx4 v5, s[24:25]
	s_add_u32 m0, s22, 0x400
	s_nop 0
	global_load_lds_dwordx4 v6, s[24:25]
	s_add_u32 m0, s23, 0x0
	s_nop 0
	global_load_lds_dwordx4 v11, s[28:29]
	s_add_u32 m0, s23, 0x400
	s_nop 0
	global_load_lds_dwordx4 v11, s[32:33]
	s_add_u32 m0, s23, 0x800
	s_nop 0
	global_load_lds_dwordx4 v11, s[36:37]
	s_add_u32 s24, s24, 0x80
	s_addc_u32 s25, s25, 0
	s_add_u32 s28, s28, 0x30000
	s_addc_u32 s29, s29, 0
	s_add_u32 s32, s32, 0x30000
	s_addc_u32 s33, s33, 0
	s_add_u32 s36, s36, 0x30000
	s_addc_u32 s37, s37, 0
.Lfc_ng_6:
	s_barrier
	s_waitcnt lgkmcnt(0)
	v_mfma_f32_16x16x32_f16 v[64:67], v[16:19], v[40:43], v[64:67]
	v_mfma_f32_16x16x32_f16 v[68:71], v[20:23], v[40:43], v[68:71]
	v_mfma_f32_16x16x32_f16 v[72:75], v[24:27], v[40:43], v[72:75]
	v_mfma_f32_16x16x32_f16 v[76:79], v[28:31], v[40:43], v[76:79]
	v_mfma_f32_16x16x32_f16 v[80:83], v[32:35], v[40:43], v[80:83]
	v_mfma_f32_16x16x32_f16 v[84:87], v[36:39], v[40:43], v[84:87]
	v_mfma_f32_16x16x32_f16 v[88:91], v[16:19], v[44:47], v[88:91]
	ds_read_b128 v[40:43], v2 offset:4096
	v_mfma_f32_16x16x32_f16 v[92:95], v[20:23], v[44:47], v[92:95]
	v_mfma_f32_16x16x32_f16 v[96:99], v[24:27], v[44:47], v[96:99]
	v_mfma_f32_16x16x32_f16 v[100:103], v[28:31], v[44:47], v[100:103]
	v_mfma_f32_16x16x32_f16 v[104:107], v[32:35], v[44:47], v[104:107]
	v_mfma_f32_16x16x32_f16 v[108:111], v[36:39], v[44:47], v[108:111]
	v_mfma_f32_16x16x32_f16 v[112:115], v[16:19], v[48:51], v[112:115]
	ds_read_b128 v[44:47], v2 offset:5120
	v_mfma_f32_16x16x32_f16 v[116:119], v[20:23], v[48:51], v[116:119]
	v_mfma_f32_16x16x32_f16 v[120:123], v[24:27], v[48:51], v[120:123]
	v_mfma_f32_16x16x32_f16 v[124:127], v[28:31], v[48:51], v[124:127]
	v_mfma_f32_16x16x32_f16 v[128:131], v[32:35], v[48:51], v[128:131]
	v_mfma_f32_16x16x32_f16 v[132:135], v[36:39], v[48:51], v[132:135]
	v_mfma_f32_16x16x32_f16 v[136:139], v[16:19], v[52:55], v[136:139]
	ds_read_b128 v[48:51], v2 offset:6144
	v_mfma_f32_16x16x32_f16 v[140:143], v[20:23], v[52:55], v[140:143]
	v_mfma_f32_16x16x32_f16 v[144:147], v[24:27], v[52:55], v[144:147]
	v_mfma_f32_16x16x32_f16 v[148:151], v[28:31], v[52:55], v[148:151]
	v_mfma_f32_16x16x32_f16 v[152:155], v[32:35], v[52:55], v[152:155]
	v_mfma_f32_16x16x32_f16 v[156:159], v[36:39], v[52:55], v[156:159]
	s_waitcnt lgkmcnt(2)
	v_mfma_f32_16x16x32_f16 v[160:163], v[16:19], v[40:43], v[160:163]
	ds_read_b128 v[52:55], v2 offset:7168
	v_mfma_f32_16x16x32_f16 v[164:167], v[20:23], v[40:43], v[164:167]
	v_mfma_f32_16x16x32_f16 v[168:171], v[24:27], v[40:43], v[168:171]
	v_mfma_f32_16x16x32_f16 v[172:175], v[28:31], v[40:43], v[172:175]
	v_mfma_f32_16x16x32_f16 v[176:179], v[32:35], v[40:43], v[176:179]
	v_mfma_f32_16x16x32_f16 v[180:183], v[36:39], v[40:43], v[180:183]
	s_waitcnt lgkmcnt(2)
	v_mfma_f32_16x16x32_f16 v[184:187], v[16:19], v[44:47], v[184:187]
	v_mfma_f32_16x16x32_f16 v[188:191], v[20:23], v[44:47], v[188:191]
	v_mfma_f32_16x16x32_f16 v[192:195], v[24:27], v[44:47], v[192:195]
	v_mfma_f32_16x16x32_f16 v[196:199], v[28:31], v[44:47], v[196:199]
	v_mfma_f32_16x16x32_f16 v[200:203], v[32:35], v[44:47], v[200:203]
	v_mfma_f32_16x16x32_f16 v[204:207], v[36:39], v[44:47], v[204:207]
	s_waitcnt lgkmcnt(1)
	v_mfma_f32_16x16x32_f16 v[208:211], v[16:19], v[48:51], v[208:211]
	v_mfma_f32_16x16x32_f16 v[212:215], v[20:23], v[48:51], v[212:215]
	v_mfma_f32_16x16x32_f16 v[216:219], v[24:27], v[48:51], v[216:219]
	v_mfma_f32_16x16x32_f16 v[220:223], v[28:31], v[48:51], v[220:223]
	v_mfma_f32_16x16x32_f16 v[224:227], v[32:35], v[48:51], v[224:227]
	v_mfma_f32_16x16x32_f16 v[228:231], v[36:39], v[48:51], v[228:231]
	s_waitcnt lgkmcnt(0)
	v_mfma_f32_16x16x32_f16 v[232:235], v[16:19], v[52:55], v[232:235]
	v_mfma_f32_16x16x32_f16 v[236:239], v[20:23], v[52:55], v[236:239]
	v_mfma_f32_16x16x32_f16 v[240:243], v[24:27], v[52:55], v[240:243]
	v_mfma_f32_16x16x32_f16 v[244:247], v[28:31], v[52:55], v[244:247]
	v_mfma_f32_16x16x32_f16 v[248:251], v[32:35], v[52:55], v[248:251]
	v_mfma_f32_16x16x32_f16 v[252:255], v[36:39], v[52:55], v[252:255]
	s_cmp_eq_u32 s21, 11
	s_cbranch_scc1 .Lfc_w0_7
	s_waitcnt vmcnt(5)
	s_branch .Lfc_w1_7

.Lfc_w1_7:
	s_barrier
	ds_read_b128 v[16:19], v4 offset:40960
	ds_read_b128 v[20:23], v4 offset:41984
	ds_read_b128 v[24:27], v4 offset:43008
	ds_read_b128 v[28:31], v4 offset:44032
	ds_read_b128 v[32:35], v4 offset:45056
	ds_read_b128 v[36:39], v4 offset:46080
	ds_read_b128 v[40:43], v2 offset:40960
	ds_read_b128 v[44:47], v2 offset:41984
	ds_read_b128 v[48:51], v2 offset:43008
	ds_read_b128 v[52:55], v2 offset:44032
	s_cmp_eq_u32 s21, 11
	s_cbranch_scc1 .Lfc_ng_8
	s_add_u32 m0, s22, 0xa000
	s_nop 0
	global_load_lds_dwordx4 v5, s[26:27]
	s_add_u32 m0, s22, 0xa400
	s_nop 0
	global_load_lds_dwordx4 v6, s[26:27]
	s_add_u32 m0, s23, 0xa000
	s_nop 0
	global_load_lds_dwordx4 v11, s[30:31]
	s_add_u32 m0, s23, 0xa400
	s_nop 0
	global_load_lds_dwordx4 v11, s[34:35]
	s_add_u32 m0, s23, 0xa800
	s_nop 0
	global_load_lds_dwordx4 v11, s[38:39]
	s_add_u32 s26, s26, 0x80
	s_addc_u32 s27, s27, 0
	s_add_u32 s30, s30, 0x30000
	s_addc_u32 s31, s31, 0
	s_add_u32 s34, s34, 0x30000
	s_addc_u32 s35, s35, 0
	s_add_u32 s38, s38, 0x30000
	s_addc_u32 s39, s39, 0
.Lfc_ng_8:
	s_barrier
	s_waitcnt lgkmcnt(0)
	v_mfma_f32_16x16x32_f16 v[64:67], v[16:19], v[40:43], v[64:67]
	v_mfma_f32_16x16x32_f16 v[68:71], v[20:23], v[40:43], v[68:71]
	v_mfma_f32_16x16x32_f16 v[72:75], v[24:27], v[40:43], v[72:75]
	v_mfma_f32_16x16x32_f16 v[76:79], v[28:31], v[40:43], v[76:79]
	v_mfma_f32_16x16x32_f16 v[80:83], v[32:35], v[40:43], v[80:83]
	v_mfma_f32_16x16x32_f16 v[84:87], v[36:39], v[40:43], v[84:87]
	v_mfma_f32_16x16x32_f16 v[88:91], v[16:19], v[44:47], v[88:91]
	ds_read_b128 v[40:43], v2 offset:45056
	v_mfma_f32_16x16x32_f16 v[92:95], v[20:23], v[44:47], v[92:95]
	v_mfma_f32_16x16x32_f16 v[96:99], v[24:27], v[44:47], v[96:99]
	v_mfma_f32_16x16x32_f16 v[100:103], v[28:31], v[44:47], v[100:103]
	v_mfma_f32_16x16x32_f16 v[104:107], v[32:35], v[44:47], v[104:107]
	v_mfma_f32_16x16x32_f16 v[108:111], v[36:39], v[44:47], v[108:111]
	v_mfma_f32_16x16x32_f16 v[112:115], v[16:19], v[48:51], v[112:115]
	ds_read_b128 v[44:47], v2 offset:46080
	v_mfma_f32_16x16x32_f16 v[116:119], v[20:23], v[48:51], v[116:119]
	v_mfma_f32_16x16x32_f16 v[120:123], v[24:27], v[48:51], v[120:123]
	v_mfma_f32_16x16x32_f16 v[124:127], v[28:31], v[48:51], v[124:127]
	v_mfma_f32_16x16x32_f16 v[128:131], v[32:35], v[48:51], v[128:131]
	v_mfma_f32_16x16x32_f16 v[132:135], v[36:39], v[48:51], v[132:135]
	v_mfma_f32_16x16x32_f16 v[136:139], v[16:19], v[52:55], v[136:139]
	ds_read_b128 v[48:51], v2 offset:47104
	v_mfma_f32_16x16x32_f16 v[140:143], v[20:23], v[52:55], v[140:143]
	v_mfma_f32_16x16x32_f16 v[144:147], v[24:27], v[52:55], v[144:147]
	v_mfma_f32_16x16x32_f16 v[148:151], v[28:31], v[52:55], v[148:151]
	v_mfma_f32_16x16x32_f16 v[152:155], v[32:35], v[52:55], v[152:155]
	v_mfma_f32_16x16x32_f16 v[156:159], v[36:39], v[52:55], v[156:159]
	s_waitcnt lgkmcnt(2)
	v_mfma_f32_16x16x32_f16 v[160:163], v[16:19], v[40:43], v[160:163]
	ds_read_b128 v[52:55], v2 offset:48128
	v_mfma_f32_16x16x32_f16 v[164:167], v[20:23], v[40:43], v[164:167]
	v_mfma_f32_16x16x32_f16 v[168:171], v[24:27], v[40:43], v[168:171]
	v_mfma_f32_16x16x32_f16 v[172:175], v[28:31], v[40:43], v[172:175]
	v_mfma_f32_16x16x32_f16 v[176:179], v[32:35], v[40:43], v[176:179]
	v_mfma_f32_16x16x32_f16 v[180:183], v[36:39], v[40:43], v[180:183]
	s_waitcnt lgkmcnt(2)
	v_mfma_f32_16x16x32_f16 v[184:187], v[16:19], v[44:47], v[184:187]
	v_mfma_f32_16x16x32_f16 v[188:191], v[20:23], v[44:47], v[188:191]
	v_mfma_f32_16x16x32_f16 v[192:195], v[24:27], v[44:47], v[192:195]
	v_mfma_f32_16x16x32_f16 v[196:199], v[28:31], v[44:47], v[196:199]
	v_mfma_f32_16x16x32_f16 v[200:203], v[32:35], v[44:47], v[200:203]
	v_mfma_f32_16x16x32_f16 v[204:207], v[36:39], v[44:47], v[204:207]
	s_waitcnt lgkmcnt(1)
	v_mfma_f32_16x16x32_f16 v[208:211], v[16:19], v[48:51], v[208:211]
	v_mfma_f32_16x16x32_f16 v[212:215], v[20:23], v[48:51], v[212:215]
	v_mfma_f32_16x16x32_f16 v[216:219], v[24:27], v[48:51], v[216:219]
	v_mfma_f32_16x16x32_f16 v[220:223], v[28:31], v[48:51], v[220:223]
	v_mfma_f32_16x16x32_f16 v[224:227], v[32:35], v[48:51], v[224:227]
	v_mfma_f32_16x16x32_f16 v[228:231], v[36:39], v[48:51], v[228:231]
	s_waitcnt lgkmcnt(0)
	v_mfma_f32_16x16x32_f16 v[232:235], v[16:19], v[52:55], v[232:235]
	v_mfma_f32_16x16x32_f16 v[236:239], v[20:23], v[52:55], v[236:239]
	v_mfma_f32_16x16x32_f16 v[240:243], v[24:27], v[52:55], v[240:243]
	v_mfma_f32_16x16x32_f16 v[244:247], v[28:31], v[52:55], v[244:247]
	v_mfma_f32_16x16x32_f16 v[248:251], v[32:35], v[52:55], v[248:251]
	v_mfma_f32_16x16x32_f16 v[252:255], v[36:39], v[52:55], v[252:255]
	s_cmp_eq_u32 s21, 11
	s_cbranch_scc1 .Lfc_w0_9
	s_waitcnt vmcnt(5)
	s_branch .Lfc_w1_9

.Lfc_w1_9:
	s_barrier
	s_add_u32 s21, s21, 1
	s_cmp_lt_u32 s21, 12
	s_cbranch_scc1 .Lfc_h0_loop
	s_barrier
	s_branch .Lfc_epi
.Lfc_h1_entry:
	s_setprio 1
	s_add_u32 m0, s22, 0x0
	s_nop 0
	global_load_lds_dwordx4 v5, s[24:25]
	s_add_u32 m0, s22, 0x400
	s_nop 0
	global_load_lds_dwordx4 v6, s[24:25]
	s_add_u32 m0, s23, 0x0
	s_nop 0
	global_load_lds_dwordx4 v11, s[28:29]
	s_add_u32 m0, s23, 0x400
	s_nop 0
	global_load_lds_dwordx4 v11, s[32:33]
	s_add_u32 m0, s23, 0x800
	s_nop 0
	global_load_lds_dwordx4 v11, s[36:37]
	s_add_u32 s24, s24, 0x80
	s_addc_u32 s25, s25, 0
	s_add_u32 s28, s28, 0x30000
	s_addc_u32 s29, s29, 0
	s_add_u32 s32, s32, 0x30000
	s_addc_u32 s33, s33, 0
	s_add_u32 s36, s36, 0x30000
	s_addc_u32 s37, s37, 0
	s_add_u32 m0, s22, 0xa000
	s_nop 0
	global_load_lds_dwordx4 v5, s[26:27]
	s_add_u32 m0, s22, 0xa400
	s_nop 0
	global_load_lds_dwordx4 v6, s[26:27]
	s_add_u32 m0, s23, 0xa000
	s_nop 0
	global_load_lds_dwordx4 v11, s[30:31]
	s_add_u32 m0, s23, 0xa400
	s_nop 0
	global_load_lds_dwordx4 v11, s[34:35]
	s_add_u32 m0, s23, 0xa800
	s_nop 0
	global_load_lds_dwordx4 v11, s[38:39]
	s_add_u32 s26, s26, 0x80
	s_addc_u32 s27, s27, 0
	s_add_u32 s30, s30, 0x30000
	s_addc_u32 s31, s31, 0
	s_add_u32 s34, s34, 0x30000
	s_addc_u32 s35, s35, 0
	s_add_u32 s38, s38, 0x30000
	s_addc_u32 s39, s39, 0
	s_add_u32 m0, s22, 0x14000
	s_nop 0
	global_load_lds_dwordx4 v5, s[24:25]
	s_add_u32 m0, s22, 0x14400
	s_nop 0
	global_load_lds_dwordx4 v6, s[24:25]
	s_add_u32 m0, s23, 0x14000
	s_nop 0
	global_load_lds_dwordx4 v11, s[28:29]
	s_add_u32 m0, s23, 0x14400
	s_nop 0
	global_load_lds_dwordx4 v11, s[32:33]
	s_add_u32 m0, s23, 0x14800
	s_nop 0
	global_load_lds_dwordx4 v11, s[36:37]
	s_add_u32 s24, s24, 0x80
	s_addc_u32 s25, s25, 0
	s_add_u32 s28, s28, 0x30000
	s_addc_u32 s29, s29, 0
	s_add_u32 s32, s32, 0x30000
	s_addc_u32 s33, s33, 0
	s_add_u32 s36, s36, 0x30000
	s_addc_u32 s37, s37, 0
	s_add_u32 m0, s22, 0x1e000
	s_nop 0
	global_load_lds_dwordx4 v5, s[26:27]
	s_add_u32 m0, s22, 0x1e400
	s_nop 0
	global_load_lds_dwordx4 v6, s[26:27]
	s_add_u32 m0, s23, 0x1e000
	s_nop 0
	global_load_lds_dwordx4 v11, s[30:31]
	s_add_u32 m0, s23, 0x1e400
	s_nop 0
	global_load_lds_dwordx4 v11, s[34:35]
	s_add_u32 m0, s23, 0x1e800
	s_nop 0
	global_load_lds_dwordx4 v11, s[38:39]
	s_add_u32 s26, s26, 0x80
	s_addc_u32 s27, s27, 0
	s_add_u32 s30, s30, 0x30000
	s_addc_u32 s31, s31, 0
	s_add_u32 s34, s34, 0x30000
	s_addc_u32 s35, s35, 0
	s_add_u32 s38, s38, 0x30000
	s_addc_u32 s39, s39, 0
	s_waitcnt vmcnt(20)
	v_cvt_pk_f16_f32 v12, v40, v41
	v_cvt_pk_f16_f32 v13, v42, v43
	v_cvt_pk_f16_f32 v14, v44, v45
	v_cvt_pk_f16_f32 v15, v46, v47
	v_cvt_pk_f16_f32 v56, v56, v57
	v_cvt_pk_f16_f32 v57, v58, v59
	v_cvt_pk_f16_f32 v58, v60, v61
	v_cvt_pk_f16_f32 v59, v62, v63
	v_cvt_pk_f16_f32 v60, v48, v49
	v_cvt_pk_f16_f32 v61, v50, v51
	v_cvt_pk_f16_f32 v62, v52, v53
	v_cvt_pk_f16_f32 v63, v54, v55
	v_mov_b32_e32 v64, v16
	v_mov_b32_e32 v65, v17
	v_mov_b32_e32 v66, v18
	v_mov_b32_e32 v67, v19
	v_mov_b32_e32 v68, v20
	v_mov_b32_e32 v69, v21
	v_mov_b32_e32 v70, v22
	v_mov_b32_e32 v71, v23
	v_mov_b32_e32 v72, v24
	v_mov_b32_e32 v73, v25
	v_mov_b32_e32 v74, v26
	v_mov_b32_e32 v75, v27
	v_mov_b32_e32 v76, v28
	v_mov_b32_e32 v77, v29
	v_mov_b32_e32 v78, v30
	v_mov_b32_e32 v79, v31
	v_mov_b32_e32 v80, v32
	v_mov_b32_e32 v81, v33
	v_mov_b32_e32 v82, v34
	v_mov_b32_e32 v83, v35
	v_mov_b32_e32 v84, v36
	v_mov_b32_e32 v85, v37
	v_mov_b32_e32 v86, v38
	v_mov_b32_e32 v87, v39
	v_mov_b32_e32 v88, v16
	v_mov_b32_e32 v89, v17
	v_mov_b32_e32 v90, v18
	v_mov_b32_e32 v91, v19
	v_mov_b32_e32 v92, v20
	v_mov_b32_e32 v93, v21
	v_mov_b32_e32 v94, v22
	v_mov_b32_e32 v95, v23
	v_mov_b32_e32 v96, v24
	v_mov_b32_e32 v97, v25
	v_mov_b32_e32 v98, v26
	v_mov_b32_e32 v99, v27
	v_mov_b32_e32 v100, v28
	v_mov_b32_e32 v101, v29
	v_mov_b32_e32 v102, v30
	v_mov_b32_e32 v103, v31
	v_mov_b32_e32 v104, v32
	v_mov_b32_e32 v105, v33
	v_mov_b32_e32 v106, v34
	v_mov_b32_e32 v107, v35
	v_mov_b32_e32 v108, v36
	v_mov_b32_e32 v109, v37
	v_mov_b32_e32 v110, v38
	v_mov_b32_e32 v111, v39
	v_mov_b32_e32 v112, v16
	v_mov_b32_e32 v113, v17
	v_mov_b32_e32 v114, v18
	v_mov_b32_e32 v115, v19
	v_mov_b32_e32 v116, v20
	v_mov_b32_e32 v117, v21
	v_mov_b32_e32 v118, v22
	v_mov_b32_e32 v119, v23
	v_mov_b32_e32 v120, v24
	v_mov_b32_e32 v121, v25
	v_mov_b32_e32 v122, v26
	v_mov_b32_e32 v123, v27
	v_mov_b32_e32 v124, v28
	v_mov_b32_e32 v125, v29
	v_mov_b32_e32 v126, v30
	v_mov_b32_e32 v127, v31
	v_mov_b32_e32 v128, v32
	v_mov_b32_e32 v129, v33
	v_mov_b32_e32 v130, v34
	v_mov_b32_e32 v131, v35
	v_mov_b32_e32 v132, v36
	v_mov_b32_e32 v133, v37
	v_mov_b32_e32 v134, v38
	v_mov_b32_e32 v135, v39
	v_mov_b32_e32 v136, v16
	v_mov_b32_e32 v137, v17
	v_mov_b32_e32 v138, v18
	v_mov_b32_e32 v139, v19
	v_mov_b32_e32 v140, v20
	v_mov_b32_e32 v141, v21
	v_mov_b32_e32 v142, v22
	v_mov_b32_e32 v143, v23
	v_mov_b32_e32 v144, v24
	v_mov_b32_e32 v145, v25
	v_mov_b32_e32 v146, v26
	v_mov_b32_e32 v147, v27
	v_mov_b32_e32 v148, v28
	v_mov_b32_e32 v149, v29
	v_mov_b32_e32 v150, v30
	v_mov_b32_e32 v151, v31
	v_mov_b32_e32 v152, v32
	v_mov_b32_e32 v153, v33
	v_mov_b32_e32 v154, v34
	v_mov_b32_e32 v155, v35
	v_mov_b32_e32 v156, v36
	v_mov_b32_e32 v157, v37
	v_mov_b32_e32 v158, v38
	v_mov_b32_e32 v159, v39
	v_mov_b32_e32 v160, v16
	v_mov_b32_e32 v161, v17
	v_mov_b32_e32 v162, v18
	v_mov_b32_e32 v163, v19
	v_mov_b32_e32 v164, v20
	v_mov_b32_e32 v165, v21
	v_mov_b32_e32 v166, v22
	v_mov_b32_e32 v167, v23
	v_mov_b32_e32 v168, v24
	v_mov_b32_e32 v169, v25
	v_mov_b32_e32 v170, v26
	v_mov_b32_e32 v171, v27
	v_mov_b32_e32 v172, v28
	v_mov_b32_e32 v173, v29
	v_mov_b32_e32 v174, v30
	v_mov_b32_e32 v175, v31
	v_mov_b32_e32 v176, v32
	v_mov_b32_e32 v177, v33
	v_mov_b32_e32 v178, v34
	v_mov_b32_e32 v179, v35
	v_mov_b32_e32 v180, v36
	v_mov_b32_e32 v181, v37
	v_mov_b32_e32 v182, v38
	v_mov_b32_e32 v183, v39
	v_mov_b32_e32 v184, v16
	v_mov_b32_e32 v185, v17
	v_mov_b32_e32 v186, v18
	v_mov_b32_e32 v187, v19
	v_mov_b32_e32 v188, v20
	v_mov_b32_e32 v189, v21
	v_mov_b32_e32 v190, v22
	v_mov_b32_e32 v191, v23
	v_mov_b32_e32 v192, v24
	v_mov_b32_e32 v193, v25
	v_mov_b32_e32 v194, v26
	v_mov_b32_e32 v195, v27
	v_mov_b32_e32 v196, v28
	v_mov_b32_e32 v197, v29
	v_mov_b32_e32 v198, v30
	v_mov_b32_e32 v199, v31
	v_mov_b32_e32 v200, v32
	v_mov_b32_e32 v201, v33
	v_mov_b32_e32 v202, v34
	v_mov_b32_e32 v203, v35
	v_mov_b32_e32 v204, v36
	v_mov_b32_e32 v205, v37
	v_mov_b32_e32 v206, v38
	v_mov_b32_e32 v207, v39
	v_mov_b32_e32 v208, v16
	v_mov_b32_e32 v209, v17
	v_mov_b32_e32 v210, v18
	v_mov_b32_e32 v211, v19
	v_mov_b32_e32 v212, v20
	v_mov_b32_e32 v213, v21
	v_mov_b32_e32 v214, v22
	v_mov_b32_e32 v215, v23
	v_mov_b32_e32 v216, v24
	v_mov_b32_e32 v217, v25
	v_mov_b32_e32 v218, v26
	v_mov_b32_e32 v219, v27
	v_mov_b32_e32 v220, v28
	v_mov_b32_e32 v221, v29
	v_mov_b32_e32 v222, v30
	v_mov_b32_e32 v223, v31
	v_mov_b32_e32 v224, v32
	v_mov_b32_e32 v225, v33
	v_mov_b32_e32 v226, v34
	v_mov_b32_e32 v227, v35
	v_mov_b32_e32 v228, v36
	v_mov_b32_e32 v229, v37
	v_mov_b32_e32 v230, v38
	v_mov_b32_e32 v231, v39
	v_mov_b32_e32 v232, v16
	v_mov_b32_e32 v233, v17
	v_mov_b32_e32 v234, v18
	v_mov_b32_e32 v235, v19
	v_mov_b32_e32 v236, v20
	v_mov_b32_e32 v237, v21
	v_mov_b32_e32 v238, v22
	v_mov_b32_e32 v239, v23
	v_mov_b32_e32 v240, v24
	v_mov_b32_e32 v241, v25
	v_mov_b32_e32 v242, v26
	v_mov_b32_e32 v243, v27
	v_mov_b32_e32 v244, v28
	v_mov_b32_e32 v245, v29
	v_mov_b32_e32 v246, v30
	v_mov_b32_e32 v247, v31
	v_mov_b32_e32 v248, v32
	v_mov_b32_e32 v249, v33
	v_mov_b32_e32 v250, v34
	v_mov_b32_e32 v251, v35
	v_mov_b32_e32 v252, v36
	v_mov_b32_e32 v253, v37
	v_mov_b32_e32 v254, v38
	v_mov_b32_e32 v255, v39
	s_waitcnt vmcnt(15)
	s_barrier
	s_barrier
.Lfc_h1_loop:
	ds_read_b128 v[16:19], v3 offset:0
	ds_read_b128 v[20:23], v3 offset:1024
	ds_read_b128 v[24:27], v3 offset:2048
	ds_read_b128 v[28:31], v3 offset:3072
	ds_read_b128 v[32:35], v3 offset:4096
	ds_read_b128 v[36:39], v3 offset:5120
	ds_read_b128 v[40:43], v1 offset:0
	ds_read_b128 v[44:47], v1 offset:1024
	ds_read_b128 v[48:51], v1 offset:2048
	ds_read_b128 v[52:55], v1 offset:3072
	s_cmp_eq_u32 s21, 0
	s_cbranch_scc1 .Lfc_ng_10
	s_add_u32 m0, s22, 0x1e000
	s_nop 0
	global_load_lds_dwordx4 v5, s[26:27]
	s_add_u32 m0, s22, 0x1e400
	s_nop 0
	global_load_lds_dwordx4 v6, s[26:27]
	s_add_u32 m0, s23, 0x1e000
	s_nop 0
	global_load_lds_dwordx4 v11, s[30:31]
	s_add_u32 m0, s23, 0x1e400
	s_nop 0
	global_load_lds_dwordx4 v11, s[34:35]
	s_add_u32 m0, s23, 0x1e800
	s_nop 0
	global_load_lds_dwordx4 v11, s[38:39]
	s_add_u32 s26, s26, 0x80
	s_addc_u32 s27, s27, 0
	s_add_u32 s30, s30, 0x30000
	s_addc_u32 s31, s31, 0
	s_add_u32 s34, s34, 0x30000
	s_addc_u32 s35, s35, 0
	s_add_u32 s38, s38, 0x30000
	s_addc_u32 s39, s39, 0
	s_cmp_eq_u32 s21, 3
	s_cbranch_scc1 .Lfc_sw_11
	s_cmp_eq_u32 s21, 7
	s_cbranch_scc0 .Lfc_swd_11

.Lfc_swd_11:
.Lfc_ng_10:
	s_cmp_eq_u32 s21, 11
	s_cbranch_scc1 .Lfc_w0_12
	s_waitcnt vmcnt(10)
	s_branch .Lfc_w1_12

.Lfc_w1_12:
	s_barrier
	s_waitcnt lgkmcnt(0)
	v_mfma_f32_16x16x32_f16 v[64:67], v[16:19], v[40:43], v[64:67]
	v_mfma_f32_16x16x32_f16 v[68:71], v[20:23], v[40:43], v[68:71]
	v_mfma_f32_16x16x32_f16 v[72:75], v[24:27], v[40:43], v[72:75]
	v_mfma_f32_16x16x32_f16 v[76:79], v[28:31], v[40:43], v[76:79]
	v_mfma_f32_16x16x32_f16 v[80:83], v[32:35], v[40:43], v[80:83]
	v_mfma_f32_16x16x32_f16 v[84:87], v[36:39], v[40:43], v[84:87]
	v_mfma_f32_16x16x32_f16 v[88:91], v[16:19], v[44:47], v[88:91]
	ds_read_b128 v[40:43], v1 offset:4096
	v_mfma_f32_16x16x32_f16 v[92:95], v[20:23], v[44:47], v[92:95]
	v_mfma_f32_16x16x32_f16 v[96:99], v[24:27], v[44:47], v[96:99]
	v_mfma_f32_16x16x32_f16 v[100:103], v[28:31], v[44:47], v[100:103]
	v_mfma_f32_16x16x32_f16 v[104:107], v[32:35], v[44:47], v[104:107]
	v_mfma_f32_16x16x32_f16 v[108:111], v[36:39], v[44:47], v[108:111]
	v_mfma_f32_16x16x32_f16 v[112:115], v[16:19], v[48:51], v[112:115]
	ds_read_b128 v[44:47], v1 offset:5120
	v_mfma_f32_16x16x32_f16 v[116:119], v[20:23], v[48:51], v[116:119]
	v_mfma_f32_16x16x32_f16 v[120:123], v[24:27], v[48:51], v[120:123]
	v_mfma_f32_16x16x32_f16 v[124:127], v[28:31], v[48:51], v[124:127]
	v_mfma_f32_16x16x32_f16 v[128:131], v[32:35], v[48:51], v[128:131]
	v_mfma_f32_16x16x32_f16 v[132:135], v[36:39], v[48:51], v[132:135]
	v_mfma_f32_16x16x32_f16 v[136:139], v[16:19], v[52:55], v[136:139]
	ds_read_b128 v[48:51], v1 offset:6144
	v_mfma_f32_16x16x32_f16 v[140:143], v[20:23], v[52:55], v[140:143]
	v_mfma_f32_16x16x32_f16 v[144:147], v[24:27], v[52:55], v[144:147]
	v_mfma_f32_16x16x32_f16 v[148:151], v[28:31], v[52:55], v[148:151]
	v_mfma_f32_16x16x32_f16 v[152:155], v[32:35], v[52:55], v[152:155]
	v_mfma_f32_16x16x32_f16 v[156:159], v[36:39], v[52:55], v[156:159]
	s_waitcnt lgkmcnt(2)
	v_mfma_f32_16x16x32_f16 v[160:163], v[16:19], v[40:43], v[160:163]
	ds_read_b128 v[52:55], v1 offset:7168
	v_mfma_f32_16x16x32_f16 v[164:167], v[20:23], v[40:43], v[164:167]
	v_mfma_f32_16x16x32_f16 v[168:171], v[24:27], v[40:43], v[168:171]
	v_mfma_f32_16x16x32_f16 v[172:175], v[28:31], v[40:43], v[172:175]
	v_mfma_f32_16x16x32_f16 v[176:179], v[32:35], v[40:43], v[176:179]
	v_mfma_f32_16x16x32_f16 v[180:183], v[36:39], v[40:43], v[180:183]
	s_waitcnt lgkmcnt(2)
	v_mfma_f32_16x16x32_f16 v[184:187], v[16:19], v[44:47], v[184:187]
	v_mfma_f32_16x16x32_f16 v[188:191], v[20:23], v[44:47], v[188:191]
	v_mfma_f32_16x16x32_f16 v[192:195], v[24:27], v[44:47], v[192:195]
	v_mfma_f32_16x16x32_f16 v[196:199], v[28:31], v[44:47], v[196:199]
	v_mfma_f32_16x16x32_f16 v[200:203], v[32:35], v[44:47], v[200:203]
	v_mfma_f32_16x16x32_f16 v[204:207], v[36:39], v[44:47], v[204:207]
	s_waitcnt lgkmcnt(1)
	v_mfma_f32_16x16x32_f16 v[208:211], v[16:19], v[48:51], v[208:211]
	v_mfma_f32_16x16x32_f16 v[212:215], v[20:23], v[48:51], v[212:215]
	v_mfma_f32_16x16x32_f16 v[216:219], v[24:27], v[48:51], v[216:219]
	v_mfma_f32_16x16x32_f16 v[220:223], v[28:31], v[48:51], v[220:223]
	v_mfma_f32_16x16x32_f16 v[224:227], v[32:35], v[48:51], v[224:227]
	v_mfma_f32_16x16x32_f16 v[228:231], v[36:39], v[48:51], v[228:231]
	s_waitcnt lgkmcnt(0)
	v_mfma_f32_16x16x32_f16 v[232:235], v[16:19], v[52:55], v[232:235]
	v_mfma_f32_16x16x32_f16 v[236:239], v[20:23], v[52:55], v[236:239]
	v_mfma_f32_16x16x32_f16 v[240:243], v[24:27], v[52:55], v[240:243]
	v_mfma_f32_16x16x32_f16 v[244:247], v[28:31], v[52:55], v[244:247]
	v_mfma_f32_16x16x32_f16 v[248:251], v[32:35], v[52:55], v[248:251]
	v_mfma_f32_16x16x32_f16 v[252:255], v[36:39], v[52:55], v[252:255]
	s_barrier
	ds_read_b128 v[16:19], v3 offset:40960
	ds_read_b128 v[20:23], v3 offset:41984
	ds_read_b128 v[24:27], v3 offset:43008
	ds_read_b128 v[28:31], v3 offset:44032
	ds_read_b128 v[32:35], v3 offset:45056
	ds_read_b128 v[36:39], v3 offset:46080
	ds_read_b128 v[40:43], v1 offset:40960
	ds_read_b128 v[44:47], v1 offset:41984
	ds_read_b128 v[48:51], v1 offset:43008
	ds_read_b128 v[52:55], v1 offset:44032
	s_cmp_eq_u32 s21, 11
	s_cbranch_scc1 .Lfc_ng_13
	s_add_u32 m0, s22, 0x0
	s_nop 0
	global_load_lds_dwordx4 v5, s[24:25]
	s_add_u32 m0, s22, 0x400
	s_nop 0
	global_load_lds_dwordx4 v6, s[24:25]
	s_add_u32 m0, s23, 0x0
	s_nop 0
	global_load_lds_dwordx4 v11, s[28:29]
	s_add_u32 m0, s23, 0x400
	s_nop 0
	global_load_lds_dwordx4 v11, s[32:33]
	s_add_u32 m0, s23, 0x800
	s_nop 0
	global_load_lds_dwordx4 v11, s[36:37]
	s_add_u32 s24, s24, 0x80
	s_addc_u32 s25, s25, 0
	s_add_u32 s28, s28, 0x30000
	s_addc_u32 s29, s29, 0
	s_add_u32 s32, s32, 0x30000
	s_addc_u32 s33, s33, 0
	s_add_u32 s36, s36, 0x30000
	s_addc_u32 s37, s37, 0
.Lfc_ng_13:
	s_cmp_eq_u32 s21, 11
	s_cbranch_scc1 .Lfc_w0_14
	s_waitcnt vmcnt(10)
	s_branch .Lfc_w1_14

.Lfc_w1_14:
	s_barrier
	s_waitcnt lgkmcnt(0)
	v_mfma_f32_16x16x32_f16 v[64:67], v[16:19], v[40:43], v[64:67]
	v_mfma_f32_16x16x32_f16 v[68:71], v[20:23], v[40:43], v[68:71]
	v_mfma_f32_16x16x32_f16 v[72:75], v[24:27], v[40:43], v[72:75]
	v_mfma_f32_16x16x32_f16 v[76:79], v[28:31], v[40:43], v[76:79]
	v_mfma_f32_16x16x32_f16 v[80:83], v[32:35], v[40:43], v[80:83]
	v_mfma_f32_16x16x32_f16 v[84:87], v[36:39], v[40:43], v[84:87]
	v_mfma_f32_16x16x32_f16 v[88:91], v[16:19], v[44:47], v[88:91]
	ds_read_b128 v[40:43], v1 offset:45056
	v_mfma_f32_16x16x32_f16 v[92:95], v[20:23], v[44:47], v[92:95]
	v_mfma_f32_16x16x32_f16 v[96:99], v[24:27], v[44:47], v[96:99]
	v_mfma_f32_16x16x32_f16 v[100:103], v[28:31], v[44:47], v[100:103]
	v_mfma_f32_16x16x32_f16 v[104:107], v[32:35], v[44:47], v[104:107]
	v_mfma_f32_16x16x32_f16 v[108:111], v[36:39], v[44:47], v[108:111]
	v_mfma_f32_16x16x32_f16 v[112:115], v[16:19], v[48:51], v[112:115]
	ds_read_b128 v[44:47], v1 offset:46080
	v_mfma_f32_16x16x32_f16 v[116:119], v[20:23], v[48:51], v[116:119]
	v_mfma_f32_16x16x32_f16 v[120:123], v[24:27], v[48:51], v[120:123]
	v_mfma_f32_16x16x32_f16 v[124:127], v[28:31], v[48:51], v[124:127]
	v_mfma_f32_16x16x32_f16 v[128:131], v[32:35], v[48:51], v[128:131]
	v_mfma_f32_16x16x32_f16 v[132:135], v[36:39], v[48:51], v[132:135]
	v_mfma_f32_16x16x32_f16 v[136:139], v[16:19], v[52:55], v[136:139]
	ds_read_b128 v[48:51], v1 offset:47104
	v_mfma_f32_16x16x32_f16 v[140:143], v[20:23], v[52:55], v[140:143]
	v_mfma_f32_16x16x32_f16 v[144:147], v[24:27], v[52:55], v[144:147]
	v_mfma_f32_16x16x32_f16 v[148:151], v[28:31], v[52:55], v[148:151]
	v_mfma_f32_16x16x32_f16 v[152:155], v[32:35], v[52:55], v[152:155]
	v_mfma_f32_16x16x32_f16 v[156:159], v[36:39], v[52:55], v[156:159]
	s_waitcnt lgkmcnt(2)
	v_mfma_f32_16x16x32_f16 v[160:163], v[16:19], v[40:43], v[160:163]
	ds_read_b128 v[52:55], v1 offset:48128
	v_mfma_f32_16x16x32_f16 v[164:167], v[20:23], v[40:43], v[164:167]
	v_mfma_f32_16x16x32_f16 v[168:171], v[24:27], v[40:43], v[168:171]
	v_mfma_f32_16x16x32_f16 v[172:175], v[28:31], v[40:43], v[172:175]
	v_mfma_f32_16x16x32_f16 v[176:179], v[32:35], v[40:43], v[176:179]
	v_mfma_f32_16x16x32_f16 v[180:183], v[36:39], v[40:43], v[180:183]
	s_waitcnt lgkmcnt(2)
	v_mfma_f32_16x16x32_f16 v[184:187], v[16:19], v[44:47], v[184:187]
	v_mfma_f32_16x16x32_f16 v[188:191], v[20:23], v[44:47], v[188:191]
	v_mfma_f32_16x16x32_f16 v[192:195], v[24:27], v[44:47], v[192:195]
	v_mfma_f32_16x16x32_f16 v[196:199], v[28:31], v[44:47], v[196:199]
	v_mfma_f32_16x16x32_f16 v[200:203], v[32:35], v[44:47], v[200:203]
	v_mfma_f32_16x16x32_f16 v[204:207], v[36:39], v[44:47], v[204:207]
	s_waitcnt lgkmcnt(1)
	v_mfma_f32_16x16x32_f16 v[208:211], v[16:19], v[48:51], v[208:211]
	v_mfma_f32_16x16x32_f16 v[212:215], v[20:23], v[48:51], v[212:215]
	v_mfma_f32_16x16x32_f16 v[216:219], v[24:27], v[48:51], v[216:219]
	v_mfma_f32_16x16x32_f16 v[220:223], v[28:31], v[48:51], v[220:223]
	v_mfma_f32_16x16x32_f16 v[224:227], v[32:35], v[48:51], v[224:227]
	v_mfma_f32_16x16x32_f16 v[228:231], v[36:39], v[48:51], v[228:231]
	s_waitcnt lgkmcnt(0)
	v_mfma_f32_16x16x32_f16 v[232:235], v[16:19], v[52:55], v[232:235]
	v_mfma_f32_16x16x32_f16 v[236:239], v[20:23], v[52:55], v[236:239]
	v_mfma_f32_16x16x32_f16 v[240:243], v[24:27], v[52:55], v[240:243]
	v_mfma_f32_16x16x32_f16 v[244:247], v[28:31], v[52:55], v[244:247]
	v_mfma_f32_16x16x32_f16 v[248:251], v[32:35], v[52:55], v[248:251]
	v_mfma_f32_16x16x32_f16 v[252:255], v[36:39], v[52:55], v[252:255]
	s_barrier
	ds_read_b128 v[16:19], v4 offset:0
	ds_read_b128 v[20:23], v4 offset:1024
	ds_read_b128 v[24:27], v4 offset:2048
	ds_read_b128 v[28:31], v4 offset:3072
	ds_read_b128 v[32:35], v4 offset:4096
	ds_read_b128 v[36:39], v4 offset:5120
	ds_read_b128 v[40:43], v2 offset:0
	ds_read_b128 v[44:47], v2 offset:1024
	ds_read_b128 v[48:51], v2 offset:2048
	ds_read_b128 v[52:55], v2 offset:3072
	s_cmp_eq_u32 s21, 11
	s_cbranch_scc1 .Lfc_ng_15
	s_add_u32 m0, s22, 0xa000
	s_nop 0
	global_load_lds_dwordx4 v5, s[26:27]
	s_add_u32 m0, s22, 0xa400
	s_nop 0
	global_load_lds_dwordx4 v6, s[26:27]
	s_add_u32 m0, s23, 0xa000
	s_nop 0
	global_load_lds_dwordx4 v11, s[30:31]
	s_add_u32 m0, s23, 0xa400
	s_nop 0
	global_load_lds_dwordx4 v11, s[34:35]
	s_add_u32 m0, s23, 0xa800
	s_nop 0
	global_load_lds_dwordx4 v11, s[38:39]
	s_add_u32 s26, s26, 0x80
	s_addc_u32 s27, s27, 0
	s_add_u32 s30, s30, 0x30000
	s_addc_u32 s31, s31, 0
	s_add_u32 s34, s34, 0x30000
	s_addc_u32 s35, s35, 0
	s_add_u32 s38, s38, 0x30000
	s_addc_u32 s39, s39, 0

.Lfc_w1_16:
	s_barrier
	s_waitcnt lgkmcnt(0)
	v_mfma_f32_16x16x32_f16 v[64:67], v[16:19], v[40:43], v[64:67]
	v_mfma_f32_16x16x32_f16 v[68:71], v[20:23], v[40:43], v[68:71]
	v_mfma_f32_16x16x32_f16 v[72:75], v[24:27], v[40:43], v[72:75]
	v_mfma_f32_16x16x32_f16 v[76:79], v[28:31], v[40:43], v[76:79]
	v_mfma_f32_16x16x32_f16 v[80:83], v[32:35], v[40:43], v[80:83]
	v_mfma_f32_16x16x32_f16 v[84:87], v[36:39], v[40:43], v[84:87]
	v_mfma_f32_16x16x32_f16 v[88:91], v[16:19], v[44:47], v[88:91]
	ds_read_b128 v[40:43], v2 offset:4096
	v_mfma_f32_16x16x32_f16 v[92:95], v[20:23], v[44:47], v[92:95]
	v_mfma_f32_16x16x32_f16 v[96:99], v[24:27], v[44:47], v[96:99]
	v_mfma_f32_16x16x32_f16 v[100:103], v[28:31], v[44:47], v[100:103]
	v_mfma_f32_16x16x32_f16 v[104:107], v[32:35], v[44:47], v[104:107]
	v_mfma_f32_16x16x32_f16 v[108:111], v[36:39], v[44:47], v[108:111]
	v_mfma_f32_16x16x32_f16 v[112:115], v[16:19], v[48:51], v[112:115]
	ds_read_b128 v[44:47], v2 offset:5120
	v_mfma_f32_16x16x32_f16 v[116:119], v[20:23], v[48:51], v[116:119]
	v_mfma_f32_16x16x32_f16 v[120:123], v[24:27], v[48:51], v[120:123]
	v_mfma_f32_16x16x32_f16 v[124:127], v[28:31], v[48:51], v[124:127]
	v_mfma_f32_16x16x32_f16 v[128:131], v[32:35], v[48:51], v[128:131]
	v_mfma_f32_16x16x32_f16 v[132:135], v[36:39], v[48:51], v[132:135]
	v_mfma_f32_16x16x32_f16 v[136:139], v[16:19], v[52:55], v[136:139]
	ds_read_b128 v[48:51], v2 offset:6144
	v_mfma_f32_16x16x32_f16 v[140:143], v[20:23], v[52:55], v[140:143]
	v_mfma_f32_16x16x32_f16 v[144:147], v[24:27], v[52:55], v[144:147]
	v_mfma_f32_16x16x32_f16 v[148:151], v[28:31], v[52:55], v[148:151]
	v_mfma_f32_16x16x32_f16 v[152:155], v[32:35], v[52:55], v[152:155]
	v_mfma_f32_16x16x32_f16 v[156:159], v[36:39], v[52:55], v[156:159]
	s_waitcnt lgkmcnt(2)
	v_mfma_f32_16x16x32_f16 v[160:163], v[16:19], v[40:43], v[160:163]
	ds_read_b128 v[52:55], v2 offset:7168
	v_mfma_f32_16x16x32_f16 v[164:167], v[20:23], v[40:43], v[164:167]
	v_mfma_f32_16x16x32_f16 v[168:171], v[24:27], v[40:43], v[168:171]
	v_mfma_f32_16x16x32_f16 v[172:175], v[28:31], v[40:43], v[172:175]
	v_mfma_f32_16x16x32_f16 v[176:179], v[32:35], v[40:43], v[176:179]
	v_mfma_f32_16x16x32_f16 v[180:183], v[36:39], v[40:43], v[180:183]
	s_waitcnt lgkmcnt(2)
	v_mfma_f32_16x16x32_f16 v[184:187], v[16:19], v[44:47], v[184:187]
	v_mfma_f32_16x16x32_f16 v[188:191], v[20:23], v[44:47], v[188:191]
	v_mfma_f32_16x16x32_f16 v[192:195], v[24:27], v[44:47], v[192:195]
	v_mfma_f32_16x16x32_f16 v[196:199], v[28:31], v[44:47], v[196:199]
	v_mfma_f32_16x16x32_f16 v[200:203], v[32:35], v[44:47], v[200:203]
	v_mfma_f32_16x16x32_f16 v[204:207], v[36:39], v[44:47], v[204:207]
	s_waitcnt lgkmcnt(1)
	v_mfma_f32_16x16x32_f16 v[208:211], v[16:19], v[48:51], v[208:211]
	v_mfma_f32_16x16x32_f16 v[212:215], v[20:23], v[48:51], v[212:215]
	v_mfma_f32_16x16x32_f16 v[216:219], v[24:27], v[48:51], v[216:219]
	v_mfma_f32_16x16x32_f16 v[220:223], v[28:31], v[48:51], v[220:223]
	v_mfma_f32_16x16x32_f16 v[224:227], v[32:35], v[48:51], v[224:227]
	v_mfma_f32_16x16x32_f16 v[228:231], v[36:39], v[48:51], v[228:231]
	s_waitcnt lgkmcnt(0)
	v_mfma_f32_16x16x32_f16 v[232:235], v[16:19], v[52:55], v[232:235]
	v_mfma_f32_16x16x32_f16 v[236:239], v[20:23], v[52:55], v[236:239]
	v_mfma_f32_16x16x32_f16 v[240:243], v[24:27], v[52:55], v[240:243]
	v_mfma_f32_16x16x32_f16 v[244:247], v[28:31], v[52:55], v[244:247]
	v_mfma_f32_16x16x32_f16 v[248:251], v[32:35], v[52:55], v[248:251]
	v_mfma_f32_16x16x32_f16 v[252:255], v[36:39], v[52:55], v[252:255]
	s_barrier
	ds_read_b128 v[16:19], v4 offset:40960
	ds_read_b128 v[20:23], v4 offset:41984
	ds_read_b128 v[24:27], v4 offset:43008
	ds_read_b128 v[28:31], v4 offset:44032
	ds_read_b128 v[32:35], v4 offset:45056
	ds_read_b128 v[36:39], v4 offset:46080
	ds_read_b128 v[40:43], v2 offset:40960
	ds_read_b128 v[44:47], v2 offset:41984
	ds_read_b128 v[48:51], v2 offset:43008
	ds_read_b128 v[52:55], v2 offset:44032
	s_cmp_eq_u32 s21, 11
	s_cbranch_scc1 .Lfc_ng_17
	s_add_u32 m0, s22, 0x14000
	s_nop 0
	global_load_lds_dwordx4 v5, s[24:25]
	s_add_u32 m0, s22, 0x14400
	s_nop 0
	global_load_lds_dwordx4 v6, s[24:25]
	s_add_u32 m0, s23, 0x14000
	s_nop 0
	global_load_lds_dwordx4 v11, s[28:29]
	s_add_u32 m0, s23, 0x14400
	s_nop 0
	global_load_lds_dwordx4 v11, s[32:33]
	s_add_u32 m0, s23, 0x14800
	s_nop 0
	global_load_lds_dwordx4 v11, s[36:37]
	s_add_u32 s24, s24, 0x80
	s_addc_u32 s25, s25, 0
	s_add_u32 s28, s28, 0x30000
	s_addc_u32 s29, s29, 0
	s_add_u32 s32, s32, 0x30000
	s_addc_u32 s33, s33, 0
	s_add_u32 s36, s36, 0x30000
	s_addc_u32 s37, s37, 0

.Lfc_w1_18:
	s_barrier
	s_waitcnt lgkmcnt(0)
	v_mfma_f32_16x16x32_f16 v[64:67], v[16:19], v[40:43], v[64:67]
	v_mfma_f32_16x16x32_f16 v[68:71], v[20:23], v[40:43], v[68:71]
	v_mfma_f32_16x16x32_f16 v[72:75], v[24:27], v[40:43], v[72:75]
	v_mfma_f32_16x16x32_f16 v[76:79], v[28:31], v[40:43], v[76:79]
	v_mfma_f32_16x16x32_f16 v[80:83], v[32:35], v[40:43], v[80:83]
	v_mfma_f32_16x16x32_f16 v[84:87], v[36:39], v[40:43], v[84:87]
	v_mfma_f32_16x16x32_f16 v[88:91], v[16:19], v[44:47], v[88:91]
	ds_read_b128 v[40:43], v2 offset:45056
	v_mfma_f32_16x16x32_f16 v[92:95], v[20:23], v[44:47], v[92:95]
	v_mfma_f32_16x16x32_f16 v[96:99], v[24:27], v[44:47], v[96:99]
	v_mfma_f32_16x16x32_f16 v[100:103], v[28:31], v[44:47], v[100:103]
	v_mfma_f32_16x16x32_f16 v[104:107], v[32:35], v[44:47], v[104:107]
	v_mfma_f32_16x16x32_f16 v[108:111], v[36:39], v[44:47], v[108:111]
	v_mfma_f32_16x16x32_f16 v[112:115], v[16:19], v[48:51], v[112:115]
	ds_read_b128 v[44:47], v2 offset:46080
	v_mfma_f32_16x16x32_f16 v[116:119], v[20:23], v[48:51], v[116:119]
	v_mfma_f32_16x16x32_f16 v[120:123], v[24:27], v[48:51], v[120:123]
	v_mfma_f32_16x16x32_f16 v[124:127], v[28:31], v[48:51], v[124:127]
	v_mfma_f32_16x16x32_f16 v[128:131], v[32:35], v[48:51], v[128:131]
	v_mfma_f32_16x16x32_f16 v[132:135], v[36:39], v[48:51], v[132:135]
	v_mfma_f32_16x16x32_f16 v[136:139], v[16:19], v[52:55], v[136:139]
	ds_read_b128 v[48:51], v2 offset:47104
	v_mfma_f32_16x16x32_f16 v[140:143], v[20:23], v[52:55], v[140:143]
	v_mfma_f32_16x16x32_f16 v[144:147], v[24:27], v[52:55], v[144:147]
	v_mfma_f32_16x16x32_f16 v[148:151], v[28:31], v[52:55], v[148:151]
	v_mfma_f32_16x16x32_f16 v[152:155], v[32:35], v[52:55], v[152:155]
	v_mfma_f32_16x16x32_f16 v[156:159], v[36:39], v[52:55], v[156:159]
	s_waitcnt lgkmcnt(2)
	v_mfma_f32_16x16x32_f16 v[160:163], v[16:19], v[40:43], v[160:163]
	ds_read_b128 v[52:55], v2 offset:48128
	v_mfma_f32_16x16x32_f16 v[164:167], v[20:23], v[40:43], v[164:167]
	v_mfma_f32_16x16x32_f16 v[168:171], v[24:27], v[40:43], v[168:171]
	v_mfma_f32_16x16x32_f16 v[172:175], v[28:31], v[40:43], v[172:175]
	v_mfma_f32_16x16x32_f16 v[176:179], v[32:35], v[40:43], v[176:179]
	v_mfma_f32_16x16x32_f16 v[180:183], v[36:39], v[40:43], v[180:183]
	s_waitcnt lgkmcnt(2)
	v_mfma_f32_16x16x32_f16 v[184:187], v[16:19], v[44:47], v[184:187]
	v_mfma_f32_16x16x32_f16 v[188:191], v[20:23], v[44:47], v[188:191]
	v_mfma_f32_16x16x32_f16 v[192:195], v[24:27], v[44:47], v[192:195]
	v_mfma_f32_16x16x32_f16 v[196:199], v[28:31], v[44:47], v[196:199]
	v_mfma_f32_16x16x32_f16 v[200:203], v[32:35], v[44:47], v[200:203]
	v_mfma_f32_16x16x32_f16 v[204:207], v[36:39], v[44:47], v[204:207]
	s_waitcnt lgkmcnt(1)
	v_mfma_f32_16x16x32_f16 v[208:211], v[16:19], v[48:51], v[208:211]
	v_mfma_f32_16x16x32_f16 v[212:215], v[20:23], v[48:51], v[212:215]
	v_mfma_f32_16x16x32_f16 v[216:219], v[24:27], v[48:51], v[216:219]
	v_mfma_f32_16x16x32_f16 v[220:223], v[28:31], v[48:51], v[220:223]
	v_mfma_f32_16x16x32_f16 v[224:227], v[32:35], v[48:51], v[224:227]
	v_mfma_f32_16x16x32_f16 v[228:231], v[36:39], v[48:51], v[228:231]
	s_waitcnt lgkmcnt(0)
	v_mfma_f32_16x16x32_f16 v[232:235], v[16:19], v[52:55], v[232:235]
	v_mfma_f32_16x16x32_f16 v[236:239], v[20:23], v[52:55], v[236:239]
	v_mfma_f32_16x16x32_f16 v[240:243], v[24:27], v[52:55], v[240:243]
	v_mfma_f32_16x16x32_f16 v[244:247], v[28:31], v[52:55], v[244:247]
	v_mfma_f32_16x16x32_f16 v[248:251], v[32:35], v[52:55], v[248:251]
	v_mfma_f32_16x16x32_f16 v[252:255], v[36:39], v[52:55], v[252:255]
	s_barrier
	s_add_u32 s21, s21, 1
	s_cmp_lt_u32 s21, 12
	s_cbranch_scc1 .Lfc_h1_loop
.Lfc_epi:
	s_nop 7
	v_and_b32_e32 v16, 63, v0
	v_and_b32_e32 v17, 15, v0
	v_lshrrev_b32_e32 v18, 4, v16
	s_lshl_b32 s90, s18, 8
	s_lshl_b32 s91, s17, 7
	s_add_u32 s90, s90, s91
	v_add_u32_e32 v1, s90, v17
	v_lshlrev_b32_e32 v1, 5, v1
	v_lshl_add_u32 v1, v18, 4, v1
	v_lshlrev_b32_e32 v2, 4, v16
	v_add_u32_e32 v2, 0x10000, v2
	v_cmp_gt_u32_e32 vcc, 2, v18
	s_nop 1
	v_cndmask_b32_e32 v1, v2, v1, vcc
	v_max_f32_e32 v64, 0, v64
	v_max_f32_e32 v65, 0, v65
	v_max_f32_e32 v66, 0, v66
	v_max_f32_e32 v67, 0, v67
	v_max_f32_e32 v68, 0, v68
	v_max_f32_e32 v69, 0, v69
	v_max_f32_e32 v70, 0, v70
	v_max_f32_e32 v71, 0, v71
	v_cvt_pk_f16_f32 v20, v64, v65
	v_cvt_pk_f16_f32 v21, v66, v67
	v_cvt_pk_f16_f32 v22, v68, v69
	v_cvt_pk_f16_f32 v23, v70, v71
	s_nop 1
	v_mfma_f32_16x16x32_f16 v[28:31], v[12:15], v[20:23], 0
	v_max_f32_e32 v72, 0, v72
	v_max_f32_e32 v73, 0, v73
	v_max_f32_e32 v74, 0, v74
	v_max_f32_e32 v75, 0, v75
	v_max_f32_e32 v76, 0, v76
	v_max_f32_e32 v77, 0, v77
	v_max_f32_e32 v78, 0, v78
	v_max_f32_e32 v79, 0, v79
	v_cvt_pk_f16_f32 v24, v72, v73
	v_cvt_pk_f16_f32 v25, v74, v75
	v_cvt_pk_f16_f32 v26, v76, v77
	v_cvt_pk_f16_f32 v27, v78, v79
	s_nop 1
	v_mfma_f32_16x16x32_f16 v[28:31], v[60:63], v[24:27], v[28:31]
	v_max_f32_e32 v80, 0, v80
	v_max_f32_e32 v81, 0, v81
	v_max_f32_e32 v82, 0, v82
	v_max_f32_e32 v83, 0, v83
	v_max_f32_e32 v84, 0, v84
	v_max_f32_e32 v85, 0, v85
	v_max_f32_e32 v86, 0, v86
	v_max_f32_e32 v87, 0, v87
	v_cvt_pk_f16_f32 v20, v80, v81
	v_cvt_pk_f16_f32 v21, v82, v83
	v_cvt_pk_f16_f32 v22, v84, v85
	v_cvt_pk_f16_f32 v23, v86, v87
	s_nop 1
	v_mfma_f32_16x16x32_f16 v[28:31], v[56:59], v[20:23], v[28:31]
	v_max_f32_e32 v88, 0, v88
	v_max_f32_e32 v89, 0, v89
	v_max_f32_e32 v90, 0, v90
	v_max_f32_e32 v91, 0, v91
	v_max_f32_e32 v92, 0, v92
	v_max_f32_e32 v93, 0, v93
	v_max_f32_e32 v94, 0, v94
	v_max_f32_e32 v95, 0, v95
	v_cvt_pk_f16_f32 v24, v88, v89
	v_cvt_pk_f16_f32 v25, v90, v91
	v_cvt_pk_f16_f32 v26, v92, v93
	v_cvt_pk_f16_f32 v27, v94, v95
	s_nop 1
	v_mfma_f32_16x16x32_f16 v[32:35], v[12:15], v[24:27], 0
	v_max_f32_e32 v96, 0, v96
	v_max_f32_e32 v97, 0, v97
	v_max_f32_e32 v98, 0, v98
	v_max_f32_e32 v99, 0, v99
	v_max_f32_e32 v100, 0, v100
	v_max_f32_e32 v101, 0, v101
	v_max_f32_e32 v102, 0, v102
	v_max_f32_e32 v103, 0, v103
	v_cvt_pk_f16_f32 v20, v96, v97
	v_cvt_pk_f16_f32 v21, v98, v99
	v_cvt_pk_f16_f32 v22, v100, v101
	v_cvt_pk_f16_f32 v23, v102, v103
	s_nop 1
	v_mfma_f32_16x16x32_f16 v[32:35], v[60:63], v[20:23], v[32:35]
	ds_write_b128 v1, v[28:31] offset:0
	v_max_f32_e32 v104, 0, v104
	v_max_f32_e32 v105, 0, v105
	v_max_f32_e32 v106, 0, v106
	v_max_f32_e32 v107, 0, v107
	v_max_f32_e32 v108, 0, v108
	v_max_f32_e32 v109, 0, v109
	v_max_f32_e32 v110, 0, v110
	v_max_f32_e32 v111, 0, v111
	v_cvt_pk_f16_f32 v24, v104, v105
	v_cvt_pk_f16_f32 v25, v106, v107
	v_cvt_pk_f16_f32 v26, v108, v109
	v_cvt_pk_f16_f32 v27, v110, v111
	s_nop 1
	v_mfma_f32_16x16x32_f16 v[32:35], v[56:59], v[24:27], v[32:35]
	v_max_f32_e32 v112, 0, v112
	v_max_f32_e32 v113, 0, v113
	v_max_f32_e32 v114, 0, v114
	v_max_f32_e32 v115, 0, v115
	v_max_f32_e32 v116, 0, v116
	v_max_f32_e32 v117, 0, v117
	v_max_f32_e32 v118, 0, v118
	v_max_f32_e32 v119, 0, v119
	v_cvt_pk_f16_f32 v20, v112, v113
	v_cvt_pk_f16_f32 v21, v114, v115
	v_cvt_pk_f16_f32 v22, v116, v117
	v_cvt_pk_f16_f32 v23, v118, v119
	s_nop 1
	v_mfma_f32_16x16x32_f16 v[28:31], v[12:15], v[20:23], 0
	v_max_f32_e32 v120, 0, v120
	v_max_f32_e32 v121, 0, v121
	v_max_f32_e32 v122, 0, v122
	v_max_f32_e32 v123, 0, v123
	v_max_f32_e32 v124, 0, v124
	v_max_f32_e32 v125, 0, v125
	v_max_f32_e32 v126, 0, v126
	v_max_f32_e32 v127, 0, v127
	v_cvt_pk_f16_f32 v24, v120, v121
	v_cvt_pk_f16_f32 v25, v122, v123
	v_cvt_pk_f16_f32 v26, v124, v125
	v_cvt_pk_f16_f32 v27, v126, v127
	s_nop 1
	v_mfma_f32_16x16x32_f16 v[28:31], v[60:63], v[24:27], v[28:31]
	ds_write_b128 v1, v[32:35] offset:512
	v_max_f32_e32 v128, 0, v128
	v_max_f32_e32 v129, 0, v129
	v_max_f32_e32 v130, 0, v130
	v_max_f32_e32 v131, 0, v131
	v_max_f32_e32 v132, 0, v132
	v_max_f32_e32 v133, 0, v133
	v_max_f32_e32 v134, 0, v134
	v_max_f32_e32 v135, 0, v135
	v_cvt_pk_f16_f32 v20, v128, v129
	v_cvt_pk_f16_f32 v21, v130, v131
	v_cvt_pk_f16_f32 v22, v132, v133
	v_cvt_pk_f16_f32 v23, v134, v135
	s_nop 1
	v_mfma_f32_16x16x32_f16 v[28:31], v[56:59], v[20:23], v[28:31]
	v_max_f32_e32 v136, 0, v136
	v_max_f32_e32 v137, 0, v137
	v_max_f32_e32 v138, 0, v138
	v_max_f32_e32 v139, 0, v139
	v_max_f32_e32 v140, 0, v140
	v_max_f32_e32 v141, 0, v141
	v_max_f32_e32 v142, 0, v142
	v_max_f32_e32 v143, 0, v143
	v_cvt_pk_f16_f32 v24, v136, v137
	v_cvt_pk_f16_f32 v25, v138, v139
	v_cvt_pk_f16_f32 v26, v140, v141
	v_cvt_pk_f16_f32 v27, v142, v143
	s_nop 1
	v_mfma_f32_16x16x32_f16 v[32:35], v[12:15], v[24:27], 0
	v_max_f32_e32 v144, 0, v144
	v_max_f32_e32 v145, 0, v145
	v_max_f32_e32 v146, 0, v146
	v_max_f32_e32 v147, 0, v147
	v_max_f32_e32 v148, 0, v148
	v_max_f32_e32 v149, 0, v149
	v_max_f32_e32 v150, 0, v150
	v_max_f32_e32 v151, 0, v151
	v_cvt_pk_f16_f32 v20, v144, v145
	v_cvt_pk_f16_f32 v21, v146, v147
	v_cvt_pk_f16_f32 v22, v148, v149
	v_cvt_pk_f16_f32 v23, v150, v151
	s_nop 1
	v_mfma_f32_16x16x32_f16 v[32:35], v[60:63], v[20:23], v[32:35]
	ds_write_b128 v1, v[28:31] offset:1024
	v_max_f32_e32 v152, 0, v152
	v_max_f32_e32 v153, 0, v153
	v_max_f32_e32 v154, 0, v154
	v_max_f32_e32 v155, 0, v155
	v_max_f32_e32 v156, 0, v156
	v_max_f32_e32 v157, 0, v157
	v_max_f32_e32 v158, 0, v158
	v_max_f32_e32 v159, 0, v159
	v_cvt_pk_f16_f32 v24, v152, v153
	v_cvt_pk_f16_f32 v25, v154, v155
	v_cvt_pk_f16_f32 v26, v156, v157
	v_cvt_pk_f16_f32 v27, v158, v159
	s_nop 1
	v_mfma_f32_16x16x32_f16 v[32:35], v[56:59], v[24:27], v[32:35]
	v_max_f32_e32 v160, 0, v160
	v_max_f32_e32 v161, 0, v161
	v_max_f32_e32 v162, 0, v162
	v_max_f32_e32 v163, 0, v163
	v_max_f32_e32 v164, 0, v164
	v_max_f32_e32 v165, 0, v165
	v_max_f32_e32 v166, 0, v166
	v_max_f32_e32 v167, 0, v167
	v_cvt_pk_f16_f32 v20, v160, v161
	v_cvt_pk_f16_f32 v21, v162, v163
	v_cvt_pk_f16_f32 v22, v164, v165
	v_cvt_pk_f16_f32 v23, v166, v167
	s_nop 1
	v_mfma_f32_16x16x32_f16 v[28:31], v[12:15], v[20:23], 0
	v_max_f32_e32 v168, 0, v168
	v_max_f32_e32 v169, 0, v169
	v_max_f32_e32 v170, 0, v170
	v_max_f32_e32 v171, 0, v171
	v_max_f32_e32 v172, 0, v172
	v_max_f32_e32 v173, 0, v173
	v_max_f32_e32 v174, 0, v174
	v_max_f32_e32 v175, 0, v175
	v_cvt_pk_f16_f32 v24, v168, v169
	v_cvt_pk_f16_f32 v25, v170, v171
	v_cvt_pk_f16_f32 v26, v172, v173
	v_cvt_pk_f16_f32 v27, v174, v175
	s_nop 1
	v_mfma_f32_16x16x32_f16 v[28:31], v[60:63], v[24:27], v[28:31]
	ds_write_b128 v1, v[32:35] offset:1536
	v_max_f32_e32 v176, 0, v176
	v_max_f32_e32 v177, 0, v177
	v_max_f32_e32 v178, 0, v178
	v_max_f32_e32 v179, 0, v179
	v_max_f32_e32 v180, 0, v180
	v_max_f32_e32 v181, 0, v181
	v_max_f32_e32 v182, 0, v182
	v_max_f32_e32 v183, 0, v183
	v_cvt_pk_f16_f32 v20, v176, v177
	v_cvt_pk_f16_f32 v21, v178, v179
	v_cvt_pk_f16_f32 v22, v180, v181
	v_cvt_pk_f16_f32 v23, v182, v183
	s_nop 1
	v_mfma_f32_16x16x32_f16 v[28:31], v[56:59], v[20:23], v[28:31]
	v_max_f32_e32 v184, 0, v184
	v_max_f32_e32 v185, 0, v185
	v_max_f32_e32 v186, 0, v186
	v_max_f32_e32 v187, 0, v187
	v_max_f32_e32 v188, 0, v188
	v_max_f32_e32 v189, 0, v189
	v_max_f32_e32 v190, 0, v190
	v_max_f32_e32 v191, 0, v191
	v_cvt_pk_f16_f32 v24, v184, v185
	v_cvt_pk_f16_f32 v25, v186, v187
	v_cvt_pk_f16_f32 v26, v188, v189
	v_cvt_pk_f16_f32 v27, v190, v191
	s_nop 1
	v_mfma_f32_16x16x32_f16 v[32:35], v[12:15], v[24:27], 0
	v_max_f32_e32 v192, 0, v192
	v_max_f32_e32 v193, 0, v193
	v_max_f32_e32 v194, 0, v194
	v_max_f32_e32 v195, 0, v195
	v_max_f32_e32 v196, 0, v196
	v_max_f32_e32 v197, 0, v197
	v_max_f32_e32 v198, 0, v198
	v_max_f32_e32 v199, 0, v199
	v_cvt_pk_f16_f32 v20, v192, v193
	v_cvt_pk_f16_f32 v21, v194, v195
	v_cvt_pk_f16_f32 v22, v196, v197
	v_cvt_pk_f16_f32 v23, v198, v199
	s_nop 1
	v_mfma_f32_16x16x32_f16 v[32:35], v[60:63], v[20:23], v[32:35]
	ds_write_b128 v1, v[28:31] offset:2048
	v_max_f32_e32 v200, 0, v200
	v_max_f32_e32 v201, 0, v201
	v_max_f32_e32 v202, 0, v202
	v_max_f32_e32 v203, 0, v203
	v_max_f32_e32 v204, 0, v204
	v_max_f32_e32 v205, 0, v205
	v_max_f32_e32 v206, 0, v206
	v_max_f32_e32 v207, 0, v207
	v_cvt_pk_f16_f32 v24, v200, v201
	v_cvt_pk_f16_f32 v25, v202, v203
	v_cvt_pk_f16_f32 v26, v204, v205
	v_cvt_pk_f16_f32 v27, v206, v207
	s_nop 1
	v_mfma_f32_16x16x32_f16 v[32:35], v[56:59], v[24:27], v[32:35]
	v_max_f32_e32 v208, 0, v208
	v_max_f32_e32 v209, 0, v209
	v_max_f32_e32 v210, 0, v210
	v_max_f32_e32 v211, 0, v211
	v_max_f32_e32 v212, 0, v212
	v_max_f32_e32 v213, 0, v213
	v_max_f32_e32 v214, 0, v214
	v_max_f32_e32 v215, 0, v215
	v_cvt_pk_f16_f32 v20, v208, v209
	v_cvt_pk_f16_f32 v21, v210, v211
	v_cvt_pk_f16_f32 v22, v212, v213
	v_cvt_pk_f16_f32 v23, v214, v215
	s_nop 1
	v_mfma_f32_16x16x32_f16 v[28:31], v[12:15], v[20:23], 0
	v_max_f32_e32 v216, 0, v216
	v_max_f32_e32 v217, 0, v217
	v_max_f32_e32 v218, 0, v218
	v_max_f32_e32 v219, 0, v219
	v_max_f32_e32 v220, 0, v220
	v_max_f32_e32 v221, 0, v221
	v_max_f32_e32 v222, 0, v222
	v_max_f32_e32 v223, 0, v223
	v_cvt_pk_f16_f32 v24, v216, v217
	v_cvt_pk_f16_f32 v25, v218, v219
	v_cvt_pk_f16_f32 v26, v220, v221
	v_cvt_pk_f16_f32 v27, v222, v223
	s_nop 1
	v_mfma_f32_16x16x32_f16 v[28:31], v[60:63], v[24:27], v[28:31]
	ds_write_b128 v1, v[32:35] offset:2560
	v_max_f32_e32 v224, 0, v224
	v_max_f32_e32 v225, 0, v225
	v_max_f32_e32 v226, 0, v226
	v_max_f32_e32 v227, 0, v227
	v_max_f32_e32 v228, 0, v228
	v_max_f32_e32 v229, 0, v229
	v_max_f32_e32 v230, 0, v230
	v_max_f32_e32 v231, 0, v231
	v_cvt_pk_f16_f32 v20, v224, v225
	v_cvt_pk_f16_f32 v21, v226, v227
	v_cvt_pk_f16_f32 v22, v228, v229
	v_cvt_pk_f16_f32 v23, v230, v231
	s_nop 1
	v_mfma_f32_16x16x32_f16 v[28:31], v[56:59], v[20:23], v[28:31]
	v_max_f32_e32 v232, 0, v232
	v_max_f32_e32 v233, 0, v233
	v_max_f32_e32 v234, 0, v234
	v_max_f32_e32 v235, 0, v235
	v_max_f32_e32 v236, 0, v236
	v_max_f32_e32 v237, 0, v237
	v_max_f32_e32 v238, 0, v238
	v_max_f32_e32 v239, 0, v239
	v_cvt_pk_f16_f32 v24, v232, v233
	v_cvt_pk_f16_f32 v25, v234, v235
	v_cvt_pk_f16_f32 v26, v236, v237
	v_cvt_pk_f16_f32 v27, v238, v239
	s_nop 1
	v_mfma_f32_16x16x32_f16 v[32:35], v[12:15], v[24:27], 0
	v_max_f32_e32 v240, 0, v240
	v_max_f32_e32 v241, 0, v241
	v_max_f32_e32 v242, 0, v242
	v_max_f32_e32 v243, 0, v243
	v_max_f32_e32 v244, 0, v244
	v_max_f32_e32 v245, 0, v245
	v_max_f32_e32 v246, 0, v246
	v_max_f32_e32 v247, 0, v247
	v_cvt_pk_f16_f32 v20, v240, v241
	v_cvt_pk_f16_f32 v21, v242, v243
	v_cvt_pk_f16_f32 v22, v244, v245
	v_cvt_pk_f16_f32 v23, v246, v247
	s_nop 1
	v_mfma_f32_16x16x32_f16 v[32:35], v[60:63], v[20:23], v[32:35]
	ds_write_b128 v1, v[28:31] offset:3072
	v_max_f32_e32 v248, 0, v248
	v_max_f32_e32 v249, 0, v249
	v_max_f32_e32 v250, 0, v250
	v_max_f32_e32 v251, 0, v251
	v_max_f32_e32 v252, 0, v252
	v_max_f32_e32 v253, 0, v253
	v_max_f32_e32 v254, 0, v254
	v_max_f32_e32 v255, 0, v255
	v_cvt_pk_f16_f32 v24, v248, v249
	v_cvt_pk_f16_f32 v25, v250, v251
	v_cvt_pk_f16_f32 v26, v252, v253
	v_cvt_pk_f16_f32 v27, v254, v255
	s_nop 1
	v_mfma_f32_16x16x32_f16 v[32:35], v[56:59], v[24:27], v[32:35]
	s_nop 7
	s_nop 1
	ds_write_b128 v1, v[32:35] offset:3584
	s_waitcnt lgkmcnt(0)
	s_barrier
	v_lshrrev_b32_e32 v2, 1, v0
	v_and_b32_e32 v3, 1, v0
	v_lshlrev_b32_e32 v4, 5, v2
	v_lshl_add_u32 v4, v3, 4, v4
	ds_read_b128 v[16:19], v4
	ds_read_b128 v[20:23], v4 offset:8192
	ds_read_b128 v[24:27], v4 offset:16384
	ds_read_b128 v[28:31], v4 offset:24576
	s_lshl_b32 s90, s20, 20
	s_lshl_b32 s91, s19, 13
	s_add_u32 s90, s90, s91
	s_add_u32 s14, s14, s90
	s_addc_u32 s15, s15, 0
	s_add_u32 s92, s14, 0x80000
	s_addc_u32 s93, s15, 0
	s_waitcnt lgkmcnt(0)
	v_pk_add_f32 v[16:17], v[16:17], v[20:21]
	v_pk_add_f32 v[18:19], v[18:19], v[22:23]
	v_pk_add_f32 v[24:25], v[24:25], v[28:29]
	v_pk_add_f32 v[26:27], v[26:27], v[30:31]
	global_store_dwordx4 v4, v[16:19], s[14:15]
	global_store_dwordx4 v4, v[24:27], s[92:93]
	s_endpgm
	.p2align	8

	.amdhsa_kernel _ZN12_GLOBAL__N_14k_fcEPKtPKiS1_PKfS5_Pf
		.amdhsa_group_segment_fixed_size 0
		.amdhsa_private_segment_fixed_size 0
		.amdhsa_kernarg_size 48
		.amdhsa_user_sgpr_count 2
		.amdhsa_user_sgpr_dispatch_ptr 0
		.amdhsa_user_sgpr_queue_ptr 0
		.amdhsa_user_sgpr_kernarg_segment_ptr 1
		.amdhsa_user_sgpr_dispatch_id 0
		.amdhsa_user_sgpr_kernarg_preload_length 0
		.amdhsa_user_sgpr_kernarg_preload_offset 0
		.amdhsa_user_sgpr_private_segment_size 0
		.amdhsa_uses_dynamic_stack 0
		.amdhsa_enable_private_segment 0
		.amdhsa_system_sgpr_workgroup_id_x 1
		.amdhsa_system_sgpr_workgroup_id_y 0
		.amdhsa_system_sgpr_workgroup_id_z 0
		.amdhsa_system_sgpr_workgroup_info 0
		.amdhsa_system_vgpr_workitem_id 0
		.amdhsa_next_free_vgpr 256
		.amdhsa_next_free_sgpr 100
		.amdhsa_accum_offset 256
		.amdhsa_reserve_vcc 1
		.amdhsa_float_round_mode_32 0
		.amdhsa_float_round_mode_16_64 0
		.amdhsa_float_denorm_mode_32 3
		.amdhsa_float_denorm_mode_16_64 3
		.amdhsa_dx10_clamp 1
		.amdhsa_ieee_mode 1
		.amdhsa_fp16_overflow 0
		.amdhsa_tg_split 0
		.amdhsa_exception_fp_ieee_invalid_op 0
		.amdhsa_exception_fp_denorm_src 0
		.amdhsa_exception_fp_ieee_div_zero 0
		.amdhsa_exception_fp_ieee_overflow 0
		.amdhsa_exception_fp_ieee_underflow 0
		.amdhsa_exception_fp_ieee_inexact 0
		.amdhsa_exception_int_div_zero 0
	.end_amdhsa_kernel

amdhsa.kernels:
  - .agpr_count:     0
    .args:
      - .actual_access:  read_only
        .address_space:  global
        .offset:         0
        .size:           8
        .value_kind:     global_buffer
      - .actual_access:  read_only
        .address_space:  global
        .offset:         8
        .size:           8
        .value_kind:     global_buffer
      - .actual_access:  read_only
        .address_space:  global
        .offset:         16
        .size:           8
        .value_kind:     global_buffer
      - .actual_access:  read_only
        .address_space:  global
        .offset:         24
        .size:           8
        .value_kind:     global_buffer
      - .actual_access:  write_only
        .address_space:  global
        .offset:         32
        .size:           8
        .value_kind:     global_buffer
      - .actual_access:  write_only
        .address_space:  global
        .offset:         40
        .size:           8
        .value_kind:     global_buffer
      - .actual_access:  write_only
        .address_space:  global
        .offset:         48
        .size:           8
        .value_kind:     global_buffer
    .group_segment_fixed_size: 0
    .kernarg_segment_align: 8
    .kernarg_segment_size: 56
    .language:       OpenCL C
    .language_version:
      - 2
      - 0
    .max_flat_workgroup_size: 256
    .name:           _ZN12_GLOBAL__N_16k_prepEPKiPKfS3_S3_PtS4_Pf
    .private_segment_fixed_size: 0
    .sgpr_count:     18
    .sgpr_spill_count: 0
    .symbol:         _ZN12_GLOBAL__N_16k_prepEPKiPKfS3_S3_PtS4_Pf.kd
    .uniform_work_group_size: 1
    .uses_dynamic_stack: false
    .vgpr_count:     16
    .vgpr_spill_count: 0
    .wavefront_size: 64
  - .agpr_count:     0
    .args:
      - .actual_access:  read_only
        .address_space:  global
        .offset:         0
        .size:           8
        .value_kind:     global_buffer
      - .actual_access:  read_only
        .address_space:  global
        .offset:         8
        .size:           8
        .value_kind:     global_buffer
      - .actual_access:  write_only
        .address_space:  global
        .offset:         16
        .size:           8
        .value_kind:     global_buffer
    .group_segment_fixed_size: 0
    .kernarg_segment_align: 8
    .kernarg_segment_size: 24
    .language:       OpenCL C
    .language_version:
      - 2
      - 0
    .max_flat_workgroup_size: 256
    .name:           _ZN12_GLOBAL__N_17k_finalEPKfS1_Pf
    .private_segment_fixed_size: 0
    .sgpr_count:     18
    .sgpr_spill_count: 0
    .symbol:         _ZN12_GLOBAL__N_17k_finalEPKfS1_Pf.kd
    .uniform_work_group_size: 1
    .uses_dynamic_stack: false
    .vgpr_count:     38
    .vgpr_spill_count: 0
    .wavefront_size: 64
  - .agpr_count:     0
    .args:
      - .address_space:  global
        .offset:         0
        .size:           8
        .value_kind:     global_buffer
      - .address_space:  global
        .offset:         8
        .size:           8
        .value_kind:     global_buffer
      - .actual_access:  read_only
        .address_space:  global
        .offset:         16
        .size:           8
        .value_kind:     global_buffer
      - .actual_access:  read_only
        .address_space:  global
        .offset:         24
        .size:           8
        .value_kind:     global_buffer
      - .actual_access:  write_only
        .address_space:  global
        .offset:         32
        .size:           8
        .value_kind:     global_buffer
      - .address_space:  global
        .offset:         40
        .size:           8
        .value_kind:     global_buffer
      - .actual_access:  write_only
        .address_space:  global
        .offset:         48
        .size:           8
        .value_kind:     global_buffer
    .group_segment_fixed_size: 0
    .kernarg_segment_align: 8
    .kernarg_segment_size: 56
    .language:       OpenCL C
    .language_version:
      - 2
      - 0
    .max_flat_workgroup_size: 512
    .name:           _ZN12_GLOBAL__N_110k_convpoolEPKtS1_PKfPKiPtS3_S6_
    .private_segment_fixed_size: 0
    .sgpr_count:     58
    .sgpr_spill_count: 0
    .symbol:         _ZN12_GLOBAL__N_110k_convpoolEPKtS1_PKfPKiPtS3_S6_.kd
    .uniform_work_group_size: 1
    .uses_dynamic_stack: false
    .vgpr_count:     208
    .vgpr_spill_count: 0
    .wavefront_size: 64
  - .agpr_count:     0
    .args:
      - .address_space:  global
        .offset:         0
        .size:           8
        .value_kind:     global_buffer
      - .address_space:  global
        .offset:         8
        .size:           8
        .value_kind:     global_buffer
      - .address_space:  global
        .offset:         16
        .size:           8
        .value_kind:     global_buffer
      - .address_space:  global
        .offset:         24
        .size:           8
        .value_kind:     global_buffer
      - .address_space:  global
        .offset:         32
        .size:           8
        .value_kind:     global_buffer
      - .address_space:  global
        .offset:         40
        .size:           8
        .value_kind:     global_buffer
    .group_segment_fixed_size: 0
    .kernarg_segment_align: 8
    .kernarg_segment_size: 48
    .language:       OpenCL C
    .language_version:
      - 2
      - 0
    .max_flat_workgroup_size: 512
    .name:           _ZN12_GLOBAL__N_14k_fcEPKtPKiS1_PKfS5_Pf
    .private_segment_fixed_size: 0
    .sgpr_count:     106
    .sgpr_spill_count: 0
    .symbol:         _ZN12_GLOBAL__N_14k_fcEPKtPKiS1_PKfS5_Pf.kd
    .uniform_work_group_size: 1
    .uses_dynamic_stack: false
    .vgpr_count:     256
    .vgpr_spill_count: 0
    .wavefront_size: 64
